# satisfied lgkmcnt-only waits left behind by the DPP shuffle conversion removed (norm1, prep, post, norm2, final): counter provably 0 on the straight-line path
# speedup vs baseline: 1.0066x; 1.0016x over previous
.LBB0_256:
	s_add_u32 s4, s46, s29
	s_addc_u32 s5, s47, s52
	global_load_dwordx4 v[126:129], v1, s[4:5] nt
	v_lshl_add_u64 v[124:125], s[46:47], 0, v[88:89]
	v_add_co_u32_e32 v150, vcc, 0x11100000, v124
	v_lshl_add_u64 v[122:123], s[46:47], 0, v[86:87]
	s_nop 0
	v_addc_co_u32_e32 v151, vcc, 0, v125, vcc
	global_load_dwordx2 v[124:125], v[150:151], off nt
	global_load_dwordx2 v[202:203], v[150:151], off offset:512 nt
	global_load_dwordx2 v[204:205], v[150:151], off offset:1024 nt
	global_load_dwordx2 v[206:207], v[150:151], off offset:1536 nt
	global_load_dwordx2 v[208:209], v[150:151], off offset:2048 nt
	global_load_dwordx2 v[210:211], v[150:151], off offset:2560 nt
	global_load_dwordx2 v[212:213], v[150:151], off offset:3072 nt
	global_load_dwordx2 v[214:215], v[150:151], off offset:3584 nt
	s_mov_b32 s4, 0x3e000000
	v_add_co_u32_e64 v122, s[38:39], s80, v122
	s_add_i32 s25, s25, s66
	s_nop 0
	v_addc_co_u32_e64 v123, s[38:39], 0, v123, s[38:39]
	v_lshl_add_u64 v[86:87], v[86:87], 0, s[22:23]
	v_lshl_add_u64 v[88:89], v[88:89], 0, s[94:95]
	s_waitcnt vmcnt(8)
	v_readfirstlane_b32 s5, v126
	v_readfirstlane_b32 s6, v127
	s_nop 0
	v_pk_mul_f32 v[126:127], v[128:129], s[4:5] op_sel_hi:[1,0]
	s_lshr_b32 s4, s5, 18
	s_lshl_b32 s5, s5, 11
	s_lshr_b32 s7, s6, 18
	s_and_b32 s4, s4, 0x3ffc
	s_and_b32 s20, s5, 0x7ffff800
	s_and_b32 s5, s7, 0x3ffc
	s_add_i32 s4, s81, s4
	s_add_i32 s5, s81, s5
	v_mov_b32_e32 v128, s4
	v_mov_b32_e32 v129, s5
	ds_read_b32 v128, v128
	ds_read_b32 v130, v129
	s_lshl_b32 s6, s6, 11
	s_waitcnt lgkmcnt(1)
	v_ashrrev_i32_e32 v129, 31, v128
	v_lshlrev_b64 v[128:129], 19, v[128:129]
	v_lshl_add_u64 v[128:129], s[48:49], 0, v[128:129]
	v_lshl_add_u64 v[128:129], v[128:129], 0, s[20:21]
	s_waitcnt lgkmcnt(0)
	v_ashrrev_i32_e32 v131, 31, v130
	v_readfirstlane_b32 s4, v128
	v_readfirstlane_b32 s5, v129
	v_lshlrev_b64 v[130:131], 19, v[130:131]
	v_lshl_add_u64 v[130:131], s[48:49], 0, v[130:131]
	s_and_b32 s20, s6, 0x7ffff800
	v_lshl_add_u64 v[130:131], v[130:131], 0, s[20:21]
	s_add_u32 s29, s29, s68
	global_load_dword v129, v170, s[4:5] nt
	v_readfirstlane_b32 s6, v130
	v_readfirstlane_b32 s7, v131
	global_load_dword v131, v170, s[4:5] offset:256 nt
	global_load_dword v145, v170, s[4:5] offset:512 nt
	global_load_dword v154, v170, s[4:5] offset:768 nt
	global_load_dword v156, v170, s[4:5] offset:1024 nt
	global_load_dword v158, v170, s[4:5] offset:1280 nt
	global_load_dword v159, v170, s[4:5] offset:1536 nt
	global_load_dword v160, v170, s[4:5] offset:1792 nt
	global_load_dword v133, v170, s[6:7] nt
	global_load_dword v141, v170, s[6:7] offset:256 nt
	global_load_dword v149, v170, s[6:7] offset:512 nt
	global_load_dword v157, v170, s[6:7] offset:768 nt
	global_load_dword v161, v170, s[6:7] offset:1024 nt
	global_load_dword v162, v170, s[6:7] offset:1280 nt
	global_load_dword v163, v170, s[6:7] offset:1536 nt
	global_load_dword v171, v170, s[6:7] offset:1792 nt
	s_addc_u32 s52, s52, s69
	s_cmp_ge_i32 s25, s28
	s_waitcnt vmcnt(14)
	v_cvt_f32_fp8_e32 v136, v131
	v_cvt_f32_fp8_sdwa v138, v131 src0_sel:BYTE_1
	v_cvt_f32_fp8_sdwa v140, v131 src0_sel:BYTE_2
	v_cvt_f32_fp8_sdwa v142, v131 src0_sel:BYTE_3
	s_waitcnt vmcnt(13)
	v_cvt_f32_fp8_sdwa v146, v145 src0_sel:BYTE_1
	v_cvt_f32_fp8_e32 v144, v145
	v_cvt_f32_fp8_sdwa v148, v145 src0_sel:BYTE_2
	s_waitcnt vmcnt(7)
	v_cvt_f32_fp8_e32 v131, v133
	v_cvt_f32_fp8_sdwa v135, v133 src0_sel:BYTE_2
	s_waitcnt vmcnt(6)
	v_cvt_f32_fp8_e32 v139, v141
	v_cvt_f32_fp8_sdwa v137, v141 src0_sel:BYTE_1
	v_cvt_f32_fp8_sdwa v130, v129 src0_sel:BYTE_1
	v_cvt_f32_fp8_sdwa v134, v129 src0_sel:BYTE_3
	v_cvt_f32_fp8_e32 v128, v129
	v_cvt_f32_fp8_sdwa v132, v129 src0_sel:BYTE_2
	v_cvt_f32_fp8_sdwa v129, v133 src0_sel:BYTE_1
	v_cvt_f32_fp8_sdwa v133, v133 src0_sel:BYTE_3
	s_waitcnt vmcnt(5)
	v_cvt_f32_fp8_e32 v147, v149
	v_cvt_f32_fp8_sdwa v143, v141 src0_sel:BYTE_2
	v_cvt_f32_fp8_sdwa v152, v145 src0_sel:BYTE_3
	v_cvt_f32_fp8_sdwa v145, v149 src0_sel:BYTE_1
	v_cvt_f32_fp8_sdwa v141, v141 src0_sel:BYTE_3
	v_pk_mul_f32 v[130:131], v[126:127], v[130:131]
	v_pk_mul_f32 v[134:135], v[126:127], v[134:135]
	v_pk_mul_f32 v[138:139], v[126:127], v[138:139]
	v_pk_fma_f32 v[128:129], v[126:127], v[128:129], v[130:131] op_sel:[0,0,1] op_sel_hi:[1,1,0]
	v_cvt_f32_fp8_e32 v130, v154
	v_pk_fma_f32 v[132:133], v[126:127], v[132:133], v[134:135] op_sel:[0,0,1] op_sel_hi:[1,1,0]
	v_cvt_f32_fp8_sdwa v134, v154 src0_sel:BYTE_1
	v_pk_fma_f32 v[136:137], v[126:127], v[136:137], v[138:139] op_sel:[0,0,1] op_sel_hi:[1,1,0]
	v_cvt_f32_fp8_sdwa v138, v154 src0_sel:BYTE_2
	v_cvt_f32_fp8_sdwa v154, v154 src0_sel:BYTE_3
	s_waitcnt vmcnt(4)
	v_cvt_f32_fp8_sdwa v155, v157 src0_sel:BYTE_2
	v_pk_mul_f32 v[146:147], v[126:127], v[146:147]
	v_cvt_f32_fp8_e32 v135, v157
	v_cvt_f32_fp8_sdwa v139, v157 src0_sel:BYTE_3
	v_pk_mul_f32 v[142:143], v[126:127], v[142:143]
	v_pk_fma_f32 v[144:145], v[126:127], v[144:145], v[146:147] op_sel:[0,0,1] op_sel_hi:[1,1,0]
	v_cvt_f32_fp8_sdwa v146, v156 src0_sel:BYTE_1
	v_cvt_f32_fp8_sdwa v131, v157 src0_sel:BYTE_1
	s_waitcnt vmcnt(3)
	v_cvt_f32_fp8_e32 v147, v161
	v_cvt_f32_fp8_sdwa v153, v149 src0_sel:BYTE_2
	v_pk_fma_f32 v[140:141], v[126:127], v[140:141], v[142:143] op_sel:[0,0,1] op_sel_hi:[1,1,0]
	v_cvt_f32_fp8_e32 v142, v156
	v_cvt_f32_fp8_sdwa v143, v161 src0_sel:BYTE_1
	v_cvt_f32_fp8_sdwa v149, v149 src0_sel:BYTE_3
	v_pk_mul_f32 v[154:155], v[126:127], v[154:155]
	v_pk_mul_f32 v[134:135], v[126:127], v[134:135]
	v_pk_fma_f32 v[172:173], v[126:127], v[138:139], v[154:155] op_sel:[0,0,1] op_sel_hi:[1,1,0]
	v_cvt_f32_fp8_sdwa v138, v158 src0_sel:BYTE_1
	s_waitcnt vmcnt(2)
	v_cvt_f32_fp8_e32 v139, v162
	v_pk_fma_f32 v[134:135], v[126:127], v[130:131], v[134:135] op_sel:[0,0,1] op_sel_hi:[1,1,0]
	v_cvt_f32_fp8_e32 v130, v158
	v_pk_mul_f32 v[146:147], v[126:127], v[146:147]
	v_cvt_f32_fp8_sdwa v154, v158 src0_sel:BYTE_3
	v_cvt_f32_fp8_sdwa v131, v162 src0_sel:BYTE_1
	v_cvt_f32_fp8_sdwa v155, v162 src0_sel:BYTE_2
	v_pk_mul_f32 v[152:153], v[126:127], v[152:153]
	v_pk_fma_f32 v[146:147], v[126:127], v[142:143], v[146:147] op_sel:[0,0,1] op_sel_hi:[1,1,0]
	v_cvt_f32_fp8_sdwa v142, v158 src0_sel:BYTE_2
	v_cvt_f32_fp8_sdwa v143, v162 src0_sel:BYTE_3
	v_pk_fma_f32 v[148:149], v[126:127], v[148:149], v[152:153] op_sel:[0,0,1] op_sel_hi:[1,1,0]
	v_cvt_f32_fp8_sdwa v152, v156 src0_sel:BYTE_2
	v_cvt_f32_fp8_sdwa v156, v156 src0_sel:BYTE_3
	v_cvt_f32_fp8_sdwa v157, v161 src0_sel:BYTE_2
	v_cvt_f32_fp8_sdwa v153, v161 src0_sel:BYTE_3
	v_pk_mul_f32 v[138:139], v[126:127], v[138:139]
	v_pk_mul_f32 v[156:157], v[126:127], v[156:157]
	v_pk_fma_f32 v[176:177], v[126:127], v[130:131], v[138:139] op_sel:[0,0,1] op_sel_hi:[1,1,0]
	v_pk_mul_f32 v[138:139], v[126:127], v[154:155]
	v_cvt_f32_fp8_sdwa v130, v159 src0_sel:BYTE_1
	v_pk_fma_f32 v[178:179], v[126:127], v[142:143], v[138:139] op_sel:[0,0,1] op_sel_hi:[1,1,0]
	v_cvt_f32_fp8_sdwa v142, v159 src0_sel:BYTE_3
	s_waitcnt vmcnt(1)
	v_cvt_f32_fp8_sdwa v143, v163 src0_sel:BYTE_2
	v_cvt_f32_fp8_sdwa v138, v159 src0_sel:BYTE_2
	v_cvt_f32_fp8_e32 v131, v163
	v_cvt_f32_fp8_sdwa v139, v163 src0_sel:BYTE_3
	v_pk_fma_f32 v[174:175], v[126:127], v[152:153], v[156:157] op_sel:[0,0,1] op_sel_hi:[1,1,0]
	v_cvt_f32_fp8_e32 v152, v159
	v_cvt_f32_fp8_sdwa v153, v163 src0_sel:BYTE_1
	v_pk_mul_f32 v[142:143], v[126:127], v[142:143]
	v_pk_mul_f32 v[130:131], v[126:127], v[130:131]
	v_pk_fma_f32 v[180:181], v[126:127], v[138:139], v[142:143] op_sel:[0,0,1] op_sel_hi:[1,1,0]
	v_cvt_f32_fp8_sdwa v138, v160 src0_sel:BYTE_1
	s_waitcnt vmcnt(0)
	v_cvt_f32_fp8_e32 v139, v171
	v_pk_fma_f32 v[154:155], v[126:127], v[152:153], v[130:131] op_sel:[0,0,1] op_sel_hi:[1,1,0]
	v_cvt_f32_fp8_e32 v130, v160
	v_cvt_f32_fp8_sdwa v131, v171 src0_sel:BYTE_1
	v_pk_mul_f32 v[138:139], v[126:127], v[138:139]
	v_lshlrev_b32_e32 v142, 16, v124
	v_and_b32_e32 v143, 0xffff0000, v124
	v_pk_fma_f32 v[152:153], v[126:127], v[130:131], v[138:139] op_sel:[0,0,1] op_sel_hi:[1,1,0]
	v_cvt_f32_fp8_sdwa v138, v160 src0_sel:BYTE_3
	v_cvt_f32_fp8_sdwa v139, v171 src0_sel:BYTE_2
	v_cvt_f32_fp8_sdwa v130, v160 src0_sel:BYTE_2
	v_cvt_f32_fp8_sdwa v131, v171 src0_sel:BYTE_3
	v_lshlrev_b32_e32 v124, 16, v125
	v_pk_mul_f32 v[138:139], v[126:127], v[138:139]
	v_and_b32_e32 v125, 0xffff0000, v125
	v_pk_fma_f32 v[156:157], v[126:127], v[130:131], v[138:139] op_sel:[0,0,1] op_sel_hi:[1,1,0]
	v_pk_fma_f32 v[124:125], v[8:9], v[132:133], v[124:125]
	v_and_b32_e32 v171, 64, v226
	v_lshlrev_b32_e32 v182, 16, v202
	v_and_b32_e32 v183, 0xffff0000, v202
	v_lshlrev_b32_e32 v186, 16, v206
	v_and_b32_e32 v187, 0xffff0000, v206
	v_lshlrev_b32_e32 v188, 16, v207
	v_and_b32_e32 v189, 0xffff0000, v207
	v_lshlrev_b32_e32 v126, 16, v203
	v_and_b32_e32 v127, 0xffff0000, v203
	v_lshlrev_b32_e32 v184, 16, v204
	v_and_b32_e32 v185, 0xffff0000, v204
	v_lshlrev_b32_e32 v130, 16, v205
	v_and_b32_e32 v131, 0xffff0000, v205
	v_pk_fma_f32 v[126:127], v[16:17], v[140:141], v[126:127]
	v_pk_fma_f32 v[140:141], v[14:15], v[136:137], v[182:183]
	v_lshlrev_b32_e32 v192, 16, v208
	v_lshlrev_b32_e32 v196, 16, v210
	v_and_b32_e32 v197, 0xffff0000, v210
	v_lshlrev_b32_e32 v198, 16, v211
	v_and_b32_e32 v199, 0xffff0000, v211
	v_lshlrev_b32_e32 v158, 16, v214
	v_and_b32_e32 v159, 0xffff0000, v214
	v_and_b32_e32 v193, 0xffff0000, v208
	v_lshlrev_b32_e32 v194, 16, v209
	v_and_b32_e32 v195, 0xffff0000, v209
	v_pk_fma_f32 v[138:139], v[6:7], v[128:129], v[142:143]
	v_pk_fma_f32 v[158:159], v[62:63], v[152:153], v[158:159]
	v_cvt_pk_bf16_f32 v152, v138, v139
	v_cvt_pk_bf16_f32 v153, v124, v125
	global_store_dwordx2 v[150:151], v[152:153], off
	v_cvt_pk_bf16_f32 v152, v140, v141
	v_cvt_pk_bf16_f32 v153, v126, v127
	v_pk_fma_f32 v[128:129], v[24:25], v[148:149], v[130:131]
	v_pk_fma_f32 v[142:143], v[22:23], v[144:145], v[184:185]
	global_store_dwordx2 v[150:151], v[152:153], off offset:512
	v_cvt_pk_bf16_f32 v152, v142, v143
	v_cvt_pk_bf16_f32 v153, v128, v129
	v_pk_fma_f32 v[130:131], v[32:33], v[172:173], v[188:189]
	v_pk_fma_f32 v[144:145], v[30:31], v[134:135], v[186:187]
	global_store_dwordx2 v[150:151], v[152:153], off offset:1024
	v_cvt_pk_bf16_f32 v152, v144, v145
	v_cvt_pk_bf16_f32 v153, v130, v131
	v_pk_fma_f32 v[132:133], v[40:41], v[174:175], v[194:195]
	v_pk_fma_f32 v[146:147], v[38:39], v[146:147], v[192:193]
	global_store_dwordx2 v[150:151], v[152:153], off offset:1536
	v_cvt_pk_bf16_f32 v152, v146, v147
	v_cvt_pk_bf16_f32 v153, v132, v133
	v_lshlrev_b32_e32 v162, 16, v212
	v_and_b32_e32 v163, 0xffff0000, v212
	v_lshlrev_b32_e32 v200, 16, v213
	v_and_b32_e32 v201, 0xffff0000, v213
	v_lshlrev_b32_e32 v160, 16, v215
	v_and_b32_e32 v161, 0xffff0000, v215
	v_pk_fma_f32 v[134:135], v[48:49], v[178:179], v[198:199]
	v_pk_fma_f32 v[148:149], v[46:47], v[176:177], v[196:197]
	global_store_dwordx2 v[150:151], v[152:153], off offset:2048
	v_cvt_pk_bf16_f32 v152, v148, v149
	v_cvt_pk_bf16_f32 v153, v134, v135
	v_pk_fma_f32 v[136:137], v[56:57], v[180:181], v[200:201]
	v_pk_fma_f32 v[154:155], v[54:55], v[154:155], v[162:163]
	v_xor_b32_e32 v163, 1, v226
	v_xor_b32_e32 v172, 2, v226
	v_pk_fma_f32 v[156:157], v[64:65], v[156:157], v[160:161]
	v_xor_b32_e32 v173, 4, v226
	v_xor_b32_e32 v174, 8, v226
	v_add_u32_e32 v160, 64, v171
	global_store_dwordx2 v[150:151], v[152:153], off offset:2560
	v_cvt_pk_bf16_f32 v152, v154, v155
	v_cvt_pk_bf16_f32 v153, v136, v137
	v_cmp_lt_i32_e32 vcc, v163, v160
	v_cmp_lt_i32_e64 s[38:39], v172, v160
	v_cmp_lt_i32_e64 s[40:41], v173, v160
	v_cmp_lt_i32_e64 s[42:43], v174, v160
	v_mul_f32_e32 v160, v139, v139
	global_store_dwordx2 v[150:151], v[152:153], off offset:3072
	v_cvt_pk_bf16_f32 v152, v158, v159
	v_cvt_pk_bf16_f32 v153, v156, v157
	global_store_dwordx2 v[150:151], v[152:153], off offset:3584
	v_mul_f32_e32 v150, v125, v125
	v_fmac_f32_e32 v160, v138, v138
	v_fmac_f32_e32 v150, v124, v124
	v_mul_f32_e32 v151, v141, v141
	v_mul_f32_e32 v152, v127, v127
	v_mul_f32_e32 v153, v143, v143
	v_add_f32_e32 v150, v160, v150
	v_mul_f32_e32 v160, v129, v129
	v_fmac_f32_e32 v151, v140, v140
	v_fmac_f32_e32 v152, v126, v126
	v_fmac_f32_e32 v153, v142, v142
	v_fmac_f32_e32 v160, v128, v128
	v_add_f32_e32 v151, v151, v152
	v_mul_f32_e32 v152, v145, v145
	v_add_f32_e32 v153, v153, v160
	v_mul_f32_e32 v160, v131, v131
	v_fmac_f32_e32 v152, v144, v144
	v_fmac_f32_e32 v160, v130, v130
	v_add_f32_e32 v152, v152, v160
	v_mul_f32_e32 v160, v147, v147
	v_mul_f32_e32 v161, v133, v133
	v_fmac_f32_e32 v160, v146, v146
	v_fmac_f32_e32 v161, v132, v132
	v_add_f32_e32 v160, v160, v161
	v_mul_f32_e32 v161, v149, v149
	v_mul_f32_e32 v162, v135, v135
	v_fmac_f32_e32 v161, v148, v148
	v_fmac_f32_e32 v162, v134, v134
	v_add_f32_e32 v150, v150, v151
	v_add_f32_e32 v161, v161, v162
	v_mul_f32_e32 v162, v155, v155
	v_mul_f32_e32 v171, v137, v137
	v_add_f32_e32 v150, v150, v153
	v_fmac_f32_e32 v162, v154, v154
	v_fmac_f32_e32 v171, v136, v136
	v_add_f32_e32 v150, v150, v152
	v_add_f32_e32 v162, v162, v171
	v_mul_f32_e32 v171, v159, v159
	v_mul_f32_e32 v175, v157, v157
	v_add_f32_e32 v150, v150, v160
	v_fmac_f32_e32 v171, v158, v158
	v_fmac_f32_e32 v175, v156, v156
	v_add_f32_e32 v150, v150, v161
	v_add_f32_e32 v171, v171, v175
	v_add_f32_e32 v150, v150, v162
	v_cndmask_b32_e32 v151, v226, v163, vcc
	v_lshlrev_b32_e32 v151, 2, v151
	v_add_f32_e32 v150, v150, v171
	s_nop 1
	v_mov_b32_dpp v151, v150 quad_perm:[1,0,3,2] row_mask:0xf bank_mask:0xf
	v_cndmask_b32_e64 v152, v226, v172, s[38:39]
	v_lshlrev_b32_e32 v152, 2, v152
	v_cndmask_b32_e64 v153, v226, v173, s[40:41]
	v_lshlrev_b32_e32 v153, 2, v153
	v_add_f32_e32 v150, v150, v151
	s_nop 1
	v_mov_b32_dpp v151, v150 quad_perm:[2,3,0,1] row_mask:0xf bank_mask:0xf
	v_cndmask_b32_e64 v163, v226, v174, s[42:43]
	v_lshlrev_b32_e32 v163, 2, v163
	v_mov_b32_e32 v160, 0
	v_mov_b32_e32 v161, 0
	v_add_f32_e32 v150, v150, v151
	s_nop 1
	v_mov_b32_dpp v151, v150 row_half_mirror row_mask:0xf bank_mask:0xf
	v_mov_b32_e32 v162, 0
	v_mov_b32_e32 v173, 0
	v_add_f32_e32 v150, v150, v151
	s_nop 1
	v_mov_b32_dpp v151, v150 row_mirror row_mask:0xf bank_mask:0xf
	v_add_f32_e32 v150, v150, v151
	v_mov_b32_e32 v151, v150
	s_nop 1
	v_permlane16_swap_b32_e32 v150, v151
	v_add_f32_e32 v150, v150, v151
	v_mov_b32_e32 v151, v150
	s_nop 1
	v_permlane32_swap_b32_e32 v150, v151
	v_add_f32_e32 v150, v150, v151
	v_fmamk_f32 v150, v150, 0x3a000000, v228
	v_mul_f32_e32 v151, 0x4f800000, v150
	v_cmp_gt_f32_e32 vcc, s82, v150
	s_nop 1
	v_cndmask_b32_e32 v150, v150, v151, vcc
	v_sqrt_f32_e32 v151, v150
	s_nop 0
	v_add_u32_e32 v152, -1, v151
	v_add_u32_e32 v153, 1, v151
	v_fma_f32 v163, -v152, v151, v150
	v_fma_f32 v171, -v153, v151, v150
	v_cmp_ge_f32_e64 s[38:39], 0, v163
	s_nop 1
	v_cndmask_b32_e64 v151, v151, v152, s[38:39]
	v_cmp_lt_f32_e64 s[38:39], 0, v171
	v_mov_b32_e32 v171, 0
	s_nop 0
	v_cndmask_b32_e64 v151, v151, v153, s[38:39]
	v_mul_f32_e32 v152, 0x37800000, v151
	v_cndmask_b32_e32 v151, v151, v152, vcc
	v_cmp_class_f32_e32 vcc, v150, v229
	s_nop 1
	v_cndmask_b32_e32 v150, v151, v150, vcc
	v_div_scale_f32 v151, s[4:5], v150, v150, 1.0
	v_rcp_f32_e32 v153, v151
	v_div_scale_f32 v152, vcc, 1.0, v150, 1.0
	v_fma_f32 v163, -v151, v153, 1.0
	v_fmac_f32_e32 v153, v163, v153
	v_mul_f32_e32 v172, v152, v153
	v_fma_f32 v163, -v151, v172, v152
	v_fmac_f32_e32 v172, v163, v153
	v_fma_f32 v151, -v151, v172, v152
	v_div_fmas_f32 v151, v151, v153, v172
	v_div_fixup_f32 v174, v151, v150, 1.0
	v_pk_mul_f32 v[138:139], v[138:139], v[174:175] op_sel_hi:[1,0]
	v_pk_mul_f32 v[150:151], v[124:125], v[174:175] op_sel_hi:[1,0]
	v_pk_mul_f32 v[124:125], v[140:141], v[174:175] op_sel_hi:[1,0]
	v_pk_fma_f32 v[138:139], v[92:93], v[138:139], v[2:3]
	v_pk_mul_f32 v[140:141], v[126:127], v[174:175] op_sel_hi:[1,0]
	v_pk_mul_f32 v[126:127], v[142:143], v[174:175] op_sel_hi:[1,0]
	v_pk_fma_f32 v[124:125], v[96:97], v[124:125], v[10:11]
	v_med3_f32 v138, v138, s33, v233
	v_med3_f32 v139, v139, s33, v233
	v_pk_mul_f32 v[142:143], v[128:129], v[174:175] op_sel_hi:[1,0]
	v_pk_mul_f32 v[128:129], v[144:145], v[174:175] op_sel_hi:[1,0]
	v_pk_fma_f32 v[126:127], v[100:101], v[126:127], v[18:19]
	v_med3_f32 v124, v124, s33, v233
	v_med3_f32 v125, v125, s33, v233
	v_cvt_pk_fp8_f32 v160, v138, v139
	v_pk_mul_f32 v[144:145], v[130:131], v[174:175] op_sel_hi:[1,0]
	v_pk_mul_f32 v[130:131], v[146:147], v[174:175] op_sel_hi:[1,0]
	v_pk_mul_f32 v[146:147], v[132:133], v[174:175] op_sel_hi:[1,0]
	v_pk_mul_f32 v[132:133], v[148:149], v[174:175] op_sel_hi:[1,0]
	v_pk_mul_f32 v[148:149], v[134:135], v[174:175] op_sel_hi:[1,0]
	v_pk_mul_f32 v[134:135], v[154:155], v[174:175] op_sel_hi:[1,0]
	v_pk_mul_f32 v[152:153], v[136:137], v[174:175] op_sel_hi:[1,0]
	v_pk_mul_f32 v[136:137], v[158:159], v[174:175] op_sel_hi:[1,0]
	v_pk_fma_f32 v[128:129], v[104:105], v[128:129], v[26:27]
	v_med3_f32 v126, v126, s33, v233
	v_med3_f32 v127, v127, s33, v233
	v_cvt_pk_fp8_f32 v161, v124, v125
	v_mov_b32_e32 v163, 0
	v_pk_fma_f32 v[150:151], v[90:91], v[150:151], v[4:5]
	v_pk_fma_f32 v[130:131], v[108:109], v[130:131], v[34:35]
	v_pk_fma_f32 v[132:133], v[112:113], v[132:133], v[42:43]
	v_pk_fma_f32 v[134:135], v[116:117], v[134:135], v[50:51]
	v_pk_fma_f32 v[136:137], v[120:121], v[136:137], v[58:59]
	v_med3_f32 v128, v128, s33, v233
	v_med3_f32 v129, v129, s33, v233
	v_cvt_pk_fp8_f32 v162, v126, v127
	v_mov_b32_e32 v172, 0
	v_pk_mul_f32 v[154:155], v[156:157], v[174:175] op_sel_hi:[1,0]
	v_mov_b32_e32 v156, 0
	v_pk_fma_f32 v[140:141], v[94:95], v[140:141], v[12:13]
	v_med3_f32 v150, v150, s33, v233
	v_med3_f32 v151, v151, s33, v233
	v_med3_f32 v130, v130, s33, v233
	v_med3_f32 v131, v131, s33, v233
	v_med3_f32 v132, v132, s33, v233
	v_med3_f32 v133, v133, s33, v233
	v_med3_f32 v134, v134, s33, v233
	v_med3_f32 v135, v135, s33, v233
	v_med3_f32 v136, v136, s33, v233
	v_med3_f32 v137, v137, s33, v233
	v_cvt_pk_fp8_f32 v163, v128, v129
	v_pk_fma_f32 v[142:143], v[98:99], v[142:143], v[20:21]
	v_med3_f32 v140, v140, s33, v233
	v_med3_f32 v141, v141, s33, v233
	v_cvt_pk_fp8_f32 v171, v130, v131
	v_cvt_pk_fp8_f32 v172, v132, v133
	v_cvt_pk_fp8_f32 v173, v134, v135
	v_cvt_pk_fp8_f32 v156, v136, v137
	v_cvt_pk_fp8_f32 v160, v150, v151 op_sel:[0,0,1]
	v_pk_fma_f32 v[144:145], v[102:103], v[144:145], v[28:29]
	v_med3_f32 v142, v142, s33, v233
	v_med3_f32 v143, v143, s33, v233
	v_cvt_pk_fp8_f32 v161, v140, v141 op_sel:[0,0,1]
	v_pk_fma_f32 v[146:147], v[106:107], v[146:147], v[36:37]
	v_pk_fma_f32 v[148:149], v[110:111], v[148:149], v[44:45]
	v_pk_fma_f32 v[152:153], v[114:115], v[152:153], v[52:53]
	v_pk_fma_f32 v[154:155], v[118:119], v[154:155], v[60:61]
	v_med3_f32 v144, v144, s33, v233
	v_med3_f32 v145, v145, s33, v233
	v_cvt_pk_fp8_f32 v162, v142, v143 op_sel:[0,0,1]
	v_med3_f32 v146, v146, s33, v233
	v_med3_f32 v147, v147, s33, v233
	v_med3_f32 v148, v148, s33, v233
	v_med3_f32 v149, v149, s33, v233
	v_med3_f32 v152, v152, s33, v233
	v_med3_f32 v153, v153, s33, v233
	v_med3_f32 v154, v154, s33, v233
	v_med3_f32 v155, v155, s33, v233
	v_cvt_pk_fp8_f32 v163, v144, v145 op_sel:[0,0,1]
	v_cvt_pk_fp8_f32 v171, v146, v147 op_sel:[0,0,1]
	v_cvt_pk_fp8_f32 v172, v148, v149 op_sel:[0,0,1]
	v_cvt_pk_fp8_f32 v173, v152, v153 op_sel:[0,0,1]
	v_cvt_pk_fp8_f32 v156, v154, v155 op_sel:[0,0,1]
	global_store_dword v[122:123], v160, off
	global_store_dword v[122:123], v161, off offset:256
	global_store_dword v[122:123], v162, off offset:512
	global_store_dword v[122:123], v163, off offset:768
	global_store_dword v[122:123], v171, off offset:1024
	global_store_dword v[122:123], v172, off offset:1280
	global_store_dword v[122:123], v173, off offset:1536
	global_store_dword v[122:123], v156, off offset:1792
	s_cbranch_scc0 .LBB0_256
	s_branch .LBB0_253

.LBB0_260:
	s_mul_hi_i32 s4, s13, 0x2aaaaaab
	s_lshr_b32 s5, s4, 31
	s_ashr_i32 s4, s4, 8
	s_add_i32 s4, s4, s5
	s_mul_i32 s5, s4, 0xfffffa00
	s_add_i32 s55, s13, s5
	s_cmpk_gt_i32 s55, 0x1ff
	s_mov_b64 s[6:7], -1
	s_cbranch_scc0 .LBB0_266
	s_ashr_i32 s5, s4, 31
	s_lshl_b64 s[6:7], s[4:5], 23
	s_cmpk_gt_u32 s55, 0x3ff
	s_mov_b64 s[8:9], -1
	s_cbranch_scc0 .LBB0_263
	s_add_u32 s56, s42, s6
	s_addc_u32 s57, s43, s7
	s_lshl_b64 s[8:9], s[4:5], 21
	s_add_u32 s58, s28, s8
	s_addc_u32 s9, s29, s9
	s_lshl_b32 s8, s4, 10
	s_sub_i32 s8, s53, s8
	s_and_b32 s59, s8, 0x780
	s_add_i32 s8, s49, 0xffffc000
	v_or_b32_e32 v0, s59, v3
	s_and_b32 s8, s8, 0x7e0
	v_lshlrev_b32_e32 v0, 13, v0
	v_lshl_add_u64 v[6:7], s[56:57], 0, v[0:1]
	s_lshl_b32 s20, s8, 2
	v_lshl_add_u64 v[6:7], v[6:7], 0, s[20:21]
	v_lshlrev_b32_e32 v0, 2, v2
	v_lshl_add_u64 v[6:7], v[6:7], 0, v[0:1]
	s_mov_b32 s20, 0x10000
	v_add_co_u32_e32 v30, vcc, s20, v6
	s_mov_b32 s20, 0x20000
	s_nop 0
	v_addc_co_u32_e32 v31, vcc, 0, v7, vcc
	v_add_co_u32_e32 v34, vcc, s20, v6
	s_mov_b32 s20, 0x30000
	s_nop 0
	v_addc_co_u32_e32 v35, vcc, 0, v7, vcc
	v_add_co_u32_e32 v38, vcc, s20, v6
	s_mov_b32 s20, 0x40000
	s_nop 0
	v_addc_co_u32_e32 v39, vcc, 0, v7, vcc
	v_add_co_u32_e32 v42, vcc, s20, v6
	s_mov_b32 s20, 0x50000
	s_nop 0
	v_addc_co_u32_e32 v43, vcc, 0, v7, vcc
	v_add_co_u32_e32 v46, vcc, s20, v6
	s_mov_b32 s20, 0x60000
	s_nop 0
	v_addc_co_u32_e32 v47, vcc, 0, v7, vcc
	v_add_co_u32_e32 v50, vcc, s20, v6
	s_mov_b32 s20, 0x70000
	s_nop 0
	v_addc_co_u32_e32 v51, vcc, 0, v7, vcc
	v_add_co_u32_e32 v54, vcc, s20, v6
	s_mov_b32 s20, 0x80000
	s_nop 0
	v_addc_co_u32_e32 v55, vcc, 0, v7, vcc
	v_add_co_u32_e32 v58, vcc, s20, v6
	s_mov_b32 s20, 0x90000
	s_nop 0
	v_addc_co_u32_e32 v59, vcc, 0, v7, vcc
	v_add_co_u32_e32 v62, vcc, s20, v6
	s_mov_b32 s20, 0xa0000
	s_nop 0
	v_addc_co_u32_e32 v63, vcc, 0, v7, vcc
	v_add_co_u32_e32 v68, vcc, s20, v6
	s_mov_b32 s20, 0xb0000
	s_nop 0
	v_addc_co_u32_e32 v69, vcc, 0, v7, vcc
	v_add_co_u32_e32 v72, vcc, s20, v6
	s_mov_b32 s20, 0xc0000
	s_nop 0
	v_addc_co_u32_e32 v73, vcc, 0, v7, vcc
	global_load_dwordx4 v[26:29], v[6:7], off nt
	s_nop 0
	global_load_dwordx4 v[30:33], v[30:31], off nt
	v_add_co_u32_e32 v76, vcc, s20, v6
	global_load_dwordx4 v[34:37], v[34:35], off nt
	s_nop 0
	global_load_dwordx4 v[38:41], v[38:39], off nt
	v_addc_co_u32_e32 v77, vcc, 0, v7, vcc
	s_mov_b32 s20, 0xd0000
	global_load_dwordx4 v[42:45], v[42:43], off nt
	s_nop 0
	global_load_dwordx4 v[46:49], v[46:47], off nt
	v_add_co_u32_e32 v80, vcc, s20, v6
	global_load_dwordx4 v[50:53], v[50:51], off nt
	s_nop 0
	global_load_dwordx4 v[54:57], v[54:55], off nt
	v_addc_co_u32_e32 v81, vcc, 0, v7, vcc
	s_mov_b32 s20, 0xe0000
	global_load_dwordx4 v[58:61], v[58:59], off nt
	s_nop 0
	global_load_dwordx4 v[62:65], v[62:63], off nt
	v_add_co_u32_e32 v84, vcc, s20, v6
	global_load_dwordx4 v[68:71], v[68:69], off nt
	s_nop 0
	global_load_dwordx4 v[72:75], v[72:73], off nt
	v_addc_co_u32_e32 v85, vcc, 0, v7, vcc
	s_mov_b32 s20, 0xf0000
	global_load_dwordx4 v[76:79], v[76:77], off nt
	s_nop 0
	global_load_dwordx4 v[80:83], v[80:81], off nt
	v_add_co_u32_e32 v6, vcc, s20, v6
	v_add_u32_e32 v0, v8, v4
	s_nop 0
	v_addc_co_u32_e32 v7, vcc, 0, v7, vcc
	global_load_dwordx4 v[84:87], v[84:85], off nt
	s_nop 0
	global_load_dwordx4 v[88:91], v[6:7], off nt
	s_waitcnt vmcnt(0)
	ds_write_b128 v0, v[26:29]
	s_waitcnt vmcnt(14)
	ds_write_b128 v0, v[30:33] offset:1024
	v_add_u32_e32 v0, v8, v9
	s_waitcnt vmcnt(13)
	ds_write_b128 v0, v[34:37] offset:2048
	s_waitcnt vmcnt(12)
	ds_write_b128 v0, v[38:41] offset:3072
	v_add_u32_e32 v0, v8, v10
	s_waitcnt vmcnt(11)
	ds_write_b128 v0, v[42:45] offset:4096
	s_waitcnt vmcnt(10)
	ds_write_b128 v0, v[46:49] offset:5120
	v_add_u32_e32 v0, v8, v11
	s_waitcnt vmcnt(9)
	ds_write_b128 v0, v[50:53] offset:6144
	s_waitcnt vmcnt(8)
	ds_write_b128 v0, v[54:57] offset:7168
	v_add_u32_e32 v0, v8, v12
	s_waitcnt vmcnt(7)
	ds_write_b128 v0, v[58:61] offset:8192
	s_waitcnt vmcnt(6)
	ds_write_b128 v0, v[62:65] offset:9216
	v_add_u32_e32 v0, v8, v13
	s_waitcnt vmcnt(5)
	ds_write_b128 v0, v[68:71] offset:10240
	s_waitcnt vmcnt(4)
	ds_write_b128 v0, v[72:75] offset:11264
	v_add_u32_e32 v0, v8, v14
	s_waitcnt vmcnt(3)
	ds_write_b128 v0, v[76:79] offset:12288
	s_waitcnt vmcnt(2)
	ds_write_b128 v0, v[80:83] offset:13312
	v_add_u32_e32 v0, v8, v15
	s_waitcnt vmcnt(1)
	ds_write_b128 v0, v[84:87] offset:14336
	s_waitcnt vmcnt(0)
	ds_write_b128 v0, v[88:91] offset:15360
	s_waitcnt lgkmcnt(0)
	v_add_u32_e32 v0, 0x400, v17
	ds_read2_b32 v[26:27], v17 offset1:32
	ds_read2_b32 v[28:29], v0 offset1:32
	ds_read2_b32 v[30:31], v17 offset0:64 offset1:96
	ds_read2_b32 v[32:33], v0 offset0:64 offset1:96
	s_add_u32 s56, s58, s59
	s_waitcnt lgkmcnt(3)
	v_mul_f32_e32 v25, 0x41800000, v26
	s_waitcnt lgkmcnt(2)
	v_mul_f32_e32 v34, 0x41800000, v28
	v_mul_f32_e32 v35, 0x41800000, v27
	v_mul_f32_e32 v36, 0x41800000, v29
	s_waitcnt lgkmcnt(1)
	v_mul_f32_e32 v37, 0x41800000, v30
	ds_read2_b32 v[26:27], v17 offset0:128 offset1:160
	s_waitcnt lgkmcnt(1)
	v_mul_f32_e32 v38, 0x41800000, v32
	v_mul_f32_e32 v39, 0x41800000, v31
	ds_read2_b32 v[28:29], v0 offset0:128 offset1:160
	v_mul_f32_e32 v40, 0x41800000, v33
	ds_read2_b32 v[30:31], v17 offset0:192 offset1:224
	ds_read2_b32 v[32:33], v0 offset0:192 offset1:224
	s_waitcnt lgkmcnt(3)
	v_mul_f32_e32 v41, 0x41800000, v26
	v_mul_f32_e32 v27, 0x41800000, v27
	s_waitcnt lgkmcnt(2)
	v_mul_f32_e32 v0, 0x41800000, v28
	s_waitcnt lgkmcnt(1)
	v_mul_f32_e32 v28, 0x41800000, v30
	s_waitcnt lgkmcnt(0)
	v_mul_f32_e32 v30, 0x41800000, v32
	v_mul_f32_e32 v32, 0x41800000, v33
	v_med3_f32 v25, v25, s33, v233
	v_med3_f32 v33, v35, s33, v233
	v_mov_b32_e32 v26, v1
	v_cvt_pk_fp8_f32 v26, v25, v33
	v_med3_f32 v25, v37, s33, v233
	v_med3_f32 v35, v41, s33, v233
	v_med3_f32 v37, v27, s33, v233
	v_mov_b32_e32 v27, v1
	v_cvt_pk_fp8_f32 v27, v35, v37
	v_mul_f32_e32 v31, 0x41800000, v31
	v_med3_f32 v33, v39, s33, v233
	v_cvt_pk_fp8_f32 v26, v25, v33 op_sel:[0,0,1]
	v_med3_f32 v25, v28, s33, v233
	v_med3_f32 v28, v31, s33, v233
	v_mul_f32_e32 v29, 0x41800000, v29
	v_cvt_pk_fp8_f32 v27, v25, v28 op_sel:[0,0,1]
	v_med3_f32 v25, v34, s33, v233
	v_med3_f32 v31, v36, s33, v233
	v_mov_b32_e32 v28, v1
	v_cvt_pk_fp8_f32 v28, v25, v31
	v_med3_f32 v0, v0, s33, v233
	v_med3_f32 v33, v29, s33, v233
	v_mov_b32_e32 v29, v1
	v_cvt_pk_fp8_f32 v29, v0, v33
	v_med3_f32 v25, v38, s33, v233
	v_med3_f32 v31, v40, s33, v233
	v_cvt_pk_fp8_f32 v28, v25, v31 op_sel:[0,0,1]
	v_med3_f32 v0, v30, s33, v233
	v_med3_f32 v25, v32, s33, v233
	v_cvt_pk_fp8_f32 v29, v0, v25 op_sel:[0,0,1]
	s_addc_u32 s57, s9, 0
	v_or_b32_e32 v0, s8, v3
	v_lshl_add_u64 v[6:7], s[56:57], 0, v[4:5]
	v_lshlrev_b32_e32 v0, 10, v0
	v_lshl_add_u64 v[34:35], v[6:7], 0, v[0:1]
	ds_read2_b32 v[30:31], v19 offset1:32
	global_store_dwordx4 v[34:35], v[26:29], off sc1
	ds_read2_b32 v[26:27], v19 offset0:64 offset1:96
	v_add_u32_e32 v25, 0x400, v19
	ds_read2_b32 v[32:33], v25 offset1:32
	s_waitcnt lgkmcnt(2)
	v_mul_f32_e32 v0, 0x41800000, v30
	ds_read2_b32 v[28:29], v25 offset0:64 offset1:96
	v_mul_f32_e32 v35, 0x41800000, v31
	s_waitcnt lgkmcnt(2)
	v_mul_f32_e32 v37, 0x41800000, v26
	ds_read2_b32 v[30:31], v19 offset0:128 offset1:160
	v_mul_f32_e32 v39, 0x41800000, v27
	ds_read2_b32 v[26:27], v25 offset0:128 offset1:160
	s_waitcnt lgkmcnt(3)
	v_mul_f32_e32 v34, 0x41800000, v32
	v_mul_f32_e32 v36, 0x41800000, v33
	s_waitcnt lgkmcnt(2)
	v_mul_f32_e32 v38, 0x41800000, v28
	v_mul_f32_e32 v40, 0x41800000, v29
	s_waitcnt lgkmcnt(1)
	v_mul_f32_e32 v30, 0x41800000, v30
	ds_read2_b32 v[28:29], v19 offset0:192 offset1:224
	ds_read2_b32 v[32:33], v25 offset0:192 offset1:224
	s_waitcnt lgkmcnt(2)
	v_mul_f32_e32 v25, 0x41800000, v26
	v_mul_f32_e32 v31, 0x41800000, v31
	v_mul_f32_e32 v41, 0x41800000, v27
	v_med3_f32 v0, v0, s33, v233
	v_med3_f32 v27, v35, s33, v233
	v_mov_b32_e32 v26, v1
	v_cvt_pk_fp8_f32 v26, v0, v27
	v_med3_f32 v30, v30, s33, v233
	v_med3_f32 v31, v31, s33, v233
	v_mov_b32_e32 v27, v1
	v_cvt_pk_fp8_f32 v27, v30, v31
	s_waitcnt lgkmcnt(1)
	v_mul_f32_e32 v28, 0x41800000, v28
	v_mul_f32_e32 v29, 0x41800000, v29
	v_med3_f32 v0, v37, s33, v233
	v_med3_f32 v35, v39, s33, v233
	v_cvt_pk_fp8_f32 v26, v0, v35 op_sel:[0,0,1]
	v_med3_f32 v0, v28, s33, v233
	v_med3_f32 v28, v29, s33, v233
	v_cvt_pk_fp8_f32 v27, v0, v28 op_sel:[0,0,1]
	v_med3_f32 v0, v34, s33, v233
	v_med3_f32 v29, v36, s33, v233
	v_mov_b32_e32 v28, v1
	v_cvt_pk_fp8_f32 v28, v0, v29
	v_med3_f32 v25, v25, s33, v233
	v_med3_f32 v31, v41, s33, v233
	v_mov_b32_e32 v29, v1
	v_cvt_pk_fp8_f32 v29, v25, v31
	s_waitcnt lgkmcnt(0)
	v_mul_f32_e32 v32, 0x41800000, v32
	v_mul_f32_e32 v33, 0x41800000, v33
	v_med3_f32 v0, v38, s33, v233
	v_med3_f32 v30, v40, s33, v233
	v_cvt_pk_fp8_f32 v28, v0, v30 op_sel:[0,0,1]
	v_med3_f32 v0, v32, s33, v233
	v_med3_f32 v25, v33, s33, v233
	v_cvt_pk_fp8_f32 v29, v0, v25 op_sel:[0,0,1]
	v_or_b32_e32 v0, s8, v18
	v_lshlrev_b32_e32 v0, 10, v0
	v_lshl_add_u64 v[34:35], v[6:7], 0, v[0:1]
	ds_read2_b32 v[30:31], v21 offset1:32
	global_store_dwordx4 v[34:35], v[26:29], off sc1
	ds_read2_b32 v[26:27], v21 offset0:64 offset1:96
	v_add_u32_e32 v25, 0x400, v21
	ds_read2_b32 v[32:33], v25 offset1:32
	s_waitcnt lgkmcnt(2)
	v_mul_f32_e32 v0, 0x41800000, v30
	ds_read2_b32 v[28:29], v25 offset0:64 offset1:96
	v_mul_f32_e32 v35, 0x41800000, v31
	s_waitcnt lgkmcnt(2)
	v_mul_f32_e32 v37, 0x41800000, v26
	ds_read2_b32 v[30:31], v21 offset0:128 offset1:160
	v_mul_f32_e32 v39, 0x41800000, v27
	ds_read2_b32 v[26:27], v25 offset0:128 offset1:160
	s_waitcnt lgkmcnt(3)
	v_mul_f32_e32 v34, 0x41800000, v32
	v_mul_f32_e32 v36, 0x41800000, v33
	s_waitcnt lgkmcnt(2)
	v_mul_f32_e32 v38, 0x41800000, v28
	v_mul_f32_e32 v40, 0x41800000, v29
	s_waitcnt lgkmcnt(1)
	v_mul_f32_e32 v30, 0x41800000, v30
	ds_read2_b32 v[28:29], v21 offset0:192 offset1:224
	ds_read2_b32 v[32:33], v25 offset0:192 offset1:224
	s_waitcnt lgkmcnt(2)
	v_mul_f32_e32 v25, 0x41800000, v26
	v_mul_f32_e32 v31, 0x41800000, v31
	v_mul_f32_e32 v41, 0x41800000, v27
	v_med3_f32 v0, v0, s33, v233
	v_med3_f32 v27, v35, s33, v233
	v_mov_b32_e32 v26, v1
	v_cvt_pk_fp8_f32 v26, v0, v27
	v_med3_f32 v30, v30, s33, v233
	v_med3_f32 v31, v31, s33, v233
	v_mov_b32_e32 v27, v1
	v_cvt_pk_fp8_f32 v27, v30, v31
	s_waitcnt lgkmcnt(1)
	v_mul_f32_e32 v28, 0x41800000, v28
	v_mul_f32_e32 v29, 0x41800000, v29
	v_med3_f32 v0, v37, s33, v233
	v_med3_f32 v35, v39, s33, v233
	v_cvt_pk_fp8_f32 v26, v0, v35 op_sel:[0,0,1]
	v_med3_f32 v0, v28, s33, v233
	v_med3_f32 v28, v29, s33, v233
	v_cvt_pk_fp8_f32 v27, v0, v28 op_sel:[0,0,1]
	v_med3_f32 v0, v34, s33, v233
	v_med3_f32 v29, v36, s33, v233
	v_mov_b32_e32 v28, v1
	v_cvt_pk_fp8_f32 v28, v0, v29
	v_med3_f32 v25, v25, s33, v233
	v_med3_f32 v31, v41, s33, v233
	v_mov_b32_e32 v29, v1
	v_cvt_pk_fp8_f32 v29, v25, v31
	s_waitcnt lgkmcnt(0)
	v_mul_f32_e32 v32, 0x41800000, v32
	v_mul_f32_e32 v33, 0x41800000, v33
	v_med3_f32 v0, v38, s33, v233
	v_med3_f32 v30, v40, s33, v233
	v_cvt_pk_fp8_f32 v28, v0, v30 op_sel:[0,0,1]
	v_med3_f32 v0, v32, s33, v233
	v_med3_f32 v25, v33, s33, v233
	v_cvt_pk_fp8_f32 v29, v0, v25 op_sel:[0,0,1]
	v_or_b32_e32 v0, s8, v20
	v_lshlrev_b32_e32 v0, 10, v0
	v_lshl_add_u64 v[34:35], v[6:7], 0, v[0:1]
	ds_read2_b32 v[30:31], v23 offset1:32
	global_store_dwordx4 v[34:35], v[26:29], off sc1
	ds_read2_b32 v[26:27], v23 offset0:64 offset1:96
	v_add_u32_e32 v25, 0x400, v23
	ds_read2_b32 v[32:33], v25 offset1:32
	s_waitcnt lgkmcnt(2)
	v_mul_f32_e32 v0, 0x41800000, v30
	ds_read2_b32 v[28:29], v25 offset0:64 offset1:96
	v_mul_f32_e32 v35, 0x41800000, v31
	s_waitcnt lgkmcnt(2)
	v_mul_f32_e32 v37, 0x41800000, v26
	ds_read2_b32 v[30:31], v23 offset0:128 offset1:160
	v_mul_f32_e32 v39, 0x41800000, v27
	ds_read2_b32 v[26:27], v25 offset0:128 offset1:160
	s_waitcnt lgkmcnt(3)
	v_mul_f32_e32 v34, 0x41800000, v32
	v_mul_f32_e32 v36, 0x41800000, v33
	s_waitcnt lgkmcnt(2)
	v_mul_f32_e32 v38, 0x41800000, v28
	v_mul_f32_e32 v40, 0x41800000, v29
	s_waitcnt lgkmcnt(1)
	v_mul_f32_e32 v30, 0x41800000, v30
	ds_read2_b32 v[28:29], v23 offset0:192 offset1:224
	ds_read2_b32 v[32:33], v25 offset0:192 offset1:224
	s_waitcnt lgkmcnt(2)
	v_mul_f32_e32 v25, 0x41800000, v26
	v_mul_f32_e32 v31, 0x41800000, v31
	v_mul_f32_e32 v41, 0x41800000, v27
	v_med3_f32 v0, v0, s33, v233
	v_med3_f32 v27, v35, s33, v233
	v_mov_b32_e32 v26, v1
	v_cvt_pk_fp8_f32 v26, v0, v27
	v_med3_f32 v30, v30, s33, v233
	v_med3_f32 v31, v31, s33, v233
	v_mov_b32_e32 v27, v1
	v_cvt_pk_fp8_f32 v27, v30, v31
	s_waitcnt lgkmcnt(1)
	v_mul_f32_e32 v28, 0x41800000, v28
	v_mul_f32_e32 v29, 0x41800000, v29
	v_med3_f32 v0, v37, s33, v233
	v_med3_f32 v35, v39, s33, v233
	v_cvt_pk_fp8_f32 v26, v0, v35 op_sel:[0,0,1]
	v_med3_f32 v0, v28, s33, v233
	v_med3_f32 v28, v29, s33, v233
	v_cvt_pk_fp8_f32 v27, v0, v28 op_sel:[0,0,1]
	v_med3_f32 v0, v34, s33, v233
	v_med3_f32 v29, v36, s33, v233
	v_mov_b32_e32 v28, v1
	v_cvt_pk_fp8_f32 v28, v0, v29
	v_med3_f32 v25, v25, s33, v233
	v_med3_f32 v31, v41, s33, v233
	v_mov_b32_e32 v29, v1
	v_cvt_pk_fp8_f32 v29, v25, v31
	s_waitcnt lgkmcnt(0)
	v_mul_f32_e32 v32, 0x41800000, v32
	v_mul_f32_e32 v33, 0x41800000, v33
	v_med3_f32 v0, v38, s33, v233
	v_med3_f32 v30, v40, s33, v233
	v_cvt_pk_fp8_f32 v28, v0, v30 op_sel:[0,0,1]
	v_med3_f32 v0, v32, s33, v233
	v_med3_f32 v25, v33, s33, v233
	v_cvt_pk_fp8_f32 v29, v0, v25 op_sel:[0,0,1]
	v_or_b32_e32 v0, s8, v22
	v_lshlrev_b32_e32 v0, 10, v0
	v_lshl_add_u64 v[6:7], v[6:7], 0, v[0:1]
	global_store_dwordx4 v[6:7], v[26:29], off sc1
	s_mov_b64 s[8:9], 0
.LBB0_263:
	s_andn2_b64 vcc, exec, s[8:9]
	s_cbranch_vccnz .LBB0_265
	s_add_u32 s6, s40, s6
	s_addc_u32 s7, s41, s7
	s_lshl_b64 s[8:9], s[4:5], 22
	s_add_u32 s5, s24, s8
	s_addc_u32 s8, s25, s9
	s_and_b32 s9, s51, 0x780
	v_or_b32_e32 v0, s9, v3
	s_and_b32 s20, s49, 0x3e0
	v_lshlrev_b32_e32 v0, 12, v0
	v_lshl_add_u64 v[6:7], s[6:7], 0, v[0:1]
	s_lshl_b32 s20, s20, 2
	v_lshl_add_u64 v[6:7], v[6:7], 0, s[20:21]
	v_lshlrev_b32_e32 v0, 2, v2
	v_lshl_add_u64 v[6:7], v[6:7], 0, v[0:1]
	s_mov_b32 s6, 0x8000
	v_add_co_u32_e32 v30, vcc, s6, v6
	s_mov_b32 s6, 0x10000
	s_nop 0
	v_addc_co_u32_e32 v31, vcc, 0, v7, vcc
	v_add_co_u32_e32 v34, vcc, s6, v6
	s_mov_b32 s6, 0x18000
	s_nop 0
	v_addc_co_u32_e32 v35, vcc, 0, v7, vcc
	v_add_co_u32_e32 v38, vcc, s6, v6
	s_mov_b32 s6, 0x20000
	s_nop 0
	v_addc_co_u32_e32 v39, vcc, 0, v7, vcc
	v_add_co_u32_e32 v42, vcc, s6, v6
	s_mov_b32 s6, 0x28000
	s_nop 0
	v_addc_co_u32_e32 v43, vcc, 0, v7, vcc
	v_add_co_u32_e32 v46, vcc, s6, v6
	s_mov_b32 s6, 0x30000
	s_nop 0
	v_addc_co_u32_e32 v47, vcc, 0, v7, vcc
	v_add_co_u32_e32 v50, vcc, s6, v6
	s_mov_b32 s6, 0x38000
	s_nop 0
	v_addc_co_u32_e32 v51, vcc, 0, v7, vcc
	v_add_co_u32_e32 v54, vcc, s6, v6
	s_mov_b32 s6, 0x40000
	s_nop 0
	v_addc_co_u32_e32 v55, vcc, 0, v7, vcc
	v_add_co_u32_e32 v58, vcc, s6, v6
	s_mov_b32 s6, 0x48000
	s_nop 0
	v_addc_co_u32_e32 v59, vcc, 0, v7, vcc
	v_add_co_u32_e32 v62, vcc, s6, v6
	s_mov_b32 s6, 0x50000
	s_nop 0
	v_addc_co_u32_e32 v63, vcc, 0, v7, vcc
	v_add_co_u32_e32 v68, vcc, s6, v6
	s_mov_b32 s6, 0x58000
	s_nop 0
	v_addc_co_u32_e32 v69, vcc, 0, v7, vcc
	v_add_co_u32_e32 v72, vcc, s6, v6
	s_mov_b32 s6, 0x60000
	s_nop 0
	v_addc_co_u32_e32 v73, vcc, 0, v7, vcc
	global_load_dwordx4 v[26:29], v[6:7], off nt
	s_nop 0
	global_load_dwordx4 v[30:33], v[30:31], off nt
	v_add_co_u32_e32 v76, vcc, s6, v6
	global_load_dwordx4 v[34:37], v[34:35], off nt
	s_nop 0
	global_load_dwordx4 v[38:41], v[38:39], off nt
	v_addc_co_u32_e32 v77, vcc, 0, v7, vcc
	s_mov_b32 s6, 0x68000
	global_load_dwordx4 v[42:45], v[42:43], off nt
	s_nop 0
	global_load_dwordx4 v[46:49], v[46:47], off nt
	v_add_co_u32_e32 v80, vcc, s6, v6
	global_load_dwordx4 v[50:53], v[50:51], off nt
	s_nop 0
	global_load_dwordx4 v[54:57], v[54:55], off nt
	v_addc_co_u32_e32 v81, vcc, 0, v7, vcc
	s_mov_b32 s6, 0x70000
	global_load_dwordx4 v[58:61], v[58:59], off nt
	s_nop 0
	global_load_dwordx4 v[62:65], v[62:63], off nt
	v_add_co_u32_e32 v84, vcc, s6, v6
	global_load_dwordx4 v[68:71], v[68:69], off nt
	s_nop 0
	global_load_dwordx4 v[72:75], v[72:73], off nt
	v_addc_co_u32_e32 v85, vcc, 0, v7, vcc
	s_mov_b32 s6, 0x78000
	global_load_dwordx4 v[76:79], v[76:77], off nt
	s_nop 0
	global_load_dwordx4 v[80:83], v[80:81], off nt
	v_add_co_u32_e32 v6, vcc, s6, v6
	v_add_u32_e32 v0, v8, v4
	s_nop 0
	v_addc_co_u32_e32 v7, vcc, 0, v7, vcc
	global_load_dwordx4 v[84:87], v[84:85], off nt
	s_nop 0
	global_load_dwordx4 v[88:91], v[6:7], off nt
	s_waitcnt vmcnt(0)
	ds_write_b128 v0, v[26:29]
	s_waitcnt vmcnt(14)
	ds_write_b128 v0, v[30:33] offset:1024
	v_add_u32_e32 v0, v8, v9
	s_waitcnt vmcnt(13)
	ds_write_b128 v0, v[34:37] offset:2048
	s_waitcnt vmcnt(12)
	ds_write_b128 v0, v[38:41] offset:3072
	v_add_u32_e32 v0, v8, v10
	s_waitcnt vmcnt(11)
	ds_write_b128 v0, v[42:45] offset:4096
	s_waitcnt vmcnt(10)
	ds_write_b128 v0, v[46:49] offset:5120
	v_add_u32_e32 v0, v8, v11
	s_waitcnt vmcnt(9)
	ds_write_b128 v0, v[50:53] offset:6144
	s_waitcnt vmcnt(8)
	ds_write_b128 v0, v[54:57] offset:7168
	v_add_u32_e32 v0, v8, v12
	s_waitcnt vmcnt(7)
	ds_write_b128 v0, v[58:61] offset:8192
	s_waitcnt vmcnt(6)
	ds_write_b128 v0, v[62:65] offset:9216
	v_add_u32_e32 v0, v8, v13
	s_waitcnt vmcnt(5)
	ds_write_b128 v0, v[68:71] offset:10240
	s_waitcnt vmcnt(4)
	ds_write_b128 v0, v[72:75] offset:11264
	v_add_u32_e32 v0, v8, v14
	s_waitcnt vmcnt(3)
	ds_write_b128 v0, v[76:79] offset:12288
	s_waitcnt vmcnt(2)
	ds_write_b128 v0, v[80:83] offset:13312
	v_add_u32_e32 v0, v8, v15
	s_waitcnt vmcnt(1)
	ds_write_b128 v0, v[84:87] offset:14336
	s_waitcnt vmcnt(0)
	ds_write_b128 v0, v[88:91] offset:15360
	s_waitcnt lgkmcnt(0)
	v_add_u32_e32 v0, 0x400, v17
	ds_read2_b32 v[26:27], v17 offset1:32
	ds_read2_b32 v[28:29], v0 offset1:32
	ds_read2_b32 v[30:31], v17 offset0:64 offset1:96
	ds_read2_b32 v[32:33], v0 offset0:64 offset1:96
	s_add_u32 s6, s5, s9
	s_waitcnt lgkmcnt(3)
	v_mul_f32_e32 v25, 0x42000000, v26
	s_waitcnt lgkmcnt(2)
	v_mul_f32_e32 v34, 0x42000000, v28
	v_mul_f32_e32 v35, 0x42000000, v27
	v_mul_f32_e32 v36, 0x42000000, v29
	s_waitcnt lgkmcnt(1)
	v_mul_f32_e32 v37, 0x42000000, v30
	ds_read2_b32 v[26:27], v17 offset0:128 offset1:160
	s_waitcnt lgkmcnt(1)
	v_mul_f32_e32 v38, 0x42000000, v32
	v_mul_f32_e32 v39, 0x42000000, v31
	ds_read2_b32 v[28:29], v0 offset0:128 offset1:160
	v_mul_f32_e32 v40, 0x42000000, v33
	ds_read2_b32 v[30:31], v17 offset0:192 offset1:224
	ds_read2_b32 v[32:33], v0 offset0:192 offset1:224
	s_waitcnt lgkmcnt(3)
	v_mul_f32_e32 v41, 0x42000000, v26
	v_mul_f32_e32 v27, 0x42000000, v27
	s_waitcnt lgkmcnt(2)
	v_mul_f32_e32 v0, 0x42000000, v28
	s_waitcnt lgkmcnt(1)
	v_mul_f32_e32 v28, 0x42000000, v30
	s_waitcnt lgkmcnt(0)
	v_mul_f32_e32 v30, 0x42000000, v32
	v_mul_f32_e32 v32, 0x42000000, v33
	v_med3_f32 v25, v25, s33, v233
	v_med3_f32 v33, v35, s33, v233
	v_mov_b32_e32 v26, v1
	v_cvt_pk_fp8_f32 v26, v25, v33
	v_med3_f32 v25, v37, s33, v233
	v_med3_f32 v35, v41, s33, v233
	v_med3_f32 v37, v27, s33, v233
	v_mov_b32_e32 v27, v1
	v_cvt_pk_fp8_f32 v27, v35, v37
	v_mul_f32_e32 v31, 0x42000000, v31
	v_med3_f32 v33, v39, s33, v233
	v_cvt_pk_fp8_f32 v26, v25, v33 op_sel:[0,0,1]
	v_med3_f32 v25, v28, s33, v233
	v_med3_f32 v28, v31, s33, v233
	v_mul_f32_e32 v29, 0x42000000, v29
	v_cvt_pk_fp8_f32 v27, v25, v28 op_sel:[0,0,1]
	v_med3_f32 v25, v34, s33, v233
	v_med3_f32 v31, v36, s33, v233
	v_mov_b32_e32 v28, v1
	v_cvt_pk_fp8_f32 v28, v25, v31
	v_med3_f32 v0, v0, s33, v233
	v_med3_f32 v33, v29, s33, v233
	v_mov_b32_e32 v29, v1
	v_cvt_pk_fp8_f32 v29, v0, v33
	v_med3_f32 v25, v38, s33, v233
	v_med3_f32 v31, v40, s33, v233
	v_cvt_pk_fp8_f32 v28, v25, v31 op_sel:[0,0,1]
	v_med3_f32 v0, v30, s33, v233
	v_med3_f32 v25, v32, s33, v233
	s_mul_i32 s5, s4, 0xfffe8000
	v_cvt_pk_fp8_f32 v29, v0, v25 op_sel:[0,0,1]
	v_add_u32_e32 v25, s5, v24
	v_add_u32_e32 v0, 0xffff8000, v25
	s_movk_i32 s5, 0x7c8
	s_addc_u32 s7, s8, 0
	v_and_or_b32 v0, v0, s5, v3
	v_mov_b32_e32 v43, 0x2000
	v_lshl_add_u64 v[6:7], s[6:7], 0, v[4:5]
	v_lshl_or_b32 v0, v0, 11, v43
	v_lshl_add_u64 v[34:35], v[6:7], 0, v[0:1]
	ds_read2_b32 v[30:31], v19 offset1:32
	global_store_dwordx4 v[34:35], v[26:29], off sc1
	ds_read2_b32 v[26:27], v19 offset0:64 offset1:96
	v_add_u32_e32 v36, 0x400, v19
	ds_read2_b32 v[32:33], v36 offset1:32
	s_waitcnt lgkmcnt(2)
	v_mul_f32_e32 v0, 0x42000000, v30
	ds_read2_b32 v[28:29], v36 offset0:64 offset1:96
	v_mul_f32_e32 v35, 0x42000000, v31
	s_waitcnt lgkmcnt(2)
	v_mul_f32_e32 v38, 0x42000000, v26
	ds_read2_b32 v[30:31], v19 offset0:128 offset1:160
	v_mul_f32_e32 v40, 0x42000000, v27
	ds_read2_b32 v[26:27], v36 offset0:128 offset1:160
	s_waitcnt lgkmcnt(3)
	v_mul_f32_e32 v34, 0x42000000, v32
	v_mul_f32_e32 v37, 0x42000000, v33
	s_waitcnt lgkmcnt(2)
	v_mul_f32_e32 v39, 0x42000000, v28
	v_mul_f32_e32 v41, 0x42000000, v29
	s_waitcnt lgkmcnt(1)
	v_mul_f32_e32 v30, 0x42000000, v30
	ds_read2_b32 v[28:29], v19 offset0:192 offset1:224
	ds_read2_b32 v[32:33], v36 offset0:192 offset1:224
	s_waitcnt lgkmcnt(2)
	v_mul_f32_e32 v36, 0x42000000, v26
	v_mul_f32_e32 v31, 0x42000000, v31
	v_mul_f32_e32 v42, 0x42000000, v27
	v_med3_f32 v0, v0, s33, v233
	v_med3_f32 v27, v35, s33, v233
	v_mov_b32_e32 v26, v1
	v_cvt_pk_fp8_f32 v26, v0, v27
	v_med3_f32 v30, v30, s33, v233
	v_med3_f32 v31, v31, s33, v233
	v_mov_b32_e32 v27, v1
	v_cvt_pk_fp8_f32 v27, v30, v31
	s_waitcnt lgkmcnt(1)
	v_mul_f32_e32 v28, 0x42000000, v28
	v_mul_f32_e32 v29, 0x42000000, v29
	v_med3_f32 v0, v38, s33, v233
	v_med3_f32 v35, v40, s33, v233
	v_cvt_pk_fp8_f32 v26, v0, v35 op_sel:[0,0,1]
	v_med3_f32 v0, v28, s33, v233
	v_med3_f32 v28, v29, s33, v233
	v_cvt_pk_fp8_f32 v27, v0, v28 op_sel:[0,0,1]
	v_med3_f32 v0, v34, s33, v233
	v_med3_f32 v29, v37, s33, v233
	v_mov_b32_e32 v28, v1
	v_cvt_pk_fp8_f32 v28, v0, v29
	v_med3_f32 v31, v36, s33, v233
	v_med3_f32 v34, v42, s33, v233
	v_mov_b32_e32 v29, v1
	v_cvt_pk_fp8_f32 v29, v31, v34
	s_waitcnt lgkmcnt(0)
	v_mul_f32_e32 v32, 0x42000000, v32
	v_mul_f32_e32 v33, 0x42000000, v33
	v_med3_f32 v0, v39, s33, v233
	v_med3_f32 v30, v41, s33, v233
	v_cvt_pk_fp8_f32 v28, v0, v30 op_sel:[0,0,1]
	v_med3_f32 v0, v32, s33, v233
	v_med3_f32 v30, v33, s33, v233
	v_cvt_pk_fp8_f32 v29, v0, v30 op_sel:[0,0,1]
	v_add_u32_e32 v0, 0xffff8010, v25
	s_movk_i32 s5, 0x7d8
	v_and_or_b32 v0, v0, s5, v3
	v_lshl_or_b32 v0, v0, 11, v43
	v_lshl_add_u64 v[34:35], v[6:7], 0, v[0:1]
	ds_read2_b32 v[30:31], v21 offset1:32
	global_store_dwordx4 v[34:35], v[26:29], off sc1
	ds_read2_b32 v[26:27], v21 offset0:64 offset1:96
	v_add_u32_e32 v36, 0x400, v21
	ds_read2_b32 v[32:33], v36 offset1:32
	s_waitcnt lgkmcnt(2)
	v_mul_f32_e32 v0, 0x42000000, v30
	ds_read2_b32 v[28:29], v36 offset0:64 offset1:96
	v_mul_f32_e32 v35, 0x42000000, v31
	s_waitcnt lgkmcnt(2)
	v_mul_f32_e32 v38, 0x42000000, v26
	ds_read2_b32 v[30:31], v21 offset0:128 offset1:160
	v_mul_f32_e32 v40, 0x42000000, v27
	ds_read2_b32 v[26:27], v36 offset0:128 offset1:160
	s_waitcnt lgkmcnt(3)
	v_mul_f32_e32 v34, 0x42000000, v32
	v_mul_f32_e32 v37, 0x42000000, v33
	s_waitcnt lgkmcnt(2)
	v_mul_f32_e32 v39, 0x42000000, v28
	v_mul_f32_e32 v41, 0x42000000, v29
	s_waitcnt lgkmcnt(1)
	v_mul_f32_e32 v30, 0x42000000, v30
	ds_read2_b32 v[28:29], v21 offset0:192 offset1:224
	ds_read2_b32 v[32:33], v36 offset0:192 offset1:224
	s_waitcnt lgkmcnt(2)
	v_mul_f32_e32 v36, 0x42000000, v26
	v_mul_f32_e32 v31, 0x42000000, v31
	v_mul_f32_e32 v42, 0x42000000, v27
	v_med3_f32 v0, v0, s33, v233
	v_med3_f32 v27, v35, s33, v233
	v_mov_b32_e32 v26, v1
	v_cvt_pk_fp8_f32 v26, v0, v27
	v_med3_f32 v30, v30, s33, v233
	v_med3_f32 v31, v31, s33, v233
	v_mov_b32_e32 v27, v1
	v_cvt_pk_fp8_f32 v27, v30, v31
	s_waitcnt lgkmcnt(1)
	v_mul_f32_e32 v28, 0x42000000, v28
	v_mul_f32_e32 v29, 0x42000000, v29
	v_med3_f32 v0, v38, s33, v233
	v_med3_f32 v35, v40, s33, v233
	v_cvt_pk_fp8_f32 v26, v0, v35 op_sel:[0,0,1]
	v_med3_f32 v0, v28, s33, v233
	v_med3_f32 v28, v29, s33, v233
	v_cvt_pk_fp8_f32 v27, v0, v28 op_sel:[0,0,1]
	v_med3_f32 v0, v34, s33, v233
	v_med3_f32 v29, v37, s33, v233
	v_mov_b32_e32 v28, v1
	v_cvt_pk_fp8_f32 v28, v0, v29
	v_med3_f32 v31, v36, s33, v233
	v_med3_f32 v34, v42, s33, v233
	v_mov_b32_e32 v29, v1
	v_cvt_pk_fp8_f32 v29, v31, v34
	s_waitcnt lgkmcnt(0)
	v_mul_f32_e32 v32, 0x42000000, v32
	v_mul_f32_e32 v33, 0x42000000, v33
	v_med3_f32 v0, v39, s33, v233
	v_med3_f32 v30, v41, s33, v233
	v_cvt_pk_fp8_f32 v28, v0, v30 op_sel:[0,0,1]
	v_med3_f32 v0, v32, s33, v233
	v_med3_f32 v30, v33, s33, v233
	v_cvt_pk_fp8_f32 v29, v0, v30 op_sel:[0,0,1]
	v_add_u32_e32 v0, 0xffff8020, v25
	s_movk_i32 s5, 0x7e8
	v_and_or_b32 v0, v0, s5, v3
	v_lshl_or_b32 v0, v0, 11, v43
	v_lshl_add_u64 v[34:35], v[6:7], 0, v[0:1]
	ds_read2_b32 v[30:31], v23 offset1:32
	global_store_dwordx4 v[34:35], v[26:29], off sc1
	ds_read2_b32 v[26:27], v23 offset0:64 offset1:96
	v_add_u32_e32 v36, 0x400, v23
	ds_read2_b32 v[32:33], v36 offset1:32
	s_waitcnt lgkmcnt(2)
	v_mul_f32_e32 v0, 0x42000000, v30
	ds_read2_b32 v[28:29], v36 offset0:64 offset1:96
	v_mul_f32_e32 v35, 0x42000000, v31
	s_waitcnt lgkmcnt(2)
	v_mul_f32_e32 v38, 0x42000000, v26
	ds_read2_b32 v[30:31], v23 offset0:128 offset1:160
	v_mul_f32_e32 v40, 0x42000000, v27
	ds_read2_b32 v[26:27], v36 offset0:128 offset1:160
	s_waitcnt lgkmcnt(3)
	v_mul_f32_e32 v34, 0x42000000, v32
	v_mul_f32_e32 v37, 0x42000000, v33
	s_waitcnt lgkmcnt(2)
	v_mul_f32_e32 v39, 0x42000000, v28
	v_mul_f32_e32 v41, 0x42000000, v29
	s_waitcnt lgkmcnt(1)
	v_mul_f32_e32 v30, 0x42000000, v30
	ds_read2_b32 v[28:29], v23 offset0:192 offset1:224
	ds_read2_b32 v[32:33], v36 offset0:192 offset1:224
	s_waitcnt lgkmcnt(2)
	v_mul_f32_e32 v36, 0x42000000, v26
	v_mul_f32_e32 v31, 0x42000000, v31
	v_mul_f32_e32 v42, 0x42000000, v27
	v_med3_f32 v0, v0, s33, v233
	v_med3_f32 v27, v35, s33, v233
	v_mov_b32_e32 v26, v1
	v_cvt_pk_fp8_f32 v26, v0, v27
	v_med3_f32 v30, v30, s33, v233
	v_med3_f32 v31, v31, s33, v233
	v_mov_b32_e32 v27, v1
	v_cvt_pk_fp8_f32 v27, v30, v31
	s_waitcnt lgkmcnt(1)
	v_mul_f32_e32 v28, 0x42000000, v28
	v_mul_f32_e32 v29, 0x42000000, v29
	v_med3_f32 v0, v38, s33, v233
	v_med3_f32 v35, v40, s33, v233
	v_cvt_pk_fp8_f32 v26, v0, v35 op_sel:[0,0,1]
	v_med3_f32 v0, v28, s33, v233
	v_med3_f32 v28, v29, s33, v233
	v_cvt_pk_fp8_f32 v27, v0, v28 op_sel:[0,0,1]
	v_med3_f32 v0, v34, s33, v233
	v_med3_f32 v29, v37, s33, v233
	v_mov_b32_e32 v28, v1
	v_cvt_pk_fp8_f32 v28, v0, v29
	v_med3_f32 v31, v36, s33, v233
	v_med3_f32 v34, v42, s33, v233
	v_mov_b32_e32 v29, v1
	v_cvt_pk_fp8_f32 v29, v31, v34
	s_waitcnt lgkmcnt(0)
	v_mul_f32_e32 v32, 0x42000000, v32
	v_mul_f32_e32 v33, 0x42000000, v33
	v_med3_f32 v0, v39, s33, v233
	v_med3_f32 v30, v41, s33, v233
	v_cvt_pk_fp8_f32 v28, v0, v30 op_sel:[0,0,1]
	v_med3_f32 v0, v32, s33, v233
	v_med3_f32 v30, v33, s33, v233
	v_cvt_pk_fp8_f32 v29, v0, v30 op_sel:[0,0,1]
	v_add_u32_e32 v0, 0xffff8030, v25
	s_movk_i32 s5, 0x7f8
	v_and_or_b32 v0, v0, s5, v3
	v_lshl_or_b32 v0, v0, 11, v43
	v_lshl_add_u64 v[6:7], v[6:7], 0, v[0:1]
	global_store_dwordx4 v[6:7], v[26:29], off sc1
.LBB0_265:
	s_mov_b64 s[6:7], 0
.LBB0_266:
	s_andn2_b64 vcc, exec, s[6:7]
	s_cbranch_vccnz .LBB0_259
	s_ashr_i32 s5, s4, 31
	s_lshl_b64 s[6:7], s[4:5], 23
	s_add_u32 s6, s38, s6
	s_addc_u32 s7, s39, s7
	s_lshl_b64 s[4:5], s[4:5], 22
	s_add_u32 s8, s24, s4
	s_addc_u32 s9, s25, s5
	s_bfe_u32 s4, s55, 0x5001a
	s_add_i32 s4, s55, s4
	s_sext_i32_i16 s5, s4
	s_lshl_b32 s5, s5, 2
	s_and_b32 s4, s4, 0xffe0
	s_and_b32 s20, s5, 0xffffff80
	s_sub_i32 s4, s55, s4
	v_or_b32_e32 v6, s20, v3
	s_sext_i32_i16 s4, s4
	v_ashrrev_i32_e32 v7, 31, v6
	s_lshl_b32 s4, s4, 5
	v_lshlrev_b64 v[6:7], 12, v[6:7]
	v_lshl_add_u64 v[6:7], s[6:7], 0, v[6:7]
	s_ashr_i32 s5, s4, 31
	v_lshl_add_u64 v[6:7], s[4:5], 2, v[6:7]
	v_lshlrev_b32_e32 v0, 2, v2
	v_lshl_add_u64 v[6:7], v[6:7], 0, v[0:1]
	s_mov_b32 s5, 0x8000
	v_add_co_u32_e32 v30, vcc, s5, v6
	s_mov_b32 s5, 0x10000
	s_nop 0
	v_addc_co_u32_e32 v31, vcc, 0, v7, vcc
	v_add_co_u32_e32 v34, vcc, s5, v6
	s_mov_b32 s5, 0x18000
	s_nop 0
	v_addc_co_u32_e32 v35, vcc, 0, v7, vcc
	v_add_co_u32_e32 v38, vcc, s5, v6
	s_mov_b32 s5, 0x20000
	s_nop 0
	v_addc_co_u32_e32 v39, vcc, 0, v7, vcc
	v_add_co_u32_e32 v42, vcc, s5, v6
	s_mov_b32 s5, 0x28000
	s_nop 0
	v_addc_co_u32_e32 v43, vcc, 0, v7, vcc
	v_add_co_u32_e32 v46, vcc, s5, v6
	s_mov_b32 s5, 0x30000
	s_nop 0
	v_addc_co_u32_e32 v47, vcc, 0, v7, vcc
	v_add_co_u32_e32 v50, vcc, s5, v6
	s_mov_b32 s5, 0x38000
	s_nop 0
	v_addc_co_u32_e32 v51, vcc, 0, v7, vcc
	v_add_co_u32_e32 v54, vcc, s5, v6
	s_mov_b32 s5, 0x40000
	s_nop 0
	v_addc_co_u32_e32 v55, vcc, 0, v7, vcc
	v_add_co_u32_e32 v58, vcc, s5, v6
	s_mov_b32 s5, 0x48000
	s_nop 0
	v_addc_co_u32_e32 v59, vcc, 0, v7, vcc
	v_add_co_u32_e32 v62, vcc, s5, v6
	s_mov_b32 s5, 0x50000
	s_nop 0
	v_addc_co_u32_e32 v63, vcc, 0, v7, vcc
	v_add_co_u32_e32 v68, vcc, s5, v6
	s_mov_b32 s5, 0x58000
	s_nop 0
	v_addc_co_u32_e32 v69, vcc, 0, v7, vcc
	v_add_co_u32_e32 v72, vcc, s5, v6
	s_mov_b32 s5, 0x60000
	s_nop 0
	v_addc_co_u32_e32 v73, vcc, 0, v7, vcc
	global_load_dwordx4 v[26:29], v[6:7], off nt
	s_nop 0
	global_load_dwordx4 v[30:33], v[30:31], off nt
	v_add_co_u32_e32 v76, vcc, s5, v6
	global_load_dwordx4 v[34:37], v[34:35], off nt
	s_nop 0
	global_load_dwordx4 v[38:41], v[38:39], off nt
	v_addc_co_u32_e32 v77, vcc, 0, v7, vcc
	s_mov_b32 s5, 0x68000
	global_load_dwordx4 v[42:45], v[42:43], off nt
	s_nop 0
	global_load_dwordx4 v[46:49], v[46:47], off nt
	v_add_co_u32_e32 v80, vcc, s5, v6
	global_load_dwordx4 v[50:53], v[50:51], off nt
	s_nop 0
	global_load_dwordx4 v[54:57], v[54:55], off nt
	v_addc_co_u32_e32 v81, vcc, 0, v7, vcc
	s_mov_b32 s5, 0x70000
	global_load_dwordx4 v[58:61], v[58:59], off nt
	s_nop 0
	global_load_dwordx4 v[62:65], v[62:63], off nt
	v_add_co_u32_e32 v84, vcc, s5, v6
	global_load_dwordx4 v[68:71], v[68:69], off nt
	s_nop 0
	global_load_dwordx4 v[72:75], v[72:73], off nt
	v_addc_co_u32_e32 v85, vcc, 0, v7, vcc
	s_mov_b32 s5, 0x78000
	global_load_dwordx4 v[76:79], v[76:77], off nt
	s_nop 0
	global_load_dwordx4 v[80:83], v[80:81], off nt
	v_add_co_u32_e32 v6, vcc, s5, v6
	v_add_u32_e32 v0, v8, v4
	s_nop 0
	v_addc_co_u32_e32 v7, vcc, 0, v7, vcc
	global_load_dwordx4 v[84:87], v[84:85], off nt
	s_nop 0
	global_load_dwordx4 v[88:91], v[6:7], off nt
	s_waitcnt vmcnt(0)
	ds_write_b128 v0, v[26:29]
	s_waitcnt vmcnt(14)
	ds_write_b128 v0, v[30:33] offset:1024
	v_add_u32_e32 v0, v8, v9
	s_waitcnt vmcnt(13)
	ds_write_b128 v0, v[34:37] offset:2048
	s_waitcnt vmcnt(12)
	ds_write_b128 v0, v[38:41] offset:3072
	v_add_u32_e32 v0, v8, v10
	s_waitcnt vmcnt(11)
	ds_write_b128 v0, v[42:45] offset:4096
	s_waitcnt vmcnt(10)
	ds_write_b128 v0, v[46:49] offset:5120
	v_add_u32_e32 v0, v8, v11
	s_waitcnt vmcnt(9)
	ds_write_b128 v0, v[50:53] offset:6144
	s_waitcnt vmcnt(8)
	ds_write_b128 v0, v[54:57] offset:7168
	v_add_u32_e32 v0, v8, v12
	s_waitcnt vmcnt(7)
	ds_write_b128 v0, v[58:61] offset:8192
	s_waitcnt vmcnt(6)
	ds_write_b128 v0, v[62:65] offset:9216
	v_add_u32_e32 v0, v8, v13
	s_waitcnt vmcnt(5)
	ds_write_b128 v0, v[68:71] offset:10240
	s_waitcnt vmcnt(4)
	ds_write_b128 v0, v[72:75] offset:11264
	v_add_u32_e32 v0, v8, v14
	s_waitcnt vmcnt(3)
	ds_write_b128 v0, v[76:79] offset:12288
	s_waitcnt vmcnt(2)
	ds_write_b128 v0, v[80:83] offset:13312
	v_add_u32_e32 v0, v8, v15
	s_waitcnt vmcnt(1)
	ds_write_b128 v0, v[84:87] offset:14336
	s_waitcnt vmcnt(0)
	ds_write_b128 v0, v[88:91] offset:15360
	s_waitcnt lgkmcnt(0)
	v_add_u32_e32 v0, 0x400, v17
	ds_read2_b32 v[26:27], v17 offset1:32
	ds_read2_b32 v[28:29], v0 offset1:32
	ds_read2_b32 v[30:31], v17 offset0:64 offset1:96
	ds_read2_b32 v[32:33], v0 offset0:64 offset1:96
	s_ashr_i32 s5, s20, 31
	s_waitcnt lgkmcnt(3)
	v_mul_f32_e32 v25, 0x42000000, v26
	s_waitcnt lgkmcnt(2)
	v_mul_f32_e32 v34, 0x42000000, v28
	v_mul_f32_e32 v35, 0x42000000, v27
	v_mul_f32_e32 v36, 0x42000000, v29
	s_waitcnt lgkmcnt(1)
	v_mul_f32_e32 v37, 0x42000000, v30
	ds_read2_b32 v[26:27], v17 offset0:128 offset1:160
	s_waitcnt lgkmcnt(1)
	v_mul_f32_e32 v38, 0x42000000, v32
	v_mul_f32_e32 v39, 0x42000000, v31
	ds_read2_b32 v[28:29], v0 offset0:128 offset1:160
	v_mul_f32_e32 v40, 0x42000000, v33
	ds_read2_b32 v[30:31], v17 offset0:192 offset1:224
	ds_read2_b32 v[32:33], v0 offset0:192 offset1:224
	s_waitcnt lgkmcnt(3)
	v_mul_f32_e32 v41, 0x42000000, v26
	v_mul_f32_e32 v27, 0x42000000, v27
	s_waitcnt lgkmcnt(2)
	v_mul_f32_e32 v0, 0x42000000, v28
	s_waitcnt lgkmcnt(1)
	v_mul_f32_e32 v28, 0x42000000, v30
	s_waitcnt lgkmcnt(0)
	v_mul_f32_e32 v30, 0x42000000, v32
	v_mul_f32_e32 v32, 0x42000000, v33
	v_med3_f32 v25, v25, s33, v233
	v_med3_f32 v33, v35, s33, v233
	v_mov_b32_e32 v26, v1
	v_cvt_pk_fp8_f32 v26, v25, v33
	v_med3_f32 v25, v37, s33, v233
	v_med3_f32 v35, v41, s33, v233
	v_med3_f32 v37, v27, s33, v233
	v_mov_b32_e32 v27, v1
	v_cvt_pk_fp8_f32 v27, v35, v37
	v_mul_f32_e32 v31, 0x42000000, v31
	v_med3_f32 v33, v39, s33, v233
	v_cvt_pk_fp8_f32 v26, v25, v33 op_sel:[0,0,1]
	v_med3_f32 v25, v28, s33, v233
	v_med3_f32 v28, v31, s33, v233
	v_mul_f32_e32 v29, 0x42000000, v29
	v_cvt_pk_fp8_f32 v27, v25, v28 op_sel:[0,0,1]
	v_med3_f32 v25, v34, s33, v233
	v_med3_f32 v31, v36, s33, v233
	v_mov_b32_e32 v28, v1
	v_cvt_pk_fp8_f32 v28, v25, v31
	v_med3_f32 v0, v0, s33, v233
	v_med3_f32 v33, v29, s33, v233
	v_mov_b32_e32 v29, v1
	v_cvt_pk_fp8_f32 v29, v0, v33
	v_med3_f32 v25, v38, s33, v233
	v_med3_f32 v31, v40, s33, v233
	v_cvt_pk_fp8_f32 v28, v25, v31 op_sel:[0,0,1]
	v_med3_f32 v0, v30, s33, v233
	v_med3_f32 v25, v32, s33, v233
	s_add_u32 s6, s8, s20
	v_cvt_pk_fp8_f32 v29, v0, v25 op_sel:[0,0,1]
	v_or_b32_e32 v0, s4, v3
	s_addc_u32 s7, s9, s5
	v_lshlrev_b32_e32 v0, 1, v0
	s_movk_i32 s5, 0xffc8
	v_and_or_b32 v30, v0, s5, v16
	v_ashrrev_i32_e32 v31, 31, v30
	v_lshl_add_u64 v[6:7], s[6:7], 0, v[4:5]
	v_lshlrev_b64 v[30:31], 11, v[30:31]
	v_lshl_add_u64 v[30:31], v[6:7], 0, v[30:31]
	global_store_dwordx4 v[30:31], v[26:29], off sc1
	ds_read2_b32 v[26:27], v19 offset0:64 offset1:96
	ds_read2_b32 v[32:33], v19 offset1:32
	v_add_u32_e32 v0, 0x400, v19
	ds_read2_b32 v[28:29], v0 offset0:64 offset1:96
	ds_read2_b32 v[30:31], v19 offset0:128 offset1:160
	s_waitcnt lgkmcnt(3)
	v_mul_f32_e32 v37, 0x42000000, v26
	v_mul_f32_e32 v39, 0x42000000, v27
	ds_read2_b32 v[26:27], v0 offset0:128 offset1:160
	s_waitcnt lgkmcnt(3)
	v_mul_f32_e32 v25, 0x42000000, v32
	v_mul_f32_e32 v36, 0x42000000, v33
	ds_read2_b32 v[34:35], v0 offset1:32
	s_waitcnt lgkmcnt(3)
	v_mul_f32_e32 v38, 0x42000000, v28
	v_mul_f32_e32 v40, 0x42000000, v29
	s_waitcnt lgkmcnt(2)
	v_mul_f32_e32 v30, 0x42000000, v30
	ds_read2_b32 v[28:29], v19 offset0:192 offset1:224
	ds_read2_b32 v[32:33], v0 offset0:192 offset1:224
	s_waitcnt lgkmcnt(3)
	v_mul_f32_e32 v0, 0x42000000, v26
	v_mul_f32_e32 v31, 0x42000000, v31
	v_mul_f32_e32 v41, 0x42000000, v27
	v_med3_f32 v25, v25, s33, v233
	v_med3_f32 v27, v36, s33, v233
	v_mov_b32_e32 v26, v1
	v_cvt_pk_fp8_f32 v26, v25, v27
	v_med3_f32 v30, v30, s33, v233
	v_med3_f32 v31, v31, s33, v233
	v_mov_b32_e32 v27, v1
	v_cvt_pk_fp8_f32 v27, v30, v31
	s_waitcnt lgkmcnt(1)
	v_mul_f32_e32 v28, 0x42000000, v28
	v_mul_f32_e32 v29, 0x42000000, v29
	v_med3_f32 v25, v37, s33, v233
	v_med3_f32 v36, v39, s33, v233
	v_mul_f32_e32 v34, 0x42000000, v34
	v_mul_f32_e32 v35, 0x42000000, v35
	v_cvt_pk_fp8_f32 v26, v25, v36 op_sel:[0,0,1]
	v_med3_f32 v25, v28, s33, v233
	v_med3_f32 v28, v29, s33, v233
	v_cvt_pk_fp8_f32 v27, v25, v28 op_sel:[0,0,1]
	v_med3_f32 v25, v34, s33, v233
	v_med3_f32 v29, v35, s33, v233
	v_mov_b32_e32 v28, v1
	v_cvt_pk_fp8_f32 v28, v25, v29
	v_med3_f32 v0, v0, s33, v233
	v_med3_f32 v31, v41, s33, v233
	v_mov_b32_e32 v29, v1
	v_cvt_pk_fp8_f32 v29, v0, v31
	s_waitcnt lgkmcnt(0)
	v_mul_f32_e32 v32, 0x42000000, v32
	v_mul_f32_e32 v33, 0x42000000, v33
	v_med3_f32 v25, v38, s33, v233
	v_med3_f32 v30, v40, s33, v233
	v_cvt_pk_fp8_f32 v28, v25, v30 op_sel:[0,0,1]
	v_med3_f32 v0, v32, s33, v233
	v_med3_f32 v25, v33, s33, v233
	v_cvt_pk_fp8_f32 v29, v0, v25 op_sel:[0,0,1]
	v_or_b32_e32 v0, s4, v18
	v_lshlrev_b32_e32 v0, 1, v0
	s_movk_i32 s5, 0xffd8
	v_and_or_b32 v30, v0, s5, v16
	v_ashrrev_i32_e32 v31, 31, v30
	v_lshlrev_b64 v[30:31], 11, v[30:31]
	v_lshl_add_u64 v[30:31], v[6:7], 0, v[30:31]
	global_store_dwordx4 v[30:31], v[26:29], off sc1
	ds_read2_b32 v[26:27], v21 offset0:64 offset1:96
	ds_read2_b32 v[32:33], v21 offset1:32
	v_add_u32_e32 v0, 0x400, v21
	ds_read2_b32 v[28:29], v0 offset0:64 offset1:96
	ds_read2_b32 v[30:31], v21 offset0:128 offset1:160
	s_waitcnt lgkmcnt(3)
	v_mul_f32_e32 v37, 0x42000000, v26
	v_mul_f32_e32 v39, 0x42000000, v27
	ds_read2_b32 v[26:27], v0 offset0:128 offset1:160
	s_waitcnt lgkmcnt(3)
	v_mul_f32_e32 v25, 0x42000000, v32
	v_mul_f32_e32 v36, 0x42000000, v33
	ds_read2_b32 v[34:35], v0 offset1:32
	s_waitcnt lgkmcnt(3)
	v_mul_f32_e32 v38, 0x42000000, v28
	v_mul_f32_e32 v40, 0x42000000, v29
	s_waitcnt lgkmcnt(2)
	v_mul_f32_e32 v30, 0x42000000, v30
	ds_read2_b32 v[28:29], v21 offset0:192 offset1:224
	ds_read2_b32 v[32:33], v0 offset0:192 offset1:224
	s_waitcnt lgkmcnt(3)
	v_mul_f32_e32 v0, 0x42000000, v26
	v_mul_f32_e32 v31, 0x42000000, v31
	v_mul_f32_e32 v41, 0x42000000, v27
	v_med3_f32 v25, v25, s33, v233
	v_med3_f32 v27, v36, s33, v233
	v_mov_b32_e32 v26, v1
	v_cvt_pk_fp8_f32 v26, v25, v27
	v_med3_f32 v30, v30, s33, v233
	v_med3_f32 v31, v31, s33, v233
	v_mov_b32_e32 v27, v1
	v_cvt_pk_fp8_f32 v27, v30, v31
	s_waitcnt lgkmcnt(1)
	v_mul_f32_e32 v28, 0x42000000, v28
	v_mul_f32_e32 v29, 0x42000000, v29
	v_med3_f32 v25, v37, s33, v233
	v_med3_f32 v36, v39, s33, v233
	v_mul_f32_e32 v34, 0x42000000, v34
	v_mul_f32_e32 v35, 0x42000000, v35
	v_cvt_pk_fp8_f32 v26, v25, v36 op_sel:[0,0,1]
	v_med3_f32 v25, v28, s33, v233
	v_med3_f32 v28, v29, s33, v233
	v_cvt_pk_fp8_f32 v27, v25, v28 op_sel:[0,0,1]
	v_med3_f32 v25, v34, s33, v233
	v_med3_f32 v29, v35, s33, v233
	v_mov_b32_e32 v28, v1
	v_cvt_pk_fp8_f32 v28, v25, v29
	v_med3_f32 v0, v0, s33, v233
	v_med3_f32 v31, v41, s33, v233
	v_mov_b32_e32 v29, v1
	v_cvt_pk_fp8_f32 v29, v0, v31
	s_waitcnt lgkmcnt(0)
	v_mul_f32_e32 v32, 0x42000000, v32
	v_mul_f32_e32 v33, 0x42000000, v33
	v_med3_f32 v25, v38, s33, v233
	v_med3_f32 v30, v40, s33, v233
	v_cvt_pk_fp8_f32 v28, v25, v30 op_sel:[0,0,1]
	v_med3_f32 v0, v32, s33, v233
	v_med3_f32 v25, v33, s33, v233
	v_cvt_pk_fp8_f32 v29, v0, v25 op_sel:[0,0,1]
	v_or_b32_e32 v0, s4, v20
	v_lshlrev_b32_e32 v0, 1, v0
	s_movk_i32 s5, 0xffe8
	v_and_or_b32 v30, v0, s5, v16
	v_ashrrev_i32_e32 v31, 31, v30
	v_lshlrev_b64 v[30:31], 11, v[30:31]
	v_lshl_add_u64 v[30:31], v[6:7], 0, v[30:31]
	global_store_dwordx4 v[30:31], v[26:29], off sc1
	ds_read2_b32 v[26:27], v23 offset0:64 offset1:96
	ds_read2_b32 v[32:33], v23 offset1:32
	v_add_u32_e32 v0, 0x400, v23
	ds_read2_b32 v[28:29], v0 offset0:64 offset1:96
	ds_read2_b32 v[30:31], v23 offset0:128 offset1:160
	s_waitcnt lgkmcnt(3)
	v_mul_f32_e32 v37, 0x42000000, v26
	v_mul_f32_e32 v39, 0x42000000, v27
	ds_read2_b32 v[26:27], v0 offset0:128 offset1:160
	s_waitcnt lgkmcnt(3)
	v_mul_f32_e32 v25, 0x42000000, v32
	v_mul_f32_e32 v36, 0x42000000, v33
	ds_read2_b32 v[34:35], v0 offset1:32
	s_waitcnt lgkmcnt(3)
	v_mul_f32_e32 v38, 0x42000000, v28
	v_mul_f32_e32 v40, 0x42000000, v29
	s_waitcnt lgkmcnt(2)
	v_mul_f32_e32 v30, 0x42000000, v30
	ds_read2_b32 v[28:29], v23 offset0:192 offset1:224
	ds_read2_b32 v[32:33], v0 offset0:192 offset1:224
	s_waitcnt lgkmcnt(3)
	v_mul_f32_e32 v0, 0x42000000, v26
	v_mul_f32_e32 v31, 0x42000000, v31
	v_mul_f32_e32 v41, 0x42000000, v27
	v_med3_f32 v25, v25, s33, v233
	v_med3_f32 v27, v36, s33, v233
	v_mov_b32_e32 v26, v1
	v_cvt_pk_fp8_f32 v26, v25, v27
	v_med3_f32 v30, v30, s33, v233
	v_med3_f32 v31, v31, s33, v233
	v_mov_b32_e32 v27, v1
	v_cvt_pk_fp8_f32 v27, v30, v31
	s_waitcnt lgkmcnt(1)
	v_mul_f32_e32 v28, 0x42000000, v28
	v_mul_f32_e32 v29, 0x42000000, v29
	v_med3_f32 v25, v37, s33, v233
	v_med3_f32 v36, v39, s33, v233
	v_mul_f32_e32 v34, 0x42000000, v34
	v_mul_f32_e32 v35, 0x42000000, v35
	v_cvt_pk_fp8_f32 v26, v25, v36 op_sel:[0,0,1]
	v_med3_f32 v25, v28, s33, v233
	v_med3_f32 v28, v29, s33, v233
	v_cvt_pk_fp8_f32 v27, v25, v28 op_sel:[0,0,1]
	v_med3_f32 v25, v34, s33, v233
	v_med3_f32 v29, v35, s33, v233
	v_mov_b32_e32 v28, v1
	v_cvt_pk_fp8_f32 v28, v25, v29
	v_med3_f32 v0, v0, s33, v233
	v_med3_f32 v31, v41, s33, v233
	v_mov_b32_e32 v29, v1
	v_cvt_pk_fp8_f32 v29, v0, v31
	s_waitcnt lgkmcnt(0)
	v_mul_f32_e32 v32, 0x42000000, v32
	v_mul_f32_e32 v33, 0x42000000, v33
	v_med3_f32 v25, v38, s33, v233
	v_med3_f32 v30, v40, s33, v233
	v_cvt_pk_fp8_f32 v28, v25, v30 op_sel:[0,0,1]
	v_med3_f32 v0, v32, s33, v233
	v_med3_f32 v25, v33, s33, v233
	v_cvt_pk_fp8_f32 v29, v0, v25 op_sel:[0,0,1]
	v_or_b32_e32 v0, s4, v22
	v_lshlrev_b32_e32 v0, 1, v0
	v_and_or_b32 v30, v0, -8, v16
	v_ashrrev_i32_e32 v31, 31, v30
	v_lshlrev_b64 v[30:31], 11, v[30:31]
	v_lshl_add_u64 v[6:7], v[6:7], 0, v[30:31]
	global_store_dwordx4 v[6:7], v[26:29], off sc1
	s_branch .LBB0_259

.LBB0_274:
	v_add_co_u32_e32 v34, vcc, 0xfffff000, v108
	s_add_i32 s24, s24, s66
	s_nop 0
	v_addc_co_u32_e32 v35, vcc, -1, v109, vcc
	global_load_dwordx4 v[126:129], v[34:35], off offset:-3072 nt
	global_load_dwordx4 v[58:61], v[34:35], off offset:-2048 nt
	global_load_dwordx4 v[54:57], v[34:35], off offset:-1024 nt
	global_load_dwordx4 v[50:53], v[108:109], off offset:-4096 nt
	global_load_dwordx4 v[46:49], v[108:109], off offset:-3072 nt
	global_load_dwordx4 v[42:45], v[108:109], off offset:-2048 nt
	global_load_dwordx4 v[38:41], v[108:109], off offset:-1024 nt
	s_nop 0
	global_load_dwordx4 v[34:37], v[108:109], off nt
	v_lshl_add_u64 v[108:109], v[108:109], 0, s[28:29]
	s_cmp_ge_i32 s24, s25
	s_waitcnt vmcnt(7)
	v_mul_f32_e32 v110, v127, v127
	v_mul_f32_e32 v112, v129, v129
	v_fmac_f32_e32 v110, v126, v126
	v_fmac_f32_e32 v112, v128, v128
	v_add_f32_e32 v110, v110, v112
	s_waitcnt vmcnt(6)
	v_mul_f32_e32 v112, v59, v59
	v_mul_f32_e32 v113, v61, v61
	v_fmac_f32_e32 v112, v58, v58
	v_fmac_f32_e32 v113, v60, v60
	v_add_f32_e32 v112, v112, v113
	v_add_f32_e32 v110, v110, v112
	s_waitcnt vmcnt(5)
	v_mul_f32_e32 v112, v55, v55
	v_mul_f32_e32 v113, v57, v57
	v_fmac_f32_e32 v112, v54, v54
	v_fmac_f32_e32 v113, v56, v56
	v_add_f32_e32 v112, v112, v113
	v_add_f32_e32 v110, v110, v112
	s_waitcnt vmcnt(4)
	v_mul_f32_e32 v112, v51, v51
	v_mul_f32_e32 v113, v53, v53
	v_fmac_f32_e32 v112, v50, v50
	v_fmac_f32_e32 v113, v52, v52
	v_add_f32_e32 v112, v112, v113
	v_add_f32_e32 v110, v110, v112
	s_waitcnt vmcnt(3)
	v_mul_f32_e32 v112, v47, v47
	v_mul_f32_e32 v113, v49, v49
	v_fmac_f32_e32 v112, v46, v46
	v_fmac_f32_e32 v113, v48, v48
	v_add_f32_e32 v112, v112, v113
	v_add_f32_e32 v110, v110, v112
	s_waitcnt vmcnt(2)
	v_mul_f32_e32 v112, v43, v43
	v_mul_f32_e32 v113, v45, v45
	v_fmac_f32_e32 v112, v42, v42
	v_fmac_f32_e32 v113, v44, v44
	v_add_f32_e32 v112, v112, v113
	v_add_f32_e32 v110, v110, v112
	s_waitcnt vmcnt(1)
	v_mul_f32_e32 v112, v39, v39
	v_mul_f32_e32 v113, v41, v41
	v_fmac_f32_e32 v112, v38, v38
	v_fmac_f32_e32 v113, v40, v40
	v_add_f32_e32 v112, v112, v113
	v_add_f32_e32 v110, v110, v112
	s_waitcnt vmcnt(0)
	v_mul_f32_e32 v112, v35, v35
	v_mul_f32_e32 v113, v37, v37
	v_fmac_f32_e32 v112, v34, v34
	v_fmac_f32_e32 v113, v36, v36
	v_add_f32_e32 v112, v112, v113
	v_add_f32_e32 v110, v110, v112
	s_nop 1
	v_mov_b32_dpp v112, v110 quad_perm:[1,0,3,2] row_mask:0xf bank_mask:0xf
	s_waitcnt lgkmcnt(0)
	v_add_f32_e32 v110, v110, v112
	s_nop 1
	v_mov_b32_dpp v112, v110 quad_perm:[2,3,0,1] row_mask:0xf bank_mask:0xf
	v_add_f32_e32 v110, v110, v112
	s_nop 1
	v_mov_b32_dpp v112, v110 row_half_mirror row_mask:0xf bank_mask:0xf
	v_add_f32_e32 v110, v110, v112
	s_nop 1
	v_mov_b32_dpp v112, v110 row_mirror row_mask:0xf bank_mask:0xf
	v_add_f32_e32 v110, v110, v112
	v_mov_b32_e32 v112, v110
	s_nop 1
	v_permlane16_swap_b32_e32 v110, v112
	v_add_f32_e32 v110, v110, v112
	v_mov_b32_e32 v112, v110
	s_nop 1
	v_permlane32_swap_b32_e32 v110, v112
	v_add_f32_e32 v110, v110, v112
	v_fmamk_f32 v110, v110, 0x3a000000, v228
	v_cmp_gt_f32_e32 vcc, s82, v110
	v_mul_f32_e32 v112, 0x4f800000, v110
	s_nop 0
	v_cndmask_b32_e32 v110, v110, v112, vcc
	v_sqrt_f32_e32 v112, v110
	s_nop 0
	v_add_u32_e32 v113, -1, v112
	v_fma_f32 v125, -v113, v112, v110
	v_cmp_ge_f32_e64 s[38:39], 0, v125
	v_add_u32_e32 v125, 1, v112
	s_nop 0
	v_cndmask_b32_e64 v113, v112, v113, s[38:39]
	v_fma_f32 v112, -v125, v112, v110
	v_cmp_lt_f32_e64 s[38:39], 0, v112
	s_nop 1
	v_cndmask_b32_e64 v112, v113, v125, s[38:39]
	v_mul_f32_e32 v113, 0x37800000, v112
	v_cndmask_b32_e32 v112, v112, v113, vcc
	v_cmp_class_f32_e32 vcc, v110, v229
	s_nop 1
	v_cndmask_b32_e32 v110, v112, v110, vcc
	v_div_scale_f32 v112, s[4:5], v110, v110, 1.0
	v_rcp_f32_e32 v113, v112
	s_nop 0
	v_fma_f32 v125, -v112, v113, 1.0
	v_fmac_f32_e32 v113, v125, v113
	v_div_scale_f32 v125, vcc, 1.0, v110, 1.0
	v_mul_f32_e32 v130, v125, v113
	v_fma_f32 v131, -v112, v130, v125
	v_fmac_f32_e32 v130, v131, v113
	v_fma_f32 v112, -v112, v130, v125
	v_div_fmas_f32 v112, v112, v113, v130
	v_div_fixup_f32 v110, v112, v110, 1.0
	v_pk_mul_f32 v[126:127], v[126:127], v[110:111] op_sel_hi:[1,0]
	v_pk_mul_f32 v[112:113], v[128:129], v[110:111] op_sel_hi:[1,0]
	v_pk_fma_f32 v[126:127], v[78:79], v[126:127], v[2:3]
	v_pk_fma_f32 v[112:113], v[76:77], v[112:113], v[4:5]
	v_med3_f32 v125, v126, s33, v233
	v_med3_f32 v126, v127, s33, v233
	v_mov_b32_e32 v127, 0
	v_cvt_pk_fp8_f32 v127, v125, v126
	v_pk_mul_f32 v[58:59], v[58:59], v[110:111] op_sel_hi:[1,0]
	v_med3_f32 v112, v112, s33, v233
	v_med3_f32 v113, v113, s33, v233
	v_pk_fma_f32 v[58:59], v[82:83], v[58:59], v[6:7]
	v_cvt_pk_fp8_f32 v127, v112, v113 op_sel:[0,0,1]
	v_med3_f32 v58, v58, s33, v233
	v_med3_f32 v59, v59, s33, v233
	v_mov_b32_e32 v112, 0
	v_cvt_pk_fp8_f32 v112, v58, v59
	v_pk_mul_f32 v[60:61], v[60:61], v[110:111] op_sel_hi:[1,0]
	v_pk_mul_f32 v[54:55], v[54:55], v[110:111] op_sel_hi:[1,0]
	v_pk_fma_f32 v[60:61], v[80:81], v[60:61], v[8:9]
	v_pk_fma_f32 v[54:55], v[86:87], v[54:55], v[10:11]
	v_med3_f32 v58, v60, s33, v233
	v_med3_f32 v59, v61, s33, v233
	v_cvt_pk_fp8_f32 v112, v58, v59 op_sel:[0,0,1]
	v_med3_f32 v54, v54, s33, v233
	v_med3_f32 v55, v55, s33, v233
	v_mov_b32_e32 v58, 0
	v_cvt_pk_fp8_f32 v58, v54, v55
	v_pk_mul_f32 v[56:57], v[56:57], v[110:111] op_sel_hi:[1,0]
	v_pk_mul_f32 v[50:51], v[50:51], v[110:111] op_sel_hi:[1,0]
	v_pk_fma_f32 v[56:57], v[84:85], v[56:57], v[12:13]
	v_pk_fma_f32 v[50:51], v[90:91], v[50:51], v[14:15]
	v_med3_f32 v54, v56, s33, v233
	v_med3_f32 v55, v57, s33, v233
	v_cvt_pk_fp8_f32 v58, v54, v55 op_sel:[0,0,1]
	v_med3_f32 v50, v50, s33, v233
	v_med3_f32 v51, v51, s33, v233
	v_mov_b32_e32 v54, 0
	v_cvt_pk_fp8_f32 v54, v50, v51
	v_pk_mul_f32 v[52:53], v[52:53], v[110:111] op_sel_hi:[1,0]
	v_pk_mul_f32 v[46:47], v[46:47], v[110:111] op_sel_hi:[1,0]
	v_pk_fma_f32 v[52:53], v[88:89], v[52:53], v[16:17]
	v_pk_fma_f32 v[46:47], v[94:95], v[46:47], v[18:19]
	v_med3_f32 v50, v52, s33, v233
	v_med3_f32 v51, v53, s33, v233
	v_cvt_pk_fp8_f32 v54, v50, v51 op_sel:[0,0,1]
	v_med3_f32 v46, v46, s33, v233
	v_med3_f32 v47, v47, s33, v233
	v_mov_b32_e32 v50, 0
	v_cvt_pk_fp8_f32 v50, v46, v47
	v_pk_mul_f32 v[48:49], v[48:49], v[110:111] op_sel_hi:[1,0]
	v_pk_mul_f32 v[42:43], v[42:43], v[110:111] op_sel_hi:[1,0]
	v_pk_fma_f32 v[48:49], v[92:93], v[48:49], v[20:21]
	v_pk_fma_f32 v[42:43], v[98:99], v[42:43], v[22:23]
	v_med3_f32 v46, v48, s33, v233
	v_med3_f32 v47, v49, s33, v233
	v_cvt_pk_fp8_f32 v50, v46, v47 op_sel:[0,0,1]
	v_med3_f32 v42, v42, s33, v233
	v_med3_f32 v43, v43, s33, v233
	v_mov_b32_e32 v46, 0
	v_cvt_pk_fp8_f32 v46, v42, v43
	v_pk_mul_f32 v[44:45], v[44:45], v[110:111] op_sel_hi:[1,0]
	v_pk_mul_f32 v[38:39], v[38:39], v[110:111] op_sel_hi:[1,0]
	v_pk_fma_f32 v[44:45], v[96:97], v[44:45], v[24:25]
	v_pk_fma_f32 v[38:39], v[102:103], v[38:39], v[26:27]
	v_med3_f32 v42, v44, s33, v233
	v_med3_f32 v43, v45, s33, v233
	v_cvt_pk_fp8_f32 v46, v42, v43 op_sel:[0,0,1]
	v_med3_f32 v38, v38, s33, v233
	v_med3_f32 v39, v39, s33, v233
	v_mov_b32_e32 v42, 0
	v_cvt_pk_fp8_f32 v42, v38, v39
	v_pk_mul_f32 v[40:41], v[40:41], v[110:111] op_sel_hi:[1,0]
	v_pk_mul_f32 v[34:35], v[34:35], v[110:111] op_sel_hi:[1,0]
	v_pk_fma_f32 v[40:41], v[100:101], v[40:41], v[28:29]
	v_pk_fma_f32 v[34:35], v[106:107], v[34:35], v[30:31]
	v_med3_f32 v38, v40, s33, v233
	v_med3_f32 v39, v41, s33, v233
	v_cvt_pk_fp8_f32 v42, v38, v39 op_sel:[0,0,1]
	v_med3_f32 v34, v34, s33, v233
	v_med3_f32 v35, v35, s33, v233
	v_mov_b32_e32 v38, 0
	v_cvt_pk_fp8_f32 v38, v34, v35
	v_pk_mul_f32 v[36:37], v[36:37], v[110:111] op_sel_hi:[1,0]
	global_store_dword v[74:75], v127, off offset:-1792
	v_pk_fma_f32 v[36:37], v[104:105], v[36:37], v[32:33]
	global_store_dword v[74:75], v112, off offset:-1536
	v_med3_f32 v34, v36, s33, v233
	v_med3_f32 v35, v37, s33, v233
	v_cvt_pk_fp8_f32 v38, v34, v35 op_sel:[0,0,1]
	global_store_dword v[74:75], v58, off offset:-1280
	global_store_dword v[74:75], v54, off offset:-1024
	global_store_dword v[74:75], v50, off offset:-768
	global_store_dword v[74:75], v46, off offset:-512
	global_store_dword v[74:75], v42, off offset:-256
	global_store_dword v[74:75], v38, off
	v_lshl_add_u64 v[74:75], v[74:75], 0, s[22:23]
	s_cbranch_scc0 .LBB0_274
	s_branch .LBB0_271

.LBB0_491:
	v_cndmask_b32_e64 v90, 0, 1, s[58:59]
	s_and_b64 vcc, exec, s[4:5]
	v_lshl_add_u64 v[62:63], s[50:51], 0, v[86:87]
	v_cmp_ne_u32_e64 s[42:43], 1, v90
	s_cbranch_vccz .LBB0_494
	v_add_co_u32_e32 v90, vcc, 0x2e200000, v62
	v_cvt_pk_bf16_f32 v124, v120, v121
	v_cvt_pk_bf16_f32 v125, v122, v123
	v_cvt_pk_bf16_f32 v126, v98, v99
	v_cvt_pk_bf16_f32 v127, v64, v65
	s_nop 1
	v_addc_co_u32_e32 v91, vcc, 0, v63, vcc
	s_and_b64 vcc, exec, s[42:43]
	global_store_dwordx4 v[90:91], v[124:127], off sc1
	s_cbranch_vccnz .LBB0_494
	v_mul_f32_e32 v121, v103, v121
	v_mul_f32_e32 v120, v104, v120
	v_mul_f32_e32 v124, v121, v121
	v_fmac_f32_e32 v124, v120, v120
	v_mul_f32_e32 v122, v110, v122
	v_fmac_f32_e32 v124, v122, v122
	v_mul_f32_e32 v123, v109, v123
	v_pk_mul_f32 v[90:91], v[72:73], v[98:99]
	v_fmac_f32_e32 v124, v123, v123
	v_pk_mul_f32 v[98:99], v[90:91], v[90:91]
	v_pk_mul_f32 v[64:65], v[78:79], v[64:65]
	v_add_f32_e32 v98, v98, v124
	v_add_f32_e32 v124, v99, v98
	v_pk_mul_f32 v[98:99], v[64:65], v[64:65]
	s_nop 0
	v_add_f32_e32 v98, v98, v124
	v_and_b32_e32 v124, 64, v226
	v_add_f32_e32 v98, v99, v98
	v_xor_b32_e32 v99, 1, v226
	v_add_u32_e32 v124, 64, v124
	v_cmp_lt_i32_e32 vcc, v99, v124
	s_nop 1
	v_cndmask_b32_e32 v99, v226, v99, vcc
	v_lshlrev_b32_e32 v99, 2, v99
	v_mov_b32_dpp v99, v98 quad_perm:[1,0,3,2] row_mask:0xf bank_mask:0xf
	s_waitcnt lgkmcnt(0)
	v_add_f32_e32 v98, v98, v99
	v_xor_b32_e32 v99, 2, v226
	v_cmp_lt_i32_e32 vcc, v99, v124
	s_nop 1
	v_cndmask_b32_e32 v99, v226, v99, vcc
	v_lshlrev_b32_e32 v99, 2, v99
	v_mov_b32_dpp v99, v98 quad_perm:[2,3,0,1] row_mask:0xf bank_mask:0xf
	v_add_f32_e32 v98, v98, v99
	v_xor_b32_e32 v99, 4, v226
	v_cmp_lt_i32_e32 vcc, v99, v124
	s_nop 1
	v_cndmask_b32_e32 v99, v226, v99, vcc
	v_lshlrev_b32_e32 v99, 2, v99
	v_mov_b32_dpp v99, v98 row_half_mirror row_mask:0xf bank_mask:0xf
	v_add_f32_e32 v98, v98, v99
	v_mul_f32_e32 v99, 0x4f800000, v98
	v_cmp_gt_f32_e32 vcc, s82, v98
	s_nop 1
	v_cndmask_b32_e32 v98, v98, v99, vcc
	v_sqrt_f32_e32 v99, v98
	s_nop 0
	v_add_u32_e32 v124, -1, v99
	v_fma_f32 v125, -v124, v99, v98
	v_cmp_ge_f32_e64 s[46:47], 0, v125
	v_add_u32_e32 v125, 1, v99
	s_nop 0
	v_cndmask_b32_e64 v124, v99, v124, s[46:47]
	v_fma_f32 v99, -v125, v99, v98
	v_cmp_lt_f32_e64 s[46:47], 0, v99
	s_nop 1
	v_cndmask_b32_e64 v99, v124, v125, s[46:47]
	v_mul_f32_e32 v124, 0x37800000, v99
	v_cndmask_b32_e32 v99, v99, v124, vcc
	v_cmp_class_f32_e32 vcc, v98, v229
	s_nop 1
	v_cndmask_b32_e32 v98, v99, v98, vcc
	v_max_f32_e32 v98, 0x2b8cbccc, v98
	v_div_scale_f32 v99, s[4:5], v98, v98, 1.0
	v_rcp_f32_e32 v124, v99
	s_nop 0
	v_fma_f32 v125, -v99, v124, 1.0
	v_fmac_f32_e32 v124, v125, v124
	v_div_scale_f32 v125, vcc, 1.0, v98, 1.0
	v_mul_f32_e32 v126, v125, v124
	v_fma_f32 v127, -v99, v126, v125
	v_fmac_f32_e32 v126, v127, v124
	v_fma_f32 v99, -v99, v126, v125
	v_div_fmas_f32 v99, v99, v124, v126
	v_div_fixup_f32 v98, v99, v98, 1.0
	v_mul_f32_e32 v99, v120, v98
	v_mul_f32_e32 v120, v121, v98
	v_mul_f32_e32 v121, v122, v98
	v_mul_f32_e32 v122, v123, v98
	v_mul_f32_e32 v64, v64, v98
	v_mul_f32_e32 v65, v65, v98
	v_mul_f32_e32 v90, v90, v98
	v_mul_f32_e32 v91, v91, v98
	v_cvt_pk_bf16_f32 v120, v99, v120
	v_cvt_pk_bf16_f32 v121, v121, v122
	v_cvt_pk_bf16_f32 v122, v90, v91
	v_cvt_pk_bf16_f32 v123, v64, v65
	v_lshl_add_u64 v[64:65], s[50:51], 0, v[84:85]
	v_add_co_u32_e32 v64, vcc, 0x2e201000, v64
	s_nop 1
	v_addc_co_u32_e32 v65, vcc, 0, v65, vcc
	global_store_dwordx4 v[64:65], v[120:123], off offset:2048 sc1

.LBB0_528:
	s_and_b64 vcc, exec, s[4:5]
	s_cbranch_vccz .LBB0_531
	v_add_co_u32_e32 v122, vcc, 0x2e202000, v62
	v_cvt_pk_bf16_f32 v92, v115, v114
	v_cvt_pk_bf16_f32 v93, v113, v0
	v_cvt_pk_bf16_f32 v94, v58, v59
	v_cvt_pk_bf16_f32 v95, v60, v61
	s_nop 1
	v_addc_co_u32_e32 v123, vcc, 0, v63, vcc
	s_and_b64 vcc, exec, s[42:43]
	global_store_dwordx4 v[122:123], v[92:95], off sc1
	s_cbranch_vccnz .LBB0_531
	s_nop 0
	v_mul_f32_e32 v95, v103, v114
	v_mul_f32_e32 v94, v104, v115
	v_mul_f32_e32 v114, v95, v95
	v_fmac_f32_e32 v114, v94, v94
	v_mul_f32_e32 v113, v110, v113
	v_fmac_f32_e32 v114, v113, v113
	v_mul_f32_e32 v0, v109, v0
	v_pk_mul_f32 v[58:59], v[72:73], v[58:59]
	v_fmac_f32_e32 v114, v0, v0
	v_pk_mul_f32 v[92:93], v[58:59], v[58:59]
	v_pk_mul_f32 v[60:61], v[78:79], v[60:61]
	v_add_f32_e32 v92, v92, v114
	v_add_f32_e32 v114, v93, v92
	v_pk_mul_f32 v[92:93], v[60:61], v[60:61]
	s_nop 0
	v_add_f32_e32 v92, v92, v114
	v_and_b32_e32 v114, 64, v226
	v_add_f32_e32 v92, v93, v92
	v_xor_b32_e32 v93, 1, v226
	v_add_u32_e32 v114, 64, v114
	v_cmp_lt_i32_e32 vcc, v93, v114
	s_nop 1
	v_cndmask_b32_e32 v93, v226, v93, vcc
	v_lshlrev_b32_e32 v93, 2, v93
	v_mov_b32_dpp v93, v92 quad_perm:[1,0,3,2] row_mask:0xf bank_mask:0xf
	s_waitcnt lgkmcnt(0)
	v_add_f32_e32 v92, v92, v93
	v_xor_b32_e32 v93, 2, v226
	v_cmp_lt_i32_e32 vcc, v93, v114
	s_nop 1
	v_cndmask_b32_e32 v93, v226, v93, vcc
	v_lshlrev_b32_e32 v93, 2, v93
	v_mov_b32_dpp v93, v92 quad_perm:[2,3,0,1] row_mask:0xf bank_mask:0xf
	v_add_f32_e32 v92, v92, v93
	v_xor_b32_e32 v93, 4, v226
	v_cmp_lt_i32_e32 vcc, v93, v114
	s_nop 1
	v_cndmask_b32_e32 v93, v226, v93, vcc
	v_lshlrev_b32_e32 v93, 2, v93
	v_mov_b32_dpp v93, v92 row_half_mirror row_mask:0xf bank_mask:0xf
	v_add_f32_e32 v92, v92, v93
	v_mul_f32_e32 v93, 0x4f800000, v92
	v_cmp_gt_f32_e32 vcc, s82, v92
	s_nop 1
	v_cndmask_b32_e32 v92, v92, v93, vcc
	v_sqrt_f32_e32 v93, v92
	s_nop 0
	v_add_u32_e32 v114, -1, v93
	v_fma_f32 v115, -v114, v93, v92
	v_cmp_ge_f32_e64 s[46:47], 0, v115
	v_add_u32_e32 v115, 1, v93
	s_nop 0
	v_cndmask_b32_e64 v114, v93, v114, s[46:47]
	v_fma_f32 v93, -v115, v93, v92
	v_cmp_lt_f32_e64 s[46:47], 0, v93
	s_nop 1
	v_cndmask_b32_e64 v93, v114, v115, s[46:47]
	v_mul_f32_e32 v114, 0x37800000, v93
	v_cndmask_b32_e32 v93, v93, v114, vcc
	v_cmp_class_f32_e32 vcc, v92, v229
	s_nop 1
	v_cndmask_b32_e32 v92, v93, v92, vcc
	v_max_f32_e32 v92, 0x2b8cbccc, v92
	v_div_scale_f32 v93, s[4:5], v92, v92, 1.0
	v_rcp_f32_e32 v114, v93
	s_nop 0
	v_fma_f32 v115, -v93, v114, 1.0
	v_fmac_f32_e32 v114, v115, v114
	v_div_scale_f32 v115, vcc, 1.0, v92, 1.0
	v_mul_f32_e32 v122, v115, v114
	v_fma_f32 v123, -v93, v122, v115
	v_fmac_f32_e32 v122, v123, v114
	v_fma_f32 v93, -v93, v122, v115
	v_div_fmas_f32 v93, v93, v114, v122
	v_div_fixup_f32 v92, v93, v92, 1.0
	v_mul_f32_e32 v93, v94, v92
	v_mul_f32_e32 v94, v95, v92
	v_mul_f32_e32 v95, v113, v92
	v_mul_f32_e32 v0, v0, v92
	v_mul_f32_e32 v113, v58, v92
	v_mul_f32_e32 v114, v59, v92
	v_mul_f32_e32 v115, v60, v92
	v_mul_f32_e32 v61, v61, v92
	v_cvt_pk_bf16_f32 v58, v93, v94
	v_lshl_add_u64 v[92:93], s[50:51], 0, v[84:85]
	v_add_co_u32_e32 v92, vcc, 0x2e203000, v92
	v_cvt_pk_bf16_f32 v59, v95, v0
	v_cvt_pk_bf16_f32 v60, v113, v114
	v_cvt_pk_bf16_f32 v61, v115, v61
	s_nop 1
	v_addc_co_u32_e32 v93, vcc, 0, v93, vcc
	global_store_dwordx4 v[92:93], v[58:61], off offset:2048 sc1

.LBB0_565:
	s_and_b64 vcc, exec, s[4:5]
	s_cbranch_vccz .LBB0_568
	v_add_co_u32_e32 v88, vcc, 0x2e204000, v62
	v_cvt_pk_bf16_f32 v116, v94, v113
	v_cvt_pk_bf16_f32 v117, v114, v115
	v_cvt_pk_bf16_f32 v118, v54, v55
	v_cvt_pk_bf16_f32 v119, v56, v57
	s_nop 1
	v_addc_co_u32_e32 v89, vcc, 0, v63, vcc
	s_and_b64 vcc, exec, s[42:43]
	global_store_dwordx4 v[88:89], v[116:119], off sc1
	s_cbranch_vccnz .LBB0_568
	v_mul_f32_e32 v96, v103, v113
	v_mul_f32_e32 v94, v104, v94
	v_mul_f32_e32 v97, v96, v96
	v_fmac_f32_e32 v97, v94, v94
	v_mul_f32_e32 v113, v110, v114
	v_fmac_f32_e32 v97, v113, v113
	v_mul_f32_e32 v114, v109, v115
	v_pk_mul_f32 v[54:55], v[72:73], v[54:55]
	v_fmac_f32_e32 v97, v114, v114
	v_pk_mul_f32 v[88:89], v[54:55], v[54:55]
	v_pk_mul_f32 v[56:57], v[78:79], v[56:57]
	v_add_f32_e32 v88, v88, v97
	v_add_f32_e32 v97, v89, v88
	v_pk_mul_f32 v[88:89], v[56:57], v[56:57]
	s_nop 0
	v_add_f32_e32 v88, v88, v97
	v_and_b32_e32 v97, 64, v226
	v_add_f32_e32 v88, v89, v88
	v_xor_b32_e32 v89, 1, v226
	v_add_u32_e32 v97, 64, v97
	v_cmp_lt_i32_e32 vcc, v89, v97
	s_nop 1
	v_cndmask_b32_e32 v89, v226, v89, vcc
	v_lshlrev_b32_e32 v89, 2, v89
	v_mov_b32_dpp v89, v88 quad_perm:[1,0,3,2] row_mask:0xf bank_mask:0xf
	s_waitcnt lgkmcnt(0)
	v_add_f32_e32 v88, v88, v89
	v_xor_b32_e32 v89, 2, v226
	v_cmp_lt_i32_e32 vcc, v89, v97
	s_nop 1
	v_cndmask_b32_e32 v89, v226, v89, vcc
	v_lshlrev_b32_e32 v89, 2, v89
	v_mov_b32_dpp v89, v88 quad_perm:[2,3,0,1] row_mask:0xf bank_mask:0xf
	v_add_f32_e32 v88, v88, v89
	v_xor_b32_e32 v89, 4, v226
	v_cmp_lt_i32_e32 vcc, v89, v97
	s_nop 1
	v_cndmask_b32_e32 v89, v226, v89, vcc
	v_lshlrev_b32_e32 v89, 2, v89
	v_mov_b32_dpp v89, v88 row_half_mirror row_mask:0xf bank_mask:0xf
	v_add_f32_e32 v88, v88, v89
	v_mul_f32_e32 v89, 0x4f800000, v88
	v_cmp_gt_f32_e32 vcc, s82, v88
	s_nop 1
	v_cndmask_b32_e32 v88, v88, v89, vcc
	v_sqrt_f32_e32 v89, v88
	s_nop 0
	v_add_u32_e32 v97, -1, v89
	v_fma_f32 v115, -v97, v89, v88
	v_cmp_ge_f32_e64 s[46:47], 0, v115
	v_add_u32_e32 v115, 1, v89
	s_nop 0
	v_cndmask_b32_e64 v97, v89, v97, s[46:47]
	v_fma_f32 v89, -v115, v89, v88
	v_cmp_lt_f32_e64 s[46:47], 0, v89
	s_nop 1
	v_cndmask_b32_e64 v89, v97, v115, s[46:47]
	v_mul_f32_e32 v97, 0x37800000, v89
	v_cndmask_b32_e32 v89, v89, v97, vcc
	v_cmp_class_f32_e32 vcc, v88, v229
	s_nop 1
	v_cndmask_b32_e32 v88, v89, v88, vcc
	v_max_f32_e32 v88, 0x2b8cbccc, v88
	v_div_scale_f32 v89, s[4:5], v88, v88, 1.0
	v_rcp_f32_e32 v97, v89
	s_nop 0
	v_fma_f32 v115, -v89, v97, 1.0
	v_fmac_f32_e32 v97, v115, v97
	v_div_scale_f32 v115, vcc, 1.0, v88, 1.0
	v_mul_f32_e32 v116, v115, v97
	v_fma_f32 v117, -v89, v116, v115
	v_fmac_f32_e32 v116, v117, v97
	v_fma_f32 v89, -v89, v116, v115
	v_div_fmas_f32 v89, v89, v97, v116
	v_div_fixup_f32 v88, v89, v88, 1.0
	v_mul_f32_e32 v89, v94, v88
	v_mul_f32_e32 v94, v96, v88
	v_mul_f32_e32 v96, v113, v88
	v_mul_f32_e32 v97, v114, v88
	v_mul_f32_e32 v113, v54, v88
	v_mul_f32_e32 v114, v55, v88
	v_mul_f32_e32 v115, v56, v88
	v_mul_f32_e32 v57, v57, v88
	v_cvt_pk_bf16_f32 v54, v89, v94
	v_lshl_add_u64 v[88:89], s[50:51], 0, v[84:85]
	v_add_co_u32_e32 v88, vcc, 0x2e205000, v88
	v_cvt_pk_bf16_f32 v55, v96, v97
	v_cvt_pk_bf16_f32 v56, v113, v114
	v_cvt_pk_bf16_f32 v57, v115, v57
	s_nop 1
	v_addc_co_u32_e32 v89, vcc, 0, v89, vcc
	global_store_dwordx4 v[88:89], v[54:57], off offset:2048 sc1

.LBB0_602:
	s_and_b64 vcc, exec, s[4:5]
	s_cbranch_vccz .LBB0_605
	v_add_co_u32_e32 v64, vcc, 0x2e206000, v62
	v_cvt_pk_bf16_f32 v114, v97, v113
	v_cvt_pk_bf16_f32 v115, v99, v98
	v_cvt_pk_bf16_f32 v116, v50, v51
	v_cvt_pk_bf16_f32 v117, v52, v53
	s_nop 1
	v_addc_co_u32_e32 v65, vcc, 0, v63, vcc
	s_and_b64 vcc, exec, s[42:43]
	global_store_dwordx4 v[64:65], v[114:117], off sc1
	s_cbranch_vccnz .LBB0_605
	v_mul_f32_e32 v91, v103, v113
	v_mul_f32_e32 v90, v104, v97
	v_mul_f32_e32 v97, v91, v91
	v_fmac_f32_e32 v97, v90, v90
	v_mul_f32_e32 v99, v110, v99
	v_fmac_f32_e32 v97, v99, v99
	v_mul_f32_e32 v98, v109, v98
	v_pk_mul_f32 v[50:51], v[72:73], v[50:51]
	v_fmac_f32_e32 v97, v98, v98
	v_pk_mul_f32 v[64:65], v[50:51], v[50:51]
	v_pk_mul_f32 v[52:53], v[78:79], v[52:53]
	v_add_f32_e32 v64, v64, v97
	v_add_f32_e32 v97, v65, v64
	v_pk_mul_f32 v[64:65], v[52:53], v[52:53]
	s_nop 0
	v_add_f32_e32 v64, v64, v97
	v_and_b32_e32 v97, 64, v226
	v_add_f32_e32 v64, v65, v64
	v_xor_b32_e32 v65, 1, v226
	v_add_u32_e32 v97, 64, v97
	v_cmp_lt_i32_e32 vcc, v65, v97
	s_nop 1
	v_cndmask_b32_e32 v65, v226, v65, vcc
	v_lshlrev_b32_e32 v65, 2, v65
	v_mov_b32_dpp v65, v64 quad_perm:[1,0,3,2] row_mask:0xf bank_mask:0xf
	s_waitcnt lgkmcnt(0)
	v_add_f32_e32 v64, v64, v65
	v_xor_b32_e32 v65, 2, v226
	v_cmp_lt_i32_e32 vcc, v65, v97
	s_nop 1
	v_cndmask_b32_e32 v65, v226, v65, vcc
	v_lshlrev_b32_e32 v65, 2, v65
	v_mov_b32_dpp v65, v64 quad_perm:[2,3,0,1] row_mask:0xf bank_mask:0xf
	v_add_f32_e32 v64, v64, v65
	v_xor_b32_e32 v65, 4, v226
	v_cmp_lt_i32_e32 vcc, v65, v97
	s_nop 1
	v_cndmask_b32_e32 v65, v226, v65, vcc
	v_lshlrev_b32_e32 v65, 2, v65
	v_mov_b32_dpp v65, v64 row_half_mirror row_mask:0xf bank_mask:0xf
	v_add_f32_e32 v64, v64, v65
	v_mul_f32_e32 v65, 0x4f800000, v64
	v_cmp_gt_f32_e32 vcc, s82, v64
	s_nop 1
	v_cndmask_b32_e32 v64, v64, v65, vcc
	v_sqrt_f32_e32 v65, v64
	s_nop 0
	v_add_u32_e32 v97, -1, v65
	v_fma_f32 v113, -v97, v65, v64
	v_cmp_ge_f32_e64 s[46:47], 0, v113
	v_add_u32_e32 v113, 1, v65
	s_nop 0
	v_cndmask_b32_e64 v97, v65, v97, s[46:47]
	v_fma_f32 v65, -v113, v65, v64
	v_cmp_lt_f32_e64 s[46:47], 0, v65
	s_nop 1
	v_cndmask_b32_e64 v65, v97, v113, s[46:47]
	v_mul_f32_e32 v97, 0x37800000, v65
	v_cndmask_b32_e32 v65, v65, v97, vcc
	v_cmp_class_f32_e32 vcc, v64, v229
	s_nop 1
	v_cndmask_b32_e32 v64, v65, v64, vcc
	v_max_f32_e32 v64, 0x2b8cbccc, v64
	v_div_scale_f32 v65, s[4:5], v64, v64, 1.0
	v_rcp_f32_e32 v97, v65
	s_nop 0
	v_fma_f32 v113, -v65, v97, 1.0
	v_fmac_f32_e32 v97, v113, v97
	v_div_scale_f32 v113, vcc, 1.0, v64, 1.0
	v_mul_f32_e32 v114, v113, v97
	v_fma_f32 v115, -v65, v114, v113
	v_fmac_f32_e32 v114, v115, v97
	v_fma_f32 v65, -v65, v114, v113
	v_div_fmas_f32 v65, v65, v97, v114
	v_div_fixup_f32 v64, v65, v64, 1.0
	v_mul_f32_e32 v65, v90, v64
	v_mul_f32_e32 v90, v91, v64
	v_mul_f32_e32 v91, v99, v64
	v_mul_f32_e32 v97, v98, v64
	v_mul_f32_e32 v98, v50, v64
	v_mul_f32_e32 v99, v51, v64
	v_mul_f32_e32 v113, v52, v64
	v_mul_f32_e32 v53, v53, v64
	v_cvt_pk_bf16_f32 v50, v65, v90
	v_lshl_add_u64 v[64:65], s[50:51], 0, v[84:85]
	v_add_co_u32_e32 v64, vcc, 0x2e207000, v64
	v_cvt_pk_bf16_f32 v51, v91, v97
	v_cvt_pk_bf16_f32 v52, v98, v99
	v_cvt_pk_bf16_f32 v53, v113, v53
	s_nop 1
	v_addc_co_u32_e32 v65, vcc, 0, v65, vcc
	global_store_dwordx4 v[64:65], v[50:53], off offset:2048 sc1

.LBB0_639:
	s_and_b64 vcc, exec, s[4:5]
	s_cbranch_vccz .LBB0_642
	v_add_co_u32_e32 v98, vcc, 0x2e208000, v62
	v_cvt_pk_bf16_f32 v58, v95, v93
	v_cvt_pk_bf16_f32 v59, v92, v0
	v_cvt_pk_bf16_f32 v60, v46, v47
	v_cvt_pk_bf16_f32 v61, v48, v49
	s_nop 1
	v_addc_co_u32_e32 v99, vcc, 0, v63, vcc
	s_and_b64 vcc, exec, s[42:43]
	global_store_dwordx4 v[98:99], v[58:61], off sc1
	s_cbranch_vccnz .LBB0_642
	s_nop 0
	v_mul_f32_e32 v61, v103, v93
	v_mul_f32_e32 v60, v104, v95
	v_mul_f32_e32 v93, v61, v61
	v_fmac_f32_e32 v93, v60, v60
	v_mul_f32_e32 v92, v110, v92
	v_fmac_f32_e32 v93, v92, v92
	v_mul_f32_e32 v0, v109, v0
	v_pk_mul_f32 v[46:47], v[72:73], v[46:47]
	v_fmac_f32_e32 v93, v0, v0
	v_pk_mul_f32 v[58:59], v[46:47], v[46:47]
	v_pk_mul_f32 v[48:49], v[78:79], v[48:49]
	v_add_f32_e32 v58, v58, v93
	v_add_f32_e32 v93, v59, v58
	v_pk_mul_f32 v[58:59], v[48:49], v[48:49]
	s_nop 0
	v_add_f32_e32 v58, v58, v93
	v_and_b32_e32 v93, 64, v226
	v_add_f32_e32 v58, v59, v58
	v_xor_b32_e32 v59, 1, v226
	v_add_u32_e32 v93, 64, v93
	v_cmp_lt_i32_e32 vcc, v59, v93
	s_nop 1
	v_cndmask_b32_e32 v59, v226, v59, vcc
	v_lshlrev_b32_e32 v59, 2, v59
	v_mov_b32_dpp v59, v58 quad_perm:[1,0,3,2] row_mask:0xf bank_mask:0xf
	s_waitcnt lgkmcnt(0)
	v_add_f32_e32 v58, v58, v59
	v_xor_b32_e32 v59, 2, v226
	v_cmp_lt_i32_e32 vcc, v59, v93
	s_nop 1
	v_cndmask_b32_e32 v59, v226, v59, vcc
	v_lshlrev_b32_e32 v59, 2, v59
	v_mov_b32_dpp v59, v58 quad_perm:[2,3,0,1] row_mask:0xf bank_mask:0xf
	v_add_f32_e32 v58, v58, v59
	v_xor_b32_e32 v59, 4, v226
	v_cmp_lt_i32_e32 vcc, v59, v93
	s_nop 1
	v_cndmask_b32_e32 v59, v226, v59, vcc
	v_lshlrev_b32_e32 v59, 2, v59
	v_mov_b32_dpp v59, v58 row_half_mirror row_mask:0xf bank_mask:0xf
	v_add_f32_e32 v58, v58, v59
	v_mul_f32_e32 v59, 0x4f800000, v58
	v_cmp_gt_f32_e32 vcc, s82, v58
	s_nop 1
	v_cndmask_b32_e32 v58, v58, v59, vcc
	v_sqrt_f32_e32 v59, v58
	s_nop 0
	v_add_u32_e32 v93, -1, v59
	v_fma_f32 v95, -v93, v59, v58
	v_cmp_ge_f32_e64 s[46:47], 0, v95
	v_add_u32_e32 v95, 1, v59
	s_nop 0
	v_cndmask_b32_e64 v93, v59, v93, s[46:47]
	v_fma_f32 v59, -v95, v59, v58
	v_cmp_lt_f32_e64 s[46:47], 0, v59
	s_nop 1
	v_cndmask_b32_e64 v59, v93, v95, s[46:47]
	v_mul_f32_e32 v93, 0x37800000, v59
	v_cndmask_b32_e32 v59, v59, v93, vcc
	v_cmp_class_f32_e32 vcc, v58, v229
	s_nop 1
	v_cndmask_b32_e32 v58, v59, v58, vcc
	v_max_f32_e32 v58, 0x2b8cbccc, v58
	v_div_scale_f32 v59, s[4:5], v58, v58, 1.0
	v_rcp_f32_e32 v93, v59
	s_nop 0
	v_fma_f32 v95, -v59, v93, 1.0
	v_fmac_f32_e32 v93, v95, v93
	v_div_scale_f32 v95, vcc, 1.0, v58, 1.0
	v_mul_f32_e32 v97, v95, v93
	v_fma_f32 v98, -v59, v97, v95
	v_fmac_f32_e32 v97, v98, v93
	v_fma_f32 v59, -v59, v97, v95
	v_div_fmas_f32 v59, v59, v93, v97
	v_div_fixup_f32 v58, v59, v58, 1.0
	v_mul_f32_e32 v59, v60, v58
	v_mul_f32_e32 v60, v61, v58
	v_mul_f32_e32 v61, v92, v58
	v_mul_f32_e32 v0, v0, v58
	v_mul_f32_e32 v92, v46, v58
	v_mul_f32_e32 v93, v47, v58
	v_mul_f32_e32 v95, v48, v58
	v_mul_f32_e32 v49, v49, v58
	v_cvt_pk_bf16_f32 v46, v59, v60
	v_lshl_add_u64 v[58:59], s[50:51], 0, v[84:85]
	v_add_co_u32_e32 v58, vcc, 0x2e209000, v58
	v_cvt_pk_bf16_f32 v47, v61, v0
	v_cvt_pk_bf16_f32 v48, v92, v93
	v_cvt_pk_bf16_f32 v49, v95, v49
	s_nop 1
	v_addc_co_u32_e32 v59, vcc, 0, v59, vcc
	global_store_dwordx4 v[58:59], v[46:49], off offset:2048 sc1

.LBB0_676:
	s_and_b64 vcc, exec, s[4:5]
	s_cbranch_vccz .LBB0_679
	v_add_co_u32_e32 v94, vcc, 0x2e20a000, v62
	v_cvt_pk_bf16_f32 v54, v0, v92
	v_cvt_pk_bf16_f32 v55, v89, v88
	v_cvt_pk_bf16_f32 v56, v48, v49
	v_cvt_pk_bf16_f32 v57, v44, v45
	s_nop 1
	v_addc_co_u32_e32 v95, vcc, 0, v63, vcc
	s_and_b64 vcc, exec, s[42:43]
	global_store_dwordx4 v[94:95], v[54:57], off sc1
	s_cbranch_vccnz .LBB0_679
	s_nop 0
	v_mul_f32_e32 v56, v103, v92
	v_mul_f32_e32 v0, v104, v0
	v_mul_f32_e32 v57, v56, v56
	v_fmac_f32_e32 v57, v0, v0
	v_mul_f32_e32 v89, v110, v89
	v_fmac_f32_e32 v57, v89, v89
	v_mul_f32_e32 v88, v109, v88
	v_pk_mul_f32 v[48:49], v[72:73], v[48:49]
	v_fmac_f32_e32 v57, v88, v88
	v_pk_mul_f32 v[54:55], v[48:49], v[48:49]
	v_pk_mul_f32 v[44:45], v[78:79], v[44:45]
	v_add_f32_e32 v54, v54, v57
	v_add_f32_e32 v57, v55, v54
	v_pk_mul_f32 v[54:55], v[44:45], v[44:45]
	s_nop 0
	v_add_f32_e32 v54, v54, v57
	v_and_b32_e32 v57, 64, v226
	v_add_f32_e32 v54, v55, v54
	v_xor_b32_e32 v55, 1, v226
	v_add_u32_e32 v57, 64, v57
	v_cmp_lt_i32_e32 vcc, v55, v57
	s_nop 1
	v_cndmask_b32_e32 v55, v226, v55, vcc
	v_lshlrev_b32_e32 v55, 2, v55
	v_mov_b32_dpp v55, v54 quad_perm:[1,0,3,2] row_mask:0xf bank_mask:0xf
	s_waitcnt lgkmcnt(0)
	v_add_f32_e32 v54, v54, v55
	v_xor_b32_e32 v55, 2, v226
	v_cmp_lt_i32_e32 vcc, v55, v57
	s_nop 1
	v_cndmask_b32_e32 v55, v226, v55, vcc
	v_lshlrev_b32_e32 v55, 2, v55
	v_mov_b32_dpp v55, v54 quad_perm:[2,3,0,1] row_mask:0xf bank_mask:0xf
	v_add_f32_e32 v54, v54, v55
	v_xor_b32_e32 v55, 4, v226
	v_cmp_lt_i32_e32 vcc, v55, v57
	s_nop 1
	v_cndmask_b32_e32 v55, v226, v55, vcc
	v_lshlrev_b32_e32 v55, 2, v55
	v_mov_b32_dpp v55, v54 row_half_mirror row_mask:0xf bank_mask:0xf
	v_add_f32_e32 v54, v54, v55
	v_mul_f32_e32 v55, 0x4f800000, v54
	v_cmp_gt_f32_e32 vcc, s82, v54
	s_nop 1
	v_cndmask_b32_e32 v54, v54, v55, vcc
	v_sqrt_f32_e32 v55, v54
	s_nop 0
	v_add_u32_e32 v57, -1, v55
	v_fma_f32 v92, -v57, v55, v54
	v_cmp_ge_f32_e64 s[46:47], 0, v92
	v_add_u32_e32 v92, 1, v55
	s_nop 0
	v_cndmask_b32_e64 v57, v55, v57, s[46:47]
	v_fma_f32 v55, -v92, v55, v54
	v_cmp_lt_f32_e64 s[46:47], 0, v55
	s_nop 1
	v_cndmask_b32_e64 v55, v57, v92, s[46:47]
	v_mul_f32_e32 v57, 0x37800000, v55
	v_cndmask_b32_e32 v55, v55, v57, vcc
	v_cmp_class_f32_e32 vcc, v54, v229
	s_nop 1
	v_cndmask_b32_e32 v54, v55, v54, vcc
	v_max_f32_e32 v54, 0x2b8cbccc, v54
	v_div_scale_f32 v55, s[4:5], v54, v54, 1.0
	v_rcp_f32_e32 v57, v55
	s_nop 0
	v_fma_f32 v92, -v55, v57, 1.0
	v_fmac_f32_e32 v57, v92, v57
	v_div_scale_f32 v92, vcc, 1.0, v54, 1.0
	v_mul_f32_e32 v93, v92, v57
	v_fma_f32 v94, -v55, v93, v92
	v_fmac_f32_e32 v93, v94, v57
	v_fma_f32 v55, -v55, v93, v92
	v_div_fmas_f32 v55, v55, v57, v93
	v_div_fixup_f32 v54, v55, v54, 1.0
	v_mul_f32_e32 v55, v56, v54
	v_mul_f32_e32 v56, v89, v54
	v_mul_f32_e32 v57, v88, v54
	v_mul_f32_e32 v44, v44, v54
	v_mul_f32_e32 v45, v45, v54
	v_mul_f32_e32 v0, v0, v54
	v_mul_f32_e32 v48, v48, v54
	v_mul_f32_e32 v49, v49, v54
	v_cvt_pk_bf16_f32 v54, v0, v55
	v_cvt_pk_bf16_f32 v55, v56, v57
	v_cvt_pk_bf16_f32 v56, v48, v49
	v_cvt_pk_bf16_f32 v57, v44, v45
	v_lshl_add_u64 v[44:45], s[50:51], 0, v[84:85]
	v_add_co_u32_e32 v44, vcc, 0x2e20b000, v44
	s_nop 1
	v_addc_co_u32_e32 v45, vcc, 0, v45, vcc
	global_store_dwordx4 v[44:45], v[54:57], off offset:2048 sc1

.LBB0_713:
	s_and_b64 vcc, exec, s[4:5]
	s_cbranch_vccz .LBB0_716
	v_add_co_u32_e32 v54, vcc, 0x2e20c000, v62
	v_cvt_pk_bf16_f32 v50, v0, v44
	v_cvt_pk_bf16_f32 v51, v45, v48
	v_cvt_pk_bf16_f32 v52, v38, v39
	v_cvt_pk_bf16_f32 v53, v40, v41
	s_nop 1
	v_addc_co_u32_e32 v55, vcc, 0, v63, vcc
	s_and_b64 vcc, exec, s[42:43]
	global_store_dwordx4 v[54:55], v[50:53], off sc1
	s_cbranch_vccnz .LBB0_716
	v_mul_f32_e32 v49, v103, v44
	v_mul_f32_e32 v0, v104, v0
	v_mul_f32_e32 v50, v49, v49
	v_fmac_f32_e32 v50, v0, v0
	v_mul_f32_e32 v51, v110, v45
	v_fmac_f32_e32 v50, v51, v51
	v_mul_f32_e32 v48, v109, v48
	v_pk_mul_f32 v[38:39], v[72:73], v[38:39]
	v_fmac_f32_e32 v50, v48, v48
	v_pk_mul_f32 v[44:45], v[38:39], v[38:39]
	v_pk_mul_f32 v[40:41], v[78:79], v[40:41]
	v_add_f32_e32 v44, v44, v50
	v_add_f32_e32 v50, v45, v44
	v_pk_mul_f32 v[44:45], v[40:41], v[40:41]
	s_nop 0
	v_add_f32_e32 v44, v44, v50
	v_and_b32_e32 v50, 64, v226
	v_add_f32_e32 v44, v45, v44
	v_xor_b32_e32 v45, 1, v226
	v_add_u32_e32 v50, 64, v50
	v_cmp_lt_i32_e32 vcc, v45, v50
	s_nop 1
	v_cndmask_b32_e32 v45, v226, v45, vcc
	v_lshlrev_b32_e32 v45, 2, v45
	v_mov_b32_dpp v45, v44 quad_perm:[1,0,3,2] row_mask:0xf bank_mask:0xf
	s_waitcnt lgkmcnt(0)
	v_add_f32_e32 v44, v44, v45
	v_xor_b32_e32 v45, 2, v226
	v_cmp_lt_i32_e32 vcc, v45, v50
	s_nop 1
	v_cndmask_b32_e32 v45, v226, v45, vcc
	v_lshlrev_b32_e32 v45, 2, v45
	v_mov_b32_dpp v45, v44 quad_perm:[2,3,0,1] row_mask:0xf bank_mask:0xf
	v_add_f32_e32 v44, v44, v45
	v_xor_b32_e32 v45, 4, v226
	v_cmp_lt_i32_e32 vcc, v45, v50
	s_nop 1
	v_cndmask_b32_e32 v45, v226, v45, vcc
	v_lshlrev_b32_e32 v45, 2, v45
	v_mov_b32_dpp v45, v44 row_half_mirror row_mask:0xf bank_mask:0xf
	v_add_f32_e32 v44, v44, v45
	v_mul_f32_e32 v45, 0x4f800000, v44
	v_cmp_gt_f32_e32 vcc, s82, v44
	s_nop 1
	v_cndmask_b32_e32 v44, v44, v45, vcc
	v_sqrt_f32_e32 v45, v44
	s_nop 0
	v_add_u32_e32 v50, -1, v45
	v_fma_f32 v52, -v50, v45, v44
	v_cmp_ge_f32_e64 s[46:47], 0, v52
	v_add_u32_e32 v52, 1, v45
	s_nop 0
	v_cndmask_b32_e64 v50, v45, v50, s[46:47]
	v_fma_f32 v45, -v52, v45, v44
	v_cmp_lt_f32_e64 s[46:47], 0, v45
	s_nop 1
	v_cndmask_b32_e64 v45, v50, v52, s[46:47]
	v_mul_f32_e32 v50, 0x37800000, v45
	v_cndmask_b32_e32 v45, v45, v50, vcc
	v_cmp_class_f32_e32 vcc, v44, v229
	s_nop 1
	v_cndmask_b32_e32 v44, v45, v44, vcc
	v_max_f32_e32 v44, 0x2b8cbccc, v44
	v_div_scale_f32 v45, s[4:5], v44, v44, 1.0
	v_rcp_f32_e32 v50, v45
	s_nop 0
	v_fma_f32 v52, -v45, v50, 1.0
	v_fmac_f32_e32 v50, v52, v50
	v_div_scale_f32 v52, vcc, 1.0, v44, 1.0
	v_mul_f32_e32 v53, v52, v50
	v_fma_f32 v54, -v45, v53, v52
	v_fmac_f32_e32 v53, v54, v50
	v_fma_f32 v45, -v45, v53, v52
	v_div_fmas_f32 v45, v45, v50, v53
	v_div_fixup_f32 v44, v45, v44, 1.0
	v_mul_f32_e32 v45, v49, v44
	v_mul_f32_e32 v0, v0, v44
	v_mul_f32_e32 v49, v51, v44
	v_mul_f32_e32 v48, v48, v44
	v_mul_f32_e32 v50, v38, v44
	v_mul_f32_e32 v51, v39, v44
	v_mul_f32_e32 v52, v40, v44
	v_mul_f32_e32 v41, v41, v44
	v_cvt_pk_bf16_f32 v38, v0, v45
	v_lshl_add_u64 v[44:45], s[50:51], 0, v[84:85]
	v_add_co_u32_e32 v44, vcc, 0x2e20d000, v44
	v_cvt_pk_bf16_f32 v39, v49, v48
	v_cvt_pk_bf16_f32 v40, v50, v51
	v_cvt_pk_bf16_f32 v41, v52, v41
	s_nop 1
	v_addc_co_u32_e32 v45, vcc, 0, v45, vcc
	global_store_dwordx4 v[44:45], v[38:41], off offset:2048 sc1

.LBB0_750:
	s_and_b64 vcc, exec, s[4:5]
	s_cbranch_vccz .LBB0_454
	v_add_co_u32_e32 v46, vcc, 0x2e20e000, v62
	v_cvt_pk_bf16_f32 v42, v38, v39
	v_cvt_pk_bf16_f32 v43, v40, v41
	v_cvt_pk_bf16_f32 v44, v34, v35
	v_cvt_pk_bf16_f32 v45, v36, v37
	s_nop 1
	v_addc_co_u32_e32 v47, vcc, 0, v63, vcc
	s_and_b64 vcc, exec, s[42:43]
	global_store_dwordx4 v[46:47], v[42:45], off sc1
	s_cbranch_vccnz .LBB0_454
	s_nop 0
	v_mul_f32_e32 v43, v103, v39
	v_mul_f32_e32 v42, v104, v38
	v_mul_f32_e32 v44, v43, v43
	v_fmac_f32_e32 v44, v42, v42
	v_mul_f32_e32 v40, v110, v40
	v_fmac_f32_e32 v44, v40, v40
	v_mul_f32_e32 v41, v109, v41
	v_pk_mul_f32 v[34:35], v[72:73], v[34:35]
	v_fmac_f32_e32 v44, v41, v41
	v_pk_mul_f32 v[38:39], v[34:35], v[34:35]
	v_pk_mul_f32 v[36:37], v[78:79], v[36:37]
	v_add_f32_e32 v38, v38, v44
	v_add_f32_e32 v44, v39, v38
	v_pk_mul_f32 v[38:39], v[36:37], v[36:37]
	s_nop 0
	v_add_f32_e32 v38, v38, v44
	v_and_b32_e32 v44, 64, v226
	v_add_f32_e32 v38, v39, v38
	v_xor_b32_e32 v39, 1, v226
	v_add_u32_e32 v44, 64, v44
	v_cmp_lt_i32_e32 vcc, v39, v44
	s_nop 1
	v_cndmask_b32_e32 v39, v226, v39, vcc
	v_lshlrev_b32_e32 v39, 2, v39
	v_mov_b32_dpp v39, v38 quad_perm:[1,0,3,2] row_mask:0xf bank_mask:0xf
	s_waitcnt lgkmcnt(0)
	v_add_f32_e32 v38, v38, v39
	v_xor_b32_e32 v39, 2, v226
	v_cmp_lt_i32_e32 vcc, v39, v44
	s_nop 1
	v_cndmask_b32_e32 v39, v226, v39, vcc
	v_lshlrev_b32_e32 v39, 2, v39
	v_mov_b32_dpp v39, v38 quad_perm:[2,3,0,1] row_mask:0xf bank_mask:0xf
	v_add_f32_e32 v38, v38, v39
	v_xor_b32_e32 v39, 4, v226
	v_cmp_lt_i32_e32 vcc, v39, v44
	s_nop 1
	v_cndmask_b32_e32 v39, v226, v39, vcc
	v_lshlrev_b32_e32 v39, 2, v39
	v_mov_b32_dpp v39, v38 row_half_mirror row_mask:0xf bank_mask:0xf
	v_add_f32_e32 v38, v38, v39
	v_mul_f32_e32 v39, 0x4f800000, v38
	v_cmp_gt_f32_e32 vcc, s82, v38
	s_nop 1
	v_cndmask_b32_e32 v38, v38, v39, vcc
	v_sqrt_f32_e32 v39, v38
	s_nop 0
	v_add_u32_e32 v44, -1, v39
	v_fma_f32 v45, -v44, v39, v38
	v_cmp_ge_f32_e64 s[42:43], 0, v45
	v_add_u32_e32 v45, 1, v39
	s_nop 0
	v_cndmask_b32_e64 v44, v39, v44, s[42:43]
	v_fma_f32 v39, -v45, v39, v38
	v_cmp_lt_f32_e64 s[42:43], 0, v39
	s_nop 1
	v_cndmask_b32_e64 v39, v44, v45, s[42:43]
	v_mul_f32_e32 v44, 0x37800000, v39
	v_cndmask_b32_e32 v39, v39, v44, vcc
	v_cmp_class_f32_e32 vcc, v38, v229
	s_nop 1
	v_cndmask_b32_e32 v38, v39, v38, vcc
	v_max_f32_e32 v38, 0x2b8cbccc, v38
	v_div_scale_f32 v39, s[4:5], v38, v38, 1.0
	v_rcp_f32_e32 v44, v39
	s_nop 0
	v_fma_f32 v45, -v39, v44, 1.0
	v_fmac_f32_e32 v44, v45, v44
	v_div_scale_f32 v45, vcc, 1.0, v38, 1.0
	v_mul_f32_e32 v46, v45, v44
	v_fma_f32 v47, -v39, v46, v45
	v_fmac_f32_e32 v46, v47, v44
	v_fma_f32 v39, -v39, v46, v45
	v_div_fmas_f32 v39, v39, v44, v46
	v_div_fixup_f32 v38, v39, v38, 1.0
	v_mul_f32_e32 v39, v42, v38
	v_mul_f32_e32 v42, v43, v38
	v_mul_f32_e32 v40, v40, v38
	v_mul_f32_e32 v41, v41, v38
	v_mul_f32_e32 v43, v34, v38
	v_mul_f32_e32 v44, v35, v38
	v_mul_f32_e32 v45, v36, v38
	v_mul_f32_e32 v37, v37, v38
	v_cvt_pk_bf16_f32 v34, v39, v42
	v_lshl_add_u64 v[38:39], s[50:51], 0, v[84:85]
	v_add_co_u32_e32 v38, vcc, 0x2e20f000, v38
	v_cvt_pk_bf16_f32 v35, v40, v41
	v_cvt_pk_bf16_f32 v36, v43, v44
	v_cvt_pk_bf16_f32 v37, v45, v37
	s_nop 1
	v_addc_co_u32_e32 v39, vcc, 0, v39, vcc
	global_store_dwordx4 v[38:39], v[34:37], off offset:2048 sc1
	s_branch .LBB0_454

.LBB0_1141:
	s_waitcnt lgkmcnt(0)
	v_lshl_add_u64 v[50:51], s[40:41], 0, v[80:81]
	s_mov_b64 s[4:5], 0x40e00000
	v_lshl_add_u64 v[46:47], v[50:51], 0, s[4:5]
	v_add_co_u32_e32 v48, vcc, 0x40e00000, v50
	s_mov_b64 s[4:5], 0x42e00000
	s_nop 0
	v_addc_co_u32_e32 v49, vcc, 0, v51, vcc
	v_lshl_add_u64 v[52:53], v[50:51], 0, s[4:5]
	s_mov_b32 s4, 0x42e00000
	v_add_co_u32_e32 v50, vcc, s4, v50
	global_load_dwordx4 v[54:57], v[48:49], off nt
	s_nop 0
	global_load_dwordx4 v[46:49], v[46:47], off offset:16 nt
	v_addc_co_u32_e32 v51, vcc, 0, v51, vcc
	global_load_dwordx4 v[58:61], v[50:51], off nt
	s_nop 0
	global_load_dwordx4 v[50:53], v[52:53], off offset:16 nt
	v_lshl_add_u64 v[108:109], s[40:41], 0, v[76:77]
	s_mov_b64 s[4:5], 0x2e200000
	v_lshl_add_u64 v[156:157], s[40:41], 0, v[74:75]
	s_mov_b64 vcc, 0x2e200800
	v_lshl_add_u64 v[184:185], v[108:109], 0, vcc
	s_mov_b64 vcc, 0x36e01800
	v_lshl_add_u64 v[186:187], v[156:157], 0, vcc
	global_load_dwordx4 v[188:191], v[184:185], off offset:-2048 nt
	global_load_dwordx4 v[192:195], v[184:185], off offset:-2032 nt
	global_load_dwordx4 v[196:199], v[184:185], off nt
	global_load_dwordx4 v[200:203], v[184:185], off offset:16 nt
	global_load_dwordx4 v[204:207], v[184:185], off offset:2048 nt
	global_load_dwordx4 v[208:211], v[184:185], off offset:2064 nt
	global_load_dwordx4 v[212:215], v[186:187], off offset:-2048 nt
	global_load_dwordx4 v[216:219], v[186:187], off offset:-2032 nt
	global_load_dwordx4 v[220:223], v[186:187], off nt
	global_load_dwordx4 v[234:237], v[186:187], off offset:16 nt
	global_load_dwordx4 v[238:241], v[186:187], off offset:2048 nt
	global_load_dwordx4 v[242:245], v[186:187], off offset:2064 nt
	s_add_i32 s48, s48, s66
	v_lshl_add_u64 v[74:75], v[74:75], 0, s[6:7]
	v_lshl_add_u64 v[76:77], v[76:77], 0, s[10:11]
	v_lshl_add_u64 v[80:81], v[80:81], 0, s[22:23]
	s_cmpk_lt_i32 s48, 0x4000
	s_waitcnt vmcnt(15)
	v_lshlrev_b32_e32 v2, 16, v54
	v_and_b32_e32 v82, 0xffff0000, v54
	v_lshlrev_b32_e32 v86, 16, v55
	v_and_b32_e32 v127, 0xffff0000, v55
	v_lshl_add_u64 v[54:55], v[108:109], 0, s[4:5]
	s_mov_b32 s4, 0x2e200000
	s_waitcnt vmcnt(13)
	v_lshlrev_b32_e32 v4, 16, v58
	v_and_b32_e32 v72, 0xffff0000, v58
	v_add_co_u32_e32 v58, vcc, s4, v108
	v_lshlrev_b32_e32 v123, 16, v59
	v_and_b32_e32 v125, 0xffff0000, v59
	v_addc_co_u32_e32 v59, vcc, 0, v109, vcc
	s_mov_b32 s4, 0x2e201000
	v_add_co_u32_e32 v110, vcc, s4, v108
	s_mov_b64 s[4:5], 0x2e200800
	v_lshlrev_b32_e32 v131, 16, v60
	v_and_b32_e32 v133, 0xffff0000, v60
	v_lshlrev_b32_e32 v137, 16, v61
	v_and_b32_e32 v136, 0xffff0000, v61
	v_addc_co_u32_e32 v111, vcc, 0, v109, vcc
	v_lshl_add_u64 v[60:61], v[108:109], 0, s[4:5]
	s_mov_b64 s[4:5], 0x2e201000
	v_lshlrev_b32_e32 v135, 16, v57
	v_lshlrev_b32_e32 v129, 16, v56
	v_and_b32_e32 v134, 0xffff0000, v56
	v_and_b32_e32 v164, 0xffff0000, v57
	s_nop 0
	s_nop 0
	s_nop 0
	v_lshl_add_u64 v[112:113], v[108:109], 0, s[4:5]
	s_nop 0
	s_mov_b64 s[4:5], 0x36e01000
	v_lshl_add_u64 v[144:145], v[156:157], 0, s[4:5]
	s_mov_b32 s4, 0x36e01000
	v_add_co_u32_e32 v148, vcc, s4, v156
	s_mov_b32 s4, 0x36e02000
	s_nop 0
	v_addc_co_u32_e32 v149, vcc, 0, v157, vcc
	v_add_co_u32_e32 v158, vcc, s4, v156
	s_mov_b64 s[4:5], 0x36e01800
	s_nop 0
	v_addc_co_u32_e32 v159, vcc, 0, v157, vcc
	v_lshl_add_u64 v[152:153], v[156:157], 0, s[4:5]
	s_mov_b64 s[4:5], 0x36e02000
	v_lshl_add_u64 v[160:161], v[156:157], 0, s[4:5]
	v_add_f32_e32 v82, v72, v82
	v_add_f32_e32 v4, v4, v2
	v_add_f32_e32 v2, 0, v4
	v_add_f32_e32 v2, v82, v2
	v_add_f32_e32 v86, v123, v86
	v_add_f32_e32 v2, v86, v2
	v_add_f32_e32 v123, v125, v127
	v_add_f32_e32 v2, v123, v2
	v_add_f32_e32 v125, v131, v129
	v_add_f32_e32 v2, v125, v2
	s_waitcnt vmcnt(11)
	v_lshlrev_b32_e32 v165, 16, v188
	v_and_b32_e32 v166, 0xffff0000, v188
	s_waitcnt vmcnt(9)
	v_lshlrev_b32_e32 v169, 16, v196
	v_and_b32_e32 v170, 0xffff0000, v196
	s_waitcnt vmcnt(7)
	v_lshlrev_b32_e32 v132, 16, v204
	v_and_b32_e32 v130, 0xffff0000, v204
	v_lshlrev_b32_e32 v124, 16, v206
	v_and_b32_e32 v122, 0xffff0000, v206
	s_waitcnt vmcnt(6)
	v_lshlrev_b32_e32 v118, 16, v208
	v_and_b32_e32 v116, 0xffff0000, v208
	v_lshlrev_b32_e32 v114, 16, v209
	v_and_b32_e32 v112, 0xffff0000, v209
	v_lshlrev_b32_e32 v110, 16, v210
	v_and_b32_e32 v108, 0xffff0000, v210
	v_lshlrev_b32_e32 v66, 16, v211
	v_and_b32_e32 v62, 0xffff0000, v211
	s_nop 0
	s_nop 0
	s_nop 0
	s_nop 0
	s_nop 0
	v_lshlrev_b32_e32 v128, 16, v205
	v_and_b32_e32 v126, 0xffff0000, v205
	v_lshlrev_b32_e32 v84, 16, v207
	v_and_b32_e32 v120, 0xffff0000, v207
	v_lshlrev_b32_e32 v171, 16, v197
	v_lshlrev_b32_e32 v167, 16, v189
	v_and_b32_e32 v168, 0xffff0000, v195
	v_and_b32_e32 v172, 0xffff0000, v203
	s_waitcnt vmcnt(5)
	v_lshlrev_b32_e32 v173, 16, v212
	s_waitcnt vmcnt(3)
	v_lshlrev_b32_e32 v175, 16, v220
	v_and_b32_e32 v140, 0xffff0000, v212
	v_and_b32_e32 v148, 0xffff0000, v220
	s_waitcnt vmcnt(1)
	v_lshlrev_b32_e32 v179, 16, v238
	v_and_b32_e32 v180, 0xffff0000, v238
	v_add_f32_e32 v156, v173, v175
	v_add_f32_e32 v156, -2.0, v156
	v_add_f32_e32 v72, v140, v148
	v_fma_f32 v156, v14, v156, 2.0
	v_add_f32_e32 v72, -2.0, v72
	v_mul_f32_e32 v156, v156, v169
	v_fma_f32 v72, v15, v72, 2.0
	v_lshlrev_b32_e32 v174, 16, v213
	s_waitcnt vmcnt(0)
	v_lshlrev_b32_e32 v115, 16, v242
	v_and_b32_e32 v113, 0xffff0000, v242
	v_lshlrev_b32_e32 v111, 16, v243
	v_and_b32_e32 v109, 0xffff0000, v243
	v_mul_f32_e32 v156, v156, v165
	v_mul_f32_e32 v72, v72, v170
	v_lshlrev_b32_e32 v161, 16, v214
	v_and_b32_e32 v160, 0xffff0000, v213
	v_lshlrev_b32_e32 v141, 16, v222
	v_and_b32_e32 v140, 0xffff0000, v221
	v_lshlrev_b32_e32 v176, 16, v221
	v_lshlrev_b32_e32 v20, 16, v244
	v_and_b32_e32 v17, 0xffff0000, v244
	v_fma_f32 v162, v6, v156, 0
	v_mul_f32_e32 v72, v72, v166
	v_pk_add_f32 v[140:141], v[160:161], v[140:141]
	v_fmac_f32_e32 v162, v7, v72
	v_add_f32_e32 v72, v174, v176
	v_pk_add_f32 v[140:141], v[140:141], -2.0 op_sel_hi:[1,0]
	v_lshlrev_b32_e32 v70, 16, v240
	v_and_b32_e32 v121, 0xffff0000, v240
	v_lshlrev_b32_e32 v119, 16, v241
	v_and_b32_e32 v117, 0xffff0000, v241
	v_add_f32_e32 v72, -2.0, v72
	v_lshlrev_b32_e32 v159, 16, v198
	v_and_b32_e32 v158, 0xffff0000, v197
	v_pk_fma_f32 v[140:141], v[98:99], v[140:141], 2.0 op_sel_hi:[1,1,0]
	v_lshlrev_b32_e32 v181, 16, v239
	v_and_b32_e32 v182, 0xffff0000, v239
	v_fma_f32 v72, v16, v72, 2.0
	v_lshlrev_b32_e32 v157, 16, v190
	v_and_b32_e32 v156, 0xffff0000, v189
	v_pk_mul_f32 v[140:141], v[140:141], v[158:159]
	v_mul_f32_e32 v72, v72, v171
	v_pk_mul_f32 v[140:141], v[140:141], v[156:157]
	v_lshlrev_b32_e32 v157, 16, v215
	v_and_b32_e32 v156, 0xffff0000, v214
	v_lshlrev_b32_e32 v159, 16, v223
	v_and_b32_e32 v158, 0xffff0000, v222
	v_mul_f32_e32 v72, v72, v167
	v_pk_add_f32 v[156:157], v[156:157], v[158:159]
	v_fmac_f32_e32 v162, v8, v72
	v_pk_mul_f32 v[140:141], v[88:89], v[140:141]
	v_pk_add_f32 v[156:157], v[156:157], -2.0 op_sel_hi:[1,0]
	v_add_f32_e32 v63, v140, v162
	v_lshlrev_b32_e32 v149, 16, v199
	v_and_b32_e32 v148, 0xffff0000, v198
	v_pk_fma_f32 v[156:157], v[100:101], v[156:157], 2.0 op_sel_hi:[1,1,0]
	v_add_f32_e32 v63, v141, v63
	v_lshlrev_b32_e32 v141, 16, v191
	v_and_b32_e32 v140, 0xffff0000, v190
	v_pk_mul_f32 v[148:149], v[156:157], v[148:149]
	v_and_b32_e32 v64, 0xffff0000, v199
	v_lshlrev_b32_e32 v69, 16, v216
	v_and_b32_e32 v68, 0xffff0000, v215
	v_lshlrev_b32_e32 v143, 16, v234
	v_and_b32_e32 v142, 0xffff0000, v223
	v_pk_mul_f32 v[140:141], v[148:149], v[140:141]
	v_pk_add_f32 v[68:69], v[68:69], v[142:143]
	v_pk_mul_f32 v[140:141], v[90:91], v[140:141]
	v_pk_add_f32 v[68:69], v[68:69], -2.0 op_sel_hi:[1,0]
	v_add_f32_e32 v63, v140, v63
	v_and_b32_e32 v140, 0xffff0000, v191
	v_lshlrev_b32_e32 v65, 16, v200
	v_pk_fma_f32 v[68:69], v[102:103], v[68:69], 2.0 op_sel_hi:[1,1,0]
	v_add_f32_e32 v63, v141, v63
	v_lshlrev_b32_e32 v141, 16, v192
	v_pk_mul_f32 v[64:65], v[68:69], v[64:65]
	v_lshlrev_b32_e32 v143, 16, v217
	v_pk_mul_f32 v[64:65], v[64:65], v[140:141]
	v_and_b32_e32 v142, 0xffff0000, v216
	v_lshlrev_b32_e32 v149, 16, v235
	v_and_b32_e32 v148, 0xffff0000, v234
	v_pk_mul_f32 v[64:65], v[92:93], v[64:65]
	v_pk_add_f32 v[142:143], v[142:143], v[148:149]
	v_add_f32_e32 v63, v64, v63
	v_pk_add_f32 v[142:143], v[142:143], -2.0 op_sel_hi:[1,0]
	v_add_f32_e32 v63, v65, v63
	v_and_b32_e32 v64, 0xffff0000, v46
	v_lshlrev_b32_e32 v65, 16, v46
	v_and_b32_e32 v68, 0xffff0000, v50
	v_lshlrev_b32_e32 v69, 16, v50
	v_lshlrev_b32_e32 v141, 16, v201
	v_and_b32_e32 v140, 0xffff0000, v200
	v_pk_fma_f32 v[142:143], v[104:105], v[142:143], 2.0 op_sel_hi:[1,1,0]
	v_pk_add_f32 v[64:65], v[64:65], v[68:69]
	v_lshlrev_b32_e32 v69, 16, v193
	v_and_b32_e32 v68, 0xffff0000, v192
	v_pk_mul_f32 v[140:141], v[142:143], v[140:141]
	v_and_b32_e32 v54, 0xffff0000, v201
	v_pk_mul_f32 v[68:69], v[140:141], v[68:69]
	v_lshlrev_b32_e32 v59, 16, v218
	v_pk_mul_f32 v[68:69], v[94:95], v[68:69]
	v_and_b32_e32 v58, 0xffff0000, v217
	v_add_f32_e32 v46, v68, v63
	v_add_f32_e32 v63, v69, v46
	v_lshlrev_b32_e32 v69, 16, v236
	v_and_b32_e32 v68, 0xffff0000, v235
	v_pk_add_f32 v[58:59], v[58:59], v[68:69]
	v_and_b32_e32 v46, 0xffff0000, v47
	v_lshlrev_b32_e32 v47, 16, v47
	v_and_b32_e32 v50, 0xffff0000, v51
	v_lshlrev_b32_e32 v51, 16, v51
	v_pk_add_f32 v[58:59], v[58:59], -2.0 op_sel_hi:[1,0]
	v_pk_add_f32 v[50:51], v[46:47], v[50:51]
	v_and_b32_e32 v46, 0xffff0000, v193
	v_lshlrev_b32_e32 v55, 16, v202
	v_pk_fma_f32 v[58:59], v[106:107], v[58:59], 2.0 op_sel_hi:[1,1,0]
	v_lshlrev_b32_e32 v47, 16, v194
	v_pk_mul_f32 v[54:55], v[58:59], v[54:55]
	v_and_b32_e32 v177, 0xffff0000, v237
	v_pk_mul_f32 v[46:47], v[54:55], v[46:47]
	v_and_b32_e32 v54, 0xffff0000, v52
	v_pk_mul_f32 v[46:47], v[96:97], v[46:47]
	v_lshlrev_b32_e32 v55, 16, v52
	v_add_f32_e32 v46, v46, v63
	v_add_f32_e32 v63, v47, v46
	v_and_b32_e32 v46, 0xffff0000, v48
	v_lshlrev_b32_e32 v47, 16, v48
	v_pk_add_f32 v[58:59], v[46:47], v[54:55]
	v_lshlrev_b32_e32 v47, 16, v195
	v_and_b32_e32 v46, 0xffff0000, v194
	v_lshlrev_b32_e32 v55, 16, v203
	v_and_b32_e32 v54, 0xffff0000, v202
	v_lshlrev_b32_e32 v57, 16, v219
	v_and_b32_e32 v56, 0xffff0000, v218
	v_lshlrev_b32_e32 v61, 16, v237
	v_and_b32_e32 v60, 0xffff0000, v236
	v_pk_add_f32 v[56:57], v[56:57], v[60:61]
	v_and_b32_e32 v178, 0xffff0000, v219
	v_pk_add_f32 v[56:57], v[56:57], -2.0 op_sel_hi:[1,0]
	v_add_f32_e32 v150, v136, v164
	v_pk_fma_f32 v[56:57], v[18:19], v[56:57], 2.0 op_sel_hi:[1,1,0]
	v_and_b32_e32 v48, 0xffff0000, v53
	v_pk_mul_f32 v[54:55], v[56:57], v[54:55]
	v_add_f32_e32 v67, v133, v134
	v_pk_mul_f32 v[46:47], v[54:55], v[46:47]
	v_add_f32_e32 v2, v67, v2
	v_pk_mul_f32 v[46:47], v[10:11], v[46:47]
	v_lshlrev_b32_e32 v12, 16, v245
	v_add_f32_e32 v46, v46, v63
	v_add_f32_e32 v136, v47, v46
	v_and_b32_e32 v46, 0xffff0000, v49
	v_lshlrev_b32_e32 v47, 16, v49
	v_lshlrev_b32_e32 v49, 16, v53
	v_pk_add_f32 v[48:49], v[46:47], v[48:49]
	v_add_f32_e32 v46, v177, v178
	v_add_f32_e32 v46, -2.0, v46
	v_fma_f32 v46, v21, v46, 2.0
	v_mul_f32_e32 v46, v46, v172
	v_mul_f32_e32 v46, v46, v168
	v_mul_f32_e32 v134, v13, v46
	v_pk_add_f32 v[46:47], v[134:135], v[136:137]
	v_and_b32_e32 v9, 0xffff0000, v245
	v_add_f32_e32 v2, v47, v2
	v_add_f32_e32 v2, v150, v2
	v_add_f32_e32 v2, v65, v2
	v_add_f32_e32 v2, v64, v2
	v_add_f32_e32 v2, v51, v2
	v_add_f32_e32 v2, v50, v2
	v_add_f32_e32 v2, v59, v2
	v_add_f32_e32 v2, v58, v2
	v_add_f32_e32 v2, v49, v2
	v_add_f32_e32 v2, v48, v2
	s_nop 1
	v_mov_b32_dpp v52, v2 quad_perm:[1,0,3,2] row_mask:0xf bank_mask:0xf
	v_add_f32_e32 v2, v2, v52
	s_nop 1
	v_mov_b32_dpp v52, v2 quad_perm:[2,3,0,1] row_mask:0xf bank_mask:0xf
	v_add_f32_e32 v2, v2, v52
	v_mov_b32_dpp v52, v46 quad_perm:[1,0,3,2] row_mask:0xf bank_mask:0xf
	v_mul_f32_e32 v53, 0x3c800000, v2
	v_fmac_f32_e32 v82, 0xbc800000, v2
	v_fmac_f32_e32 v4, 0xbc800000, v2
	v_fmac_f32_e32 v86, 0xbc800000, v2
	v_pk_add_f32 v[54:55], v[46:47], v[52:53]
	v_pk_add_f32 v[56:57], v[46:47], v[52:53] neg_lo:[0,1] neg_hi:[0,1]
	v_mul_f32_e32 v47, v82, v82
	v_fmac_f32_e32 v47, v4, v4
	v_fmac_f32_e32 v47, v86, v86
	v_fmac_f32_e32 v123, 0xbc800000, v2
	v_fmac_f32_e32 v47, v123, v123
	v_fmac_f32_e32 v125, 0xbc800000, v2
	v_fmac_f32_e32 v47, v125, v125
	v_fmac_f32_e32 v67, 0xbc800000, v2
	v_fmac_f32_e32 v47, v67, v67
	v_fmac_f32_e32 v47, v57, v57
	v_fmac_f32_e32 v150, 0xbc800000, v2
	v_fmac_f32_e32 v47, v150, v150
	v_fmamk_f32 v60, v2, 0xbc800000, v65
	v_fmac_f32_e32 v64, 0xbc800000, v2
	v_mov_b32_e32 v2, v53
	v_fmac_f32_e32 v47, v60, v60
	v_pk_add_f32 v[52:53], v[50:51], v[2:3] op_sel_hi:[1,0] neg_lo:[0,1] neg_hi:[0,1]
	v_fmac_f32_e32 v47, v64, v64
	v_pk_mul_f32 v[50:51], v[52:53], v[52:53]
	v_pk_add_f32 v[48:49], v[48:49], v[2:3] op_sel_hi:[1,0] neg_lo:[0,1] neg_hi:[0,1]
	v_add_f32_e32 v47, v51, v47
	v_add_f32_e32 v47, v50, v47
	v_pk_add_f32 v[50:51], v[58:59], v[2:3] op_sel_hi:[1,0] neg_lo:[0,1] neg_hi:[0,1]
	v_mov_b32_dpp v46, v54 quad_perm:[2,3,0,1] row_mask:0xf bank_mask:0xf
	v_pk_mul_f32 v[58:59], v[50:51], v[50:51]
	s_nop 0
	v_add_f32_e32 v47, v59, v47
	v_add_f32_e32 v47, v58, v47
	v_pk_mul_f32 v[58:59], v[48:49], v[48:49]
	s_nop 0
	v_add_f32_e32 v2, v59, v47
	v_add_f32_e32 v2, v58, v2
	s_nop 1
	v_mov_b32_dpp v47, v2 quad_perm:[1,0,3,2] row_mask:0xf bank_mask:0xf
	v_add_f32_e32 v2, v2, v47
	s_nop 1
	v_mov_b32_dpp v47, v2 quad_perm:[2,3,0,1] row_mask:0xf bank_mask:0xf
	v_add_f32_e32 v2, v2, v47
	v_mov_b32_e32 v47, 0x3a27c5ac
	v_fmamk_f32 v2, v2, 0x3c800000, v47
	v_cmp_gt_f32_e32 vcc, s82, v2
	v_mul_f32_e32 v47, 0x4f800000, v2
	s_nop 0
	v_cndmask_b32_e32 v2, v2, v47, vcc
	v_sqrt_f32_e32 v47, v2
	s_nop 0
	v_add_u32_e32 v58, -1, v47
	v_fma_f32 v59, -v58, v47, v2
	v_cmp_ge_f32_e64 s[38:39], 0, v59
	v_add_u32_e32 v59, 1, v47
	s_nop 0
	v_cndmask_b32_e64 v58, v47, v58, s[38:39]
	v_fma_f32 v47, -v59, v47, v2
	v_cmp_lt_f32_e64 s[38:39], 0, v47
	s_nop 1
	v_cndmask_b32_e64 v47, v58, v59, s[38:39]
	v_mul_f32_e32 v58, 0x37800000, v47
	v_cndmask_b32_e32 v47, v47, v58, vcc
	v_cmp_class_f32_e32 vcc, v2, v229
	s_nop 1
	v_cndmask_b32_e32 v2, v47, v2, vcc
	v_div_scale_f32 v47, s[4:5], v2, v2, 1.0
	v_rcp_f32_e32 v58, v47
	s_nop 0
	v_fma_f32 v59, -v47, v58, 1.0
	v_fmac_f32_e32 v58, v59, v58
	v_div_scale_f32 v59, vcc, 1.0, v2, 1.0
	v_mul_f32_e32 v61, v59, v58
	v_fma_f32 v63, -v47, v61, v59
	v_fmac_f32_e32 v61, v63, v58
	v_fma_f32 v47, -v47, v61, v59
	v_div_fmas_f32 v47, v47, v58, v61
	v_div_fixup_f32 v47, v47, v2, 1.0
	v_pk_add_f32 v[54:55], v[54:55], v[46:47]
	v_mul_f32_e32 v133, v4, v47
	v_pk_mul_f32 v[56:57], v[56:57], v[46:47]
	v_mov_b32_e32 v72, v54
	v_mov_b32_e32 v55, v57
	v_pk_mul_f32 v[56:57], v[72:73], v[132:133]
	v_mul_f32_e32 v131, v82, v47
	v_add_f32_e32 v2, v22, v57
	v_add_f32_e32 v2, v56, v2
	v_mul_f32_e32 v58, v2, v179
	v_mov_b32_e32 v2, v54
	v_pk_mul_f32 v[56:57], v[2:3], v[130:131]
	v_mul_f32_e32 v129, v86, v47
	v_add_f32_e32 v2, v23, v57
	v_mov_b32_e32 v82, v54
	v_add_f32_e32 v2, v56, v2
	v_pk_mul_f32 v[56:57], v[82:83], v[128:129]
	v_mul_f32_e32 v127, v123, v47
	v_add_f32_e32 v4, v24, v57
	v_add_f32_e32 v4, v56, v4
	v_mul_f32_e32 v59, v4, v181
	v_mov_b32_e32 v4, v54
	v_pk_mul_f32 v[56:57], v[4:5], v[126:127]
	v_mul_f32_e32 v125, v125, v47
	v_add_f32_e32 v4, v25, v57
	v_mov_b32_e32 v86, v54
	v_add_f32_e32 v4, v56, v4
	v_pk_mul_f32 v[56:57], v[86:87], v[124:125]
	v_mul_f32_e32 v123, v67, v47
	v_add_f32_e32 v46, v26, v57
	v_add_f32_e32 v46, v56, v46
	v_mul_f32_e32 v61, v46, v70
	v_mov_b32_e32 v70, v54
	v_pk_mul_f32 v[56:57], v[70:71], v[122:123]
	v_mul_f32_e32 v2, v2, v180
	v_add_f32_e32 v46, v27, v57
	v_add_f32_e32 v46, v56, v46
	v_pk_mul_f32 v[56:57], v[54:55], v[84:85]
	v_mul_f32_e32 v65, v46, v121
	v_add_f32_e32 v46, v28, v57
	v_mul_f32_e32 v121, v150, v47
	v_mov_b32_e32 v55, v38
	v_add_f32_e32 v46, v56, v46
	v_pk_mul_f32 v[56:57], v[54:55], v[120:121]
	v_mul_f32_e32 v68, v46, v119
	v_add_f32_e32 v46, v29, v57
	v_mul_f32_e32 v119, v60, v47
	v_mov_b32_e32 v55, v39
	v_add_f32_e32 v46, v56, v46
	v_pk_mul_f32 v[56:57], v[54:55], v[118:119]
	v_mul_f32_e32 v69, v46, v117
	v_add_f32_e32 v46, v30, v57
	v_mul_f32_e32 v117, v64, v47
	v_mov_b32_e32 v55, v40
	v_add_f32_e32 v46, v56, v46
	v_pk_mul_f32 v[56:57], v[54:55], v[116:117]
	v_mul_f32_e32 v60, v46, v115
	v_add_f32_e32 v46, v31, v57
	v_mul_f32_e32 v115, v53, v47
	v_mov_b32_e32 v55, v41
	v_add_f32_e32 v46, v56, v46
	v_pk_mul_f32 v[56:57], v[54:55], v[114:115]
	v_mul_f32_e32 v64, v46, v113
	v_add_f32_e32 v46, v32, v57
	v_mul_f32_e32 v113, v52, v47
	v_mov_b32_e32 v55, v42
	v_add_f32_e32 v46, v56, v46
	v_pk_mul_f32 v[52:53], v[54:55], v[112:113]
	v_mul_f32_e32 v70, v46, v111
	v_add_f32_e32 v46, v33, v53
	v_mul_f32_e32 v111, v51, v47
	v_mov_b32_e32 v55, v43
	v_add_f32_e32 v46, v52, v46
	v_pk_mul_f32 v[52:53], v[54:55], v[110:111]
	v_mul_f32_e32 v72, v46, v109
	v_add_f32_e32 v46, v34, v53
	v_mul_f32_e32 v109, v50, v47
	v_mov_b32_e32 v55, v44
	v_add_f32_e32 v46, v52, v46
	v_pk_mul_f32 v[50:51], v[54:55], v[108:109]
	v_mul_f32_e32 v20, v46, v20
	v_add_f32_e32 v46, v35, v51
	v_mul_f32_e32 v67, v49, v47
	v_mov_b32_e32 v55, v45
	v_add_f32_e32 v46, v50, v46
	v_pk_mul_f32 v[50:51], v[54:55], v[66:67]
	v_mul_f32_e32 v56, 0x41000000, v58
	v_mul_f32_e32 v57, 0x41000000, v2
	v_mul_f32_e32 v82, v46, v17
	v_add_f32_e32 v17, v36, v51
	v_mul_f32_e32 v63, v48, v47
	v_mov_b32_e32 v55, v0
	v_mul_f32_e32 v48, 0x41000000, v60
	v_mul_f32_e32 v49, 0x41000000, v64
	v_med3_f32 v58, v56, s33, v233
	v_med3_f32 v57, v57, s33, v233
	v_mov_b32_e32 v56, v1
	v_add_f32_e32 v17, v50, v17
	v_pk_mul_f32 v[46:47], v[54:55], v[62:63]
	v_cvt_pk_fp8_f32 v56, v58, v57
	v_med3_f32 v48, v48, s33, v233
	v_med3_f32 v49, v49, s33, v233
	v_mov_b32_e32 v58, v1
	v_mul_f32_e32 v51, v17, v12
	v_add_f32_e32 v12, v37, v47
	v_cvt_pk_fp8_f32 v58, v48, v49
	v_mul_f32_e32 v4, v4, v182
	v_add_f32_e32 v12, v46, v12
	v_mul_f32_e32 v46, v12, v9
	v_mul_f32_e32 v52, 0x41000000, v59
	v_mul_f32_e32 v9, 0x41000000, v70
	v_mul_f32_e32 v53, 0x41000000, v4
	v_mul_f32_e32 v12, 0x41000000, v72
	v_mul_f32_e32 v54, 0x41000000, v61
	v_mul_f32_e32 v17, 0x41000000, v20
	v_mul_f32_e32 v55, 0x41000000, v65
	v_mul_f32_e32 v20, 0x41000000, v82
	v_med3_f32 v52, v52, s33, v233
	v_med3_f32 v53, v53, s33, v233
	v_med3_f32 v9, v9, s33, v233
	v_med3_f32 v12, v12, s33, v233
	v_cvt_pk_fp8_f32 v56, v52, v53 op_sel:[0,0,1]
	v_med3_f32 v52, v54, s33, v233
	v_med3_f32 v53, v55, s33, v233
	v_mov_b32_e32 v57, v1
	v_cvt_pk_fp8_f32 v58, v9, v12 op_sel:[0,0,1]
	v_med3_f32 v9, v17, s33, v233
	v_med3_f32 v12, v20, s33, v233
	v_mov_b32_e32 v59, v1
	v_cvt_pk_fp8_f32 v57, v52, v53
	v_cvt_pk_fp8_f32 v59, v9, v12
	v_mul_f32_e32 v50, 0x41000000, v68
	v_mul_f32_e32 v2, 0x41000000, v51
	v_mul_f32_e32 v51, 0x41000000, v69
	v_mul_f32_e32 v4, 0x41000000, v46
	v_med3_f32 v50, v50, s33, v233
	v_med3_f32 v51, v51, s33, v233
	v_med3_f32 v2, v2, s33, v233
	v_med3_f32 v4, v4, s33, v233
	v_cvt_pk_fp8_f32 v57, v50, v51 op_sel:[0,0,1]
	v_cvt_pk_fp8_f32 v59, v2, v4 op_sel:[0,0,1]
	v_lshl_add_u64 v[46:47], s[40:41], 0, v[78:79]
	v_add_co_u32_e32 v46, vcc, 0x1d200000, v46
	v_lshl_add_u64 v[78:79], v[78:79], 0, s[22:23]
	s_nop 0
	v_addc_co_u32_e32 v47, vcc, 0, v47, vcc
	global_store_dwordx4 v[46:47], v[56:59], off offset:1024 sc1
	s_cbranch_scc1 .LBB0_1141

.LBB0_1300:
	v_lshl_add_u64 v[2:3], s[58:59], 0, v[60:61]
	v_add_co_u32_e32 v4, vcc, 0x11100000, v2
	v_lshl_add_u64 v[158:159], s[58:59], 0, v[58:59]
	s_nop 0
	v_addc_co_u32_e32 v5, vcc, 0, v3, vcc
	global_load_dwordx2 v[94:95], v[4:5], off nt
	v_add_co_u32_e32 v96, vcc, 0x11101000, v2
	s_nop 1
	v_addc_co_u32_e32 v97, vcc, 0, v3, vcc
	global_load_dwordx2 v[98:99], v[96:97], off nt
	global_load_dwordx2 v[100:101], v[4:5], off offset:512 nt
	global_load_dwordx2 v[106:107], v[96:97], off offset:512 nt
	global_load_dwordx2 v[108:109], v[4:5], off offset:1024 nt
	global_load_dwordx2 v[110:111], v[96:97], off offset:1024 nt
	global_load_dwordx2 v[20:21], v[4:5], off offset:1536 nt
	global_load_dwordx2 v[18:19], v[96:97], off offset:1536 nt
	global_load_dwordx2 v[16:17], v[4:5], off offset:2048 nt
	global_load_dwordx2 v[14:15], v[96:97], off offset:2048 nt
	global_load_dwordx2 v[12:13], v[4:5], off offset:2560 nt
	global_load_dwordx2 v[10:11], v[96:97], off offset:2560 nt
	global_load_dwordx2 v[8:9], v[4:5], off offset:3072 nt
	global_load_dwordx2 v[6:7], v[96:97], off offset:3072 nt
	global_load_dwordx2 v[2:3], v[4:5], off offset:3584 nt
	s_nop 0
	global_load_dwordx2 v[4:5], v[96:97], off offset:3584 nt
	s_waitcnt vmcnt(15)
	v_and_b32_e32 v157, 0xffff0000, v94
	v_and_b32_e32 v155, 0xffff0000, v95
	v_lshlrev_b32_e32 v156, 16, v94
	v_lshlrev_b32_e32 v154, 16, v95
	v_mul_f32_e32 v47, v157, v157
	v_mul_f32_e32 v49, v155, v155
	v_fmac_f32_e32 v47, v156, v156
	v_fmac_f32_e32 v49, v154, v154
	v_add_f32_e32 v47, v47, v49
	s_waitcnt vmcnt(14)
	v_and_b32_e32 v153, 0xffff0000, v98
	v_and_b32_e32 v119, 0xffff0000, v99
	v_lshlrev_b32_e32 v152, 16, v98
	v_lshlrev_b32_e32 v118, 16, v99
	v_mul_f32_e32 v49, v153, v153
	v_mul_f32_e32 v51, v119, v119
	v_fmac_f32_e32 v49, v152, v152
	v_fmac_f32_e32 v51, v118, v118
	s_waitcnt vmcnt(13)
	v_and_b32_e32 v151, 0xffff0000, v100
	v_and_b32_e32 v149, 0xffff0000, v101
	v_add_f32_e32 v49, v49, v51
	v_lshlrev_b32_e32 v150, 16, v100
	v_lshlrev_b32_e32 v148, 16, v101
	v_mul_f32_e32 v51, v151, v151
	v_mul_f32_e32 v53, v149, v149
	v_fmac_f32_e32 v51, v150, v150
	v_fmac_f32_e32 v53, v148, v148
	s_waitcnt vmcnt(12)
	v_and_b32_e32 v147, 0xffff0000, v106
	v_and_b32_e32 v145, 0xffff0000, v107
	v_add_f32_e32 v51, v51, v53
	v_lshlrev_b32_e32 v146, 16, v106
	v_lshlrev_b32_e32 v144, 16, v107
	v_add_f32_e32 v47, v47, v51
	v_mul_f32_e32 v51, v147, v147
	v_mul_f32_e32 v53, v145, v145
	v_fmac_f32_e32 v51, v146, v146
	v_fmac_f32_e32 v53, v144, v144
	v_add_f32_e32 v51, v51, v53
	s_waitcnt vmcnt(11)
	v_and_b32_e32 v143, 0xffff0000, v108
	v_and_b32_e32 v141, 0xffff0000, v109
	v_add_f32_e32 v49, v49, v51
	v_lshlrev_b32_e32 v142, 16, v108
	v_lshlrev_b32_e32 v140, 16, v109
	v_mul_f32_e32 v51, v143, v143
	v_mul_f32_e32 v53, v141, v141
	v_fmac_f32_e32 v51, v142, v142
	v_fmac_f32_e32 v53, v140, v140
	s_waitcnt vmcnt(9)
	v_and_b32_e32 v131, 0xffff0000, v20
	v_and_b32_e32 v129, 0xffff0000, v21
	v_and_b32_e32 v139, 0xffff0000, v110
	v_and_b32_e32 v137, 0xffff0000, v111
	v_add_f32_e32 v51, v51, v53
	v_lshlrev_b32_e32 v130, 16, v20
	v_lshlrev_b32_e32 v128, 16, v21
	s_waitcnt vmcnt(8)
	v_lshlrev_b32_e32 v132, 16, v18
	v_and_b32_e32 v133, 0xffff0000, v18
	v_lshlrev_b32_e32 v134, 16, v19
	v_and_b32_e32 v135, 0xffff0000, v19
	v_mul_f32_e32 v18, v131, v131
	v_mul_f32_e32 v19, v129, v129
	s_waitcnt vmcnt(7)
	v_and_b32_e32 v127, 0xffff0000, v16
	v_and_b32_e32 v125, 0xffff0000, v17
	v_lshlrev_b32_e32 v138, 16, v110
	v_lshlrev_b32_e32 v136, 16, v111
	v_add_f32_e32 v47, v47, v51
	v_mul_f32_e32 v51, v139, v139
	v_mul_f32_e32 v53, v137, v137
	v_fmac_f32_e32 v18, v130, v130
	v_fmac_f32_e32 v19, v128, v128
	v_lshlrev_b32_e32 v126, 16, v16
	v_lshlrev_b32_e32 v124, 16, v17
	s_waitcnt vmcnt(6)
	v_lshlrev_b32_e32 v122, 16, v14
	v_and_b32_e32 v123, 0xffff0000, v14
	v_lshlrev_b32_e32 v120, 16, v15
	v_and_b32_e32 v121, 0xffff0000, v15
	v_mul_f32_e32 v14, v127, v127
	v_mul_f32_e32 v15, v125, v125
	v_fmac_f32_e32 v51, v138, v138
	v_fmac_f32_e32 v53, v136, v136
	v_add_f32_e32 v18, v18, v19
	v_mul_f32_e32 v19, v133, v133
	v_mul_f32_e32 v20, v135, v135
	v_fmac_f32_e32 v14, v126, v126
	v_fmac_f32_e32 v15, v124, v124
	v_add_f32_e32 v51, v51, v53
	v_fmac_f32_e32 v19, v132, v132
	v_fmac_f32_e32 v20, v134, v134
	v_add_f32_e32 v14, v14, v15
	v_mul_f32_e32 v15, v123, v123
	v_mul_f32_e32 v16, v121, v121
	v_add_f32_e32 v49, v49, v51
	v_add_f32_e32 v19, v19, v20
	v_fmac_f32_e32 v15, v122, v122
	v_fmac_f32_e32 v16, v120, v120
	s_waitcnt vmcnt(5)
	v_and_b32_e32 v117, 0xffff0000, v12
	v_and_b32_e32 v115, 0xffff0000, v13
	v_add_f32_e32 v18, v47, v18
	v_add_f32_e32 v19, v49, v19
	v_add_f32_e32 v15, v15, v16
	v_lshlrev_b32_e32 v116, 16, v12
	v_lshlrev_b32_e32 v114, 16, v13
	s_waitcnt vmcnt(4)
	v_lshlrev_b32_e32 v112, 16, v10
	v_and_b32_e32 v113, 0xffff0000, v10
	v_lshlrev_b32_e32 v110, 16, v11
	v_and_b32_e32 v111, 0xffff0000, v11
	v_mul_f32_e32 v10, v117, v117
	v_mul_f32_e32 v11, v115, v115
	s_waitcnt vmcnt(3)
	v_and_b32_e32 v109, 0xffff0000, v8
	v_and_b32_e32 v107, 0xffff0000, v9
	v_add_f32_e32 v14, v18, v14
	v_add_f32_e32 v15, v19, v15
	v_fmac_f32_e32 v10, v116, v116
	v_fmac_f32_e32 v11, v114, v114
	v_lshlrev_b32_e32 v108, 16, v8
	v_lshlrev_b32_e32 v106, 16, v9
	s_waitcnt vmcnt(2)
	v_lshlrev_b32_e32 v20, 16, v6
	v_and_b32_e32 v21, 0xffff0000, v6
	v_lshlrev_b32_e32 v18, 16, v7
	v_and_b32_e32 v19, 0xffff0000, v7
	v_mul_f32_e32 v6, v109, v109
	v_mul_f32_e32 v7, v107, v107
	s_waitcnt vmcnt(1)
	v_and_b32_e32 v101, 0xffff0000, v2
	v_and_b32_e32 v99, 0xffff0000, v3
	v_add_f32_e32 v10, v10, v11
	v_fmac_f32_e32 v6, v108, v108
	v_fmac_f32_e32 v7, v106, v106
	v_lshlrev_b32_e32 v100, 16, v2
	v_lshlrev_b32_e32 v98, 16, v3
	v_mul_f32_e32 v2, v101, v101
	v_mul_f32_e32 v3, v99, v99
	v_add_f32_e32 v10, v14, v10
	v_add_f32_e32 v6, v6, v7
	s_waitcnt vmcnt(0)
	v_and_b32_e32 v97, 0xffff0000, v4
	v_and_b32_e32 v95, 0xffff0000, v5
	v_fmac_f32_e32 v2, v100, v100
	v_fmac_f32_e32 v3, v98, v98
	v_add_f32_e32 v6, v10, v6
	v_lshlrev_b32_e32 v96, 16, v4
	v_lshlrev_b32_e32 v94, 16, v5
	v_add_f32_e32 v2, v2, v3
	v_mul_f32_e32 v3, v97, v97
	v_mul_f32_e32 v4, v95, v95
	v_add_f32_e32 v2, v6, v2
	v_fmac_f32_e32 v3, v96, v96
	v_fmac_f32_e32 v4, v94, v94
	v_add_f32_e32 v3, v3, v4
	v_mov_b32_dpp v4, v2 quad_perm:[1,0,3,2] row_mask:0xf bank_mask:0xf
	v_mul_f32_e32 v11, v113, v113
	v_mul_f32_e32 v12, v111, v111
	v_fmac_f32_e32 v11, v112, v112
	v_fmac_f32_e32 v12, v110, v110
	s_waitcnt lgkmcnt(0)
	v_add_f32_e32 v2, v2, v4
	s_nop 1
	v_mov_b32_dpp v4, v2 quad_perm:[2,3,0,1] row_mask:0xf bank_mask:0xf
	v_mul_f32_e32 v7, v21, v21
	v_mul_f32_e32 v8, v19, v19
	v_add_f32_e32 v11, v11, v12
	v_fmac_f32_e32 v7, v20, v20
	v_add_f32_e32 v2, v2, v4
	s_nop 1
	v_mov_b32_dpp v4, v2 row_half_mirror row_mask:0xf bank_mask:0xf
	v_fmac_f32_e32 v8, v18, v18
	v_add_f32_e32 v11, v15, v11
	v_add_f32_e32 v7, v7, v8
	v_add_f32_e32 v7, v11, v7
	v_add_f32_e32 v2, v2, v4
	s_nop 1
	v_mov_b32_dpp v4, v2 row_mirror row_mask:0xf bank_mask:0xf
	v_add_f32_e32 v3, v7, v3
	v_mov_b32_e32 v51, 0
	v_add_f32_e32 v2, v2, v4
	v_mov_b32_e32 v4, v2
	s_nop 1
	v_permlane16_swap_b32_e32 v2, v4
	v_add_f32_e32 v2, v2, v4
	v_mov_b32_e32 v4, v2
	s_nop 1
	v_permlane32_swap_b32_e32 v2, v4
	v_add_f32_e32 v2, v2, v4
	v_fmamk_f32 v2, v2, 0x3a000000, v228
	v_cmp_gt_f32_e32 vcc, s82, v2
	v_mul_f32_e32 v4, 0x4f800000, v2
	s_nop 0
	v_cndmask_b32_e32 v2, v2, v4, vcc
	v_sqrt_f32_e32 v4, v2
	s_nop 0
	v_add_u32_e32 v5, -1, v4
	v_fma_f32 v6, -v5, v4, v2
	v_cmp_ge_f32_e64 s[44:45], 0, v6
	v_add_u32_e32 v6, 1, v4
	s_nop 0
	v_cndmask_b32_e64 v5, v4, v5, s[44:45]
	v_fma_f32 v4, -v6, v4, v2
	v_cmp_lt_f32_e64 s[44:45], 0, v4
	s_nop 1
	v_cndmask_b32_e64 v4, v5, v6, s[44:45]
	v_mul_f32_e32 v5, 0x37800000, v4
	v_cndmask_b32_e32 v4, v4, v5, vcc
	v_cmp_class_f32_e32 vcc, v2, v229
	s_nop 1
	v_cndmask_b32_e32 v2, v4, v2, vcc
	v_mov_b32_dpp v4, v3 quad_perm:[1,0,3,2] row_mask:0xf bank_mask:0xf
	v_add_f32_e32 v3, v3, v4
	s_nop 1
	v_mov_b32_dpp v4, v3 quad_perm:[2,3,0,1] row_mask:0xf bank_mask:0xf
	v_add_f32_e32 v3, v3, v4
	s_nop 1
	v_mov_b32_dpp v4, v3 row_half_mirror row_mask:0xf bank_mask:0xf
	v_add_f32_e32 v3, v3, v4
	s_nop 1
	v_mov_b32_dpp v4, v3 row_mirror row_mask:0xf bank_mask:0xf
	v_add_f32_e32 v3, v3, v4
	v_mov_b32_e32 v4, v3
	s_nop 1
	v_permlane16_swap_b32_e32 v3, v4
	v_add_f32_e32 v3, v3, v4
	v_mov_b32_e32 v4, v3
	s_nop 1
	v_permlane32_swap_b32_e32 v3, v4
	v_add_f32_e32 v3, v3, v4
	v_fmamk_f32 v3, v3, 0x3a000000, v228
	v_cmp_gt_f32_e32 vcc, s82, v3
	v_mul_f32_e32 v4, 0x4f800000, v3
	s_nop 0
	v_cndmask_b32_e32 v3, v3, v4, vcc
	v_sqrt_f32_e32 v4, v3
	s_nop 0
	v_add_u32_e32 v5, -1, v4
	v_fma_f32 v6, -v5, v4, v3
	v_cmp_ge_f32_e64 s[44:45], 0, v6
	v_add_u32_e32 v6, 1, v4
	s_nop 0
	v_cndmask_b32_e64 v5, v4, v5, s[44:45]
	v_fma_f32 v4, -v6, v4, v3
	v_cmp_lt_f32_e64 s[44:45], 0, v4
	s_nop 1
	v_cndmask_b32_e64 v4, v5, v6, s[44:45]
	v_mul_f32_e32 v5, 0x37800000, v4
	v_cndmask_b32_e32 v4, v4, v5, vcc
	v_cmp_class_f32_e32 vcc, v3, v229
	s_nop 1
	v_cndmask_b32_e32 v3, v4, v3, vcc
	v_div_scale_f32 v4, s[4:5], v2, v2, 1.0
	v_rcp_f32_e32 v5, v4
	s_nop 0
	v_fma_f32 v6, -v4, v5, 1.0
	v_fmac_f32_e32 v5, v6, v5
	v_div_scale_f32 v6, vcc, 1.0, v2, 1.0
	v_mul_f32_e32 v7, v6, v5
	v_fma_f32 v8, -v4, v7, v6
	v_fmac_f32_e32 v7, v8, v5
	v_fma_f32 v4, -v4, v7, v6
	v_div_fmas_f32 v4, v4, v5, v7
	v_div_fixup_f32 v102, v4, v2, 1.0
	v_div_scale_f32 v2, s[4:5], v3, v3, 1.0
	v_rcp_f32_e32 v4, v2
	v_pk_mul_f32 v[156:157], v[102:103], v[156:157] op_sel_hi:[0,1]
	v_pk_mul_f32 v[154:155], v[102:103], v[154:155] op_sel_hi:[0,1]
	v_fma_f32 v5, -v2, v4, 1.0
	v_fmac_f32_e32 v4, v5, v4
	v_div_scale_f32 v5, vcc, 1.0, v3, 1.0
	v_mul_f32_e32 v6, v5, v4
	v_fma_f32 v7, -v2, v6, v5
	v_fmac_f32_e32 v6, v7, v4
	v_fma_f32 v2, -v2, v6, v5
	v_div_fmas_f32 v2, v2, v4, v6
	v_div_fixup_f32 v104, v2, v3, 1.0
	global_load_dwordx4 v[2:5], v[26:27], off
	global_load_dwordx4 v[6:9], v[62:63], off
	global_load_dwordx4 v[14:17], v[64:65], off
	v_pk_mul_f32 v[152:153], v[104:105], v[152:153] op_sel_hi:[0,1]
	v_pk_mul_f32 v[118:119], v[104:105], v[118:119] op_sel_hi:[0,1]
	s_waitcnt vmcnt(1)
	v_pk_add_f32 v[8:9], v[8:9], 1.0 op_sel_hi:[1,0]
	v_pk_add_f32 v[6:7], v[6:7], 1.0 op_sel_hi:[1,0]
	v_pk_mul_f32 v[160:161], v[4:5], v[8:9]
	v_pk_mul_f32 v[162:163], v[2:3], v[6:7]
	global_load_dwordx4 v[2:5], v[66:67], off
	global_load_dwordx4 v[10:13], v[68:69], off
	global_load_dwordx4 v[6:9], v[28:29], off
	s_waitcnt vmcnt(3)
	v_pk_fma_f32 v[156:157], v[162:163], v[156:157], v[14:15]
	v_pk_fma_f32 v[154:155], v[160:161], v[154:155], v[16:17]
	v_med3_f32 v47, v156, s33, v233
	v_med3_f32 v49, v157, s33, v233
	v_cvt_pk_fp8_f32 v51, v47, v49
	ds_read_b128 v[206:209], v105
	ds_read_b128 v[238:241], v105 offset:2048
	v_med3_f32 v47, v154, s33, v233
	v_med3_f32 v49, v155, s33, v233
	v_cvt_pk_fp8_f32 v51, v47, v49 op_sel:[0,0,1]
	v_pk_fma_f32 v[16:17], v[160:161], v[118:119], v[16:17]
	v_pk_fma_f32 v[14:15], v[162:163], v[152:153], v[14:15]
	v_add_co_u32_e32 v118, vcc, s80, v158
	s_waitcnt lgkmcnt(1)
	v_fma_f32 v224, v156, v206, 0
	v_addc_co_u32_e32 v119, vcc, 0, v159, vcc
	v_fma_f32 v223, v156, v207, 0
	v_fma_f32 v221, v156, v208, 0
	v_fma_f32 v217, v156, v209, 0
	v_fma_f32 v225, v14, v206, 0
	v_fma_f32 v222, v14, v207, 0
	v_fma_f32 v219, v14, v208, 0
	v_fma_f32 v215, v14, v209, 0
	ds_read_b128 v[206:209], v105 offset:1024
	global_store_dword v[118:119], v51, off
	v_med3_f32 v47, v14, s33, v233
	v_med3_f32 v49, v15, s33, v233
	v_mov_b32_e32 v51, 0
	v_cvt_pk_fp8_f32 v51, v47, v49
	v_med3_f32 v47, v16, s33, v233
	v_med3_f32 v49, v17, s33, v233
	s_waitcnt lgkmcnt(0)
	v_fma_f32 v220, v156, v206, 0
	v_fma_f32 v216, v156, v207, 0
	v_fma_f32 v213, v156, v208, 0
	v_fma_f32 v211, v156, v209, 0
	v_fma_f32 v218, v14, v206, 0
	v_fma_f32 v214, v14, v207, 0
	v_fma_f32 v212, v14, v208, 0
	v_fma_f32 v210, v14, v209, 0
	v_fma_f32 v209, v156, v238, 0
	v_fma_f32 v207, v156, v239, 0
	v_fma_f32 v205, v156, v240, 0
	v_fma_f32 v153, v156, v241, 0
	v_fma_f32 v208, v14, v238, 0
	v_fma_f32 v206, v14, v239, 0
	v_fma_f32 v158, v14, v240, 0
	v_fma_f32 v57, v14, v241, 0
	ds_read_b128 v[238:241], v105 offset:3072
	v_cvt_pk_fp8_f32 v51, v47, v49 op_sel:[0,0,1]
	global_store_dword v[118:119], v51, off offset:2048
	s_waitcnt lgkmcnt(0)
	v_fma_f32 v159, v156, v238, 0
	v_fma_f32 v152, v156, v239, 0
	v_fma_f32 v53, v156, v240, 0
	v_fma_f32 v49, v156, v241, 0
	v_fma_f32 v156, v14, v238, 0
	v_fma_f32 v55, v14, v239, 0
	v_fma_f32 v51, v14, v240, 0
	v_fma_f32 v47, v14, v241, 0
	ds_read_b128 v[234:237], v105 offset:4096
	ds_read_b128 v[242:245], v105 offset:5120
	ds_read_b128 v[246:249], v105 offset:6144
	s_waitcnt lgkmcnt(2)
	v_fmac_f32_e32 v224, v157, v234
	v_fmac_f32_e32 v223, v157, v235
	v_fmac_f32_e32 v221, v157, v236
	v_fmac_f32_e32 v217, v157, v237
	v_fmac_f32_e32 v225, v15, v234
	v_fmac_f32_e32 v222, v15, v235
	v_fmac_f32_e32 v219, v15, v236
	v_fmac_f32_e32 v215, v15, v237
	ds_read_b128 v[234:237], v105 offset:7168
	s_waitcnt lgkmcnt(2)
	v_fmac_f32_e32 v220, v157, v242
	v_fmac_f32_e32 v216, v157, v243
	v_fmac_f32_e32 v213, v157, v244
	v_fmac_f32_e32 v211, v157, v245
	v_fmac_f32_e32 v218, v15, v242
	v_fmac_f32_e32 v214, v15, v243
	v_fmac_f32_e32 v212, v15, v244
	v_fmac_f32_e32 v210, v15, v245
	ds_read_b128 v[242:245], v105 offset:8192
	s_waitcnt lgkmcnt(2)
	v_fmac_f32_e32 v209, v157, v246
	v_fmac_f32_e32 v207, v157, v247
	v_fmac_f32_e32 v205, v157, v248
	v_fmac_f32_e32 v153, v157, v249
	v_fmac_f32_e32 v208, v15, v246
	v_fmac_f32_e32 v206, v15, v247
	v_fmac_f32_e32 v158, v15, v248
	v_fmac_f32_e32 v57, v15, v249
	ds_read_b128 v[246:249], v105 offset:9216
	s_waitcnt lgkmcnt(2)
	v_fmac_f32_e32 v159, v157, v234
	v_fmac_f32_e32 v152, v157, v235
	v_fmac_f32_e32 v53, v157, v236
	v_fmac_f32_e32 v49, v157, v237
	v_fmac_f32_e32 v156, v15, v234
	v_fmac_f32_e32 v55, v15, v235
	v_fmac_f32_e32 v51, v15, v236
	v_fmac_f32_e32 v47, v15, v237
	ds_read_b128 v[234:237], v105 offset:10240
	s_waitcnt lgkmcnt(2)
	v_fmac_f32_e32 v224, v154, v242
	v_fmac_f32_e32 v223, v154, v243
	v_fmac_f32_e32 v221, v154, v244
	v_fmac_f32_e32 v217, v154, v245
	v_fmac_f32_e32 v225, v16, v242
	v_fmac_f32_e32 v222, v16, v243
	v_fmac_f32_e32 v219, v16, v244
	v_fmac_f32_e32 v215, v16, v245
	ds_read_b128 v[242:245], v105 offset:11264
	s_waitcnt lgkmcnt(2)
	v_fmac_f32_e32 v220, v154, v246
	v_fmac_f32_e32 v216, v154, v247
	v_fmac_f32_e32 v213, v154, v248
	v_fmac_f32_e32 v211, v154, v249
	v_fmac_f32_e32 v218, v16, v246
	v_fmac_f32_e32 v214, v16, v247
	v_fmac_f32_e32 v212, v16, v248
	v_fmac_f32_e32 v210, v16, v249
	ds_read_b128 v[246:249], v105 offset:12288
	s_waitcnt lgkmcnt(2)
	v_fmac_f32_e32 v209, v154, v234
	v_fmac_f32_e32 v207, v154, v235
	v_fmac_f32_e32 v205, v154, v236
	v_fmac_f32_e32 v153, v154, v237
	v_fmac_f32_e32 v208, v16, v234
	v_fmac_f32_e32 v206, v16, v235
	v_fmac_f32_e32 v158, v16, v236
	v_fmac_f32_e32 v57, v16, v237
	ds_read_b128 v[234:237], v105 offset:13312
	s_waitcnt lgkmcnt(2)
	v_fmac_f32_e32 v159, v154, v242
	v_fmac_f32_e32 v152, v154, v243
	v_fmac_f32_e32 v53, v154, v244
	v_fmac_f32_e32 v49, v154, v245
	v_fmac_f32_e32 v156, v16, v242
	v_fmac_f32_e32 v55, v16, v243
	v_fmac_f32_e32 v51, v16, v244
	v_fmac_f32_e32 v47, v16, v245
	ds_read_b128 v[242:245], v105 offset:14336
	s_waitcnt lgkmcnt(2)
	v_fmac_f32_e32 v224, v155, v246
	v_fmac_f32_e32 v223, v155, v247
	v_fmac_f32_e32 v221, v155, v248
	v_fmac_f32_e32 v217, v155, v249
	v_fmac_f32_e32 v225, v17, v246
	v_fmac_f32_e32 v222, v17, v247
	v_fmac_f32_e32 v219, v17, v248
	v_fmac_f32_e32 v215, v17, v249
	ds_read_b128 v[246:249], v105 offset:15360
	s_waitcnt lgkmcnt(2)
	v_fmac_f32_e32 v220, v155, v234
	v_fmac_f32_e32 v216, v155, v235
	v_fmac_f32_e32 v213, v155, v236
	v_fmac_f32_e32 v211, v155, v237
	v_fmac_f32_e32 v218, v17, v234
	v_fmac_f32_e32 v214, v17, v235
	v_fmac_f32_e32 v212, v17, v236
	v_fmac_f32_e32 v210, v17, v237
	ds_read_b128 v[234:237], v105 offset:16384
	s_waitcnt lgkmcnt(2)
	v_fmac_f32_e32 v209, v155, v242
	v_fmac_f32_e32 v207, v155, v243
	v_fmac_f32_e32 v205, v155, v244
	v_fmac_f32_e32 v153, v155, v245
	v_fmac_f32_e32 v208, v17, v242
	v_fmac_f32_e32 v206, v17, v243
	v_fmac_f32_e32 v158, v17, v244
	v_fmac_f32_e32 v57, v17, v245
	ds_read_b128 v[242:245], v105 offset:17408
	s_waitcnt lgkmcnt(2)
	v_fmac_f32_e32 v53, v155, v248
	v_fmac_f32_e32 v55, v17, v247
	v_fmac_f32_e32 v51, v17, v248
	v_fmac_f32_e32 v159, v155, v246
	v_fmac_f32_e32 v152, v155, v247
	v_fmac_f32_e32 v49, v155, v249
	v_fmac_f32_e32 v156, v17, v246
	v_fmac_f32_e32 v47, v17, v249
	ds_read_b128 v[246:249], v105 offset:18432
	s_waitcnt vmcnt(3)
	v_pk_add_f32 v[10:11], v[10:11], 1.0 op_sel_hi:[1,0]
	v_pk_mul_f32 v[150:151], v[102:103], v[150:151] op_sel_hi:[0,1]
	s_waitcnt vmcnt(2)
	v_pk_mul_f32 v[154:155], v[6:7], v[10:11]
	v_pk_add_f32 v[12:13], v[12:13], 1.0 op_sel_hi:[1,0]
	v_pk_fma_f32 v[160:161], v[150:151], v[154:155], v[2:3]
	v_pk_mul_f32 v[146:147], v[104:105], v[146:147] op_sel_hi:[0,1]
	v_pk_mul_f32 v[16:17], v[8:9], v[12:13]
	v_pk_mul_f32 v[14:15], v[102:103], v[148:149] op_sel_hi:[0,1]
	v_pk_mul_f32 v[144:145], v[104:105], v[144:145] op_sel_hi:[0,1]
	v_pk_fma_f32 v[154:155], v[154:155], v[146:147], v[2:3]
	v_med3_f32 v2, v160, s33, v233
	v_med3_f32 v3, v161, s33, v233
	v_mov_b32_e32 v148, 0
	v_pk_fma_f32 v[14:15], v[14:15], v[16:17], v[4:5]
	v_pk_fma_f32 v[16:17], v[16:17], v[144:145], v[4:5]
	v_cvt_pk_fp8_f32 v148, v2, v3
	v_med3_f32 v4, v154, s33, v233
	v_med3_f32 v5, v155, s33, v233
	v_mov_b32_e32 v149, 0
	v_cvt_pk_fp8_f32 v149, v4, v5
	v_med3_f32 v2, v14, s33, v233
	v_med3_f32 v3, v15, s33, v233
	v_cvt_pk_fp8_f32 v148, v2, v3 op_sel:[0,0,1]
	v_med3_f32 v2, v16, s33, v233
	v_med3_f32 v3, v17, s33, v233
	global_load_dwordx4 v[6:9], v[70:71], off
	global_load_dwordx4 v[10:13], v[72:73], off
	v_cvt_pk_fp8_f32 v149, v2, v3 op_sel:[0,0,1]
	global_load_dwordx4 v[2:5], v[30:31], off
	global_store_dword v[118:119], v148, off offset:256
	global_store_dword v[118:119], v149, off offset:2304
	s_waitcnt lgkmcnt(2)
	v_fmac_f32_e32 v224, v160, v234
	v_fmac_f32_e32 v223, v160, v235
	v_fmac_f32_e32 v221, v160, v236
	v_fmac_f32_e32 v217, v160, v237
	v_fmac_f32_e32 v225, v154, v234
	v_fmac_f32_e32 v222, v154, v235
	v_fmac_f32_e32 v219, v154, v236
	v_fmac_f32_e32 v215, v154, v237
	ds_read_b128 v[234:237], v105 offset:19456
	s_waitcnt lgkmcnt(2)
	v_fmac_f32_e32 v220, v160, v242
	v_fmac_f32_e32 v216, v160, v243
	v_fmac_f32_e32 v213, v160, v244
	v_fmac_f32_e32 v211, v160, v245
	v_fmac_f32_e32 v218, v154, v242
	v_fmac_f32_e32 v214, v154, v243
	v_fmac_f32_e32 v212, v154, v244
	v_fmac_f32_e32 v210, v154, v245
	ds_read_b128 v[242:245], v105 offset:20480
	s_waitcnt lgkmcnt(2)
	v_fmac_f32_e32 v209, v160, v246
	v_fmac_f32_e32 v207, v160, v247
	v_fmac_f32_e32 v205, v160, v248
	v_fmac_f32_e32 v153, v160, v249
	v_fmac_f32_e32 v208, v154, v246
	v_fmac_f32_e32 v206, v154, v247
	v_fmac_f32_e32 v158, v154, v248
	v_fmac_f32_e32 v57, v154, v249
	ds_read_b128 v[246:249], v105 offset:21504
	s_waitcnt lgkmcnt(2)
	v_fmac_f32_e32 v159, v160, v234
	v_fmac_f32_e32 v152, v160, v235
	v_fmac_f32_e32 v53, v160, v236
	v_fmac_f32_e32 v49, v160, v237
	v_fmac_f32_e32 v156, v154, v234
	v_fmac_f32_e32 v55, v154, v235
	v_fmac_f32_e32 v51, v154, v236
	v_fmac_f32_e32 v47, v154, v237
	ds_read_b128 v[234:237], v105 offset:22528
	s_waitcnt lgkmcnt(2)
	v_fmac_f32_e32 v224, v161, v242
	v_fmac_f32_e32 v223, v161, v243
	v_fmac_f32_e32 v221, v161, v244
	v_fmac_f32_e32 v217, v161, v245
	v_fmac_f32_e32 v225, v155, v242
	v_fmac_f32_e32 v222, v155, v243
	v_fmac_f32_e32 v219, v155, v244
	v_fmac_f32_e32 v215, v155, v245
	ds_read_b128 v[242:245], v105 offset:23552
	s_waitcnt lgkmcnt(2)
	v_fmac_f32_e32 v220, v161, v246
	v_fmac_f32_e32 v216, v161, v247
	v_fmac_f32_e32 v213, v161, v248
	v_fmac_f32_e32 v211, v161, v249
	v_fmac_f32_e32 v218, v155, v246
	v_fmac_f32_e32 v214, v155, v247
	v_fmac_f32_e32 v212, v155, v248
	v_fmac_f32_e32 v210, v155, v249
	ds_read_b128 v[246:249], v105 offset:24576
	s_waitcnt lgkmcnt(2)
	v_fmac_f32_e32 v209, v161, v234
	v_fmac_f32_e32 v207, v161, v235
	v_fmac_f32_e32 v205, v161, v236
	v_fmac_f32_e32 v153, v161, v237
	v_fmac_f32_e32 v208, v155, v234
	v_fmac_f32_e32 v206, v155, v235
	v_fmac_f32_e32 v158, v155, v236
	v_fmac_f32_e32 v57, v155, v237
	ds_read_b128 v[234:237], v105 offset:25600
	s_waitcnt lgkmcnt(2)
	v_fmac_f32_e32 v159, v161, v242
	v_fmac_f32_e32 v152, v161, v243
	v_fmac_f32_e32 v53, v161, v244
	v_fmac_f32_e32 v49, v161, v245
	v_fmac_f32_e32 v156, v155, v242
	v_fmac_f32_e32 v55, v155, v243
	v_fmac_f32_e32 v51, v155, v244
	v_fmac_f32_e32 v47, v155, v245
	ds_read_b128 v[242:245], v105 offset:26624
	s_waitcnt lgkmcnt(2)
	v_fmac_f32_e32 v224, v14, v246
	v_fmac_f32_e32 v223, v14, v247
	v_fmac_f32_e32 v221, v14, v248
	v_fmac_f32_e32 v217, v14, v249
	v_fmac_f32_e32 v225, v16, v246
	v_fmac_f32_e32 v222, v16, v247
	v_fmac_f32_e32 v219, v16, v248
	v_fmac_f32_e32 v215, v16, v249
	ds_read_b128 v[246:249], v105 offset:27648
	s_waitcnt lgkmcnt(2)
	v_fmac_f32_e32 v220, v14, v234
	v_fmac_f32_e32 v216, v14, v235
	v_fmac_f32_e32 v213, v14, v236
	v_fmac_f32_e32 v211, v14, v237
	v_fmac_f32_e32 v218, v16, v234
	v_fmac_f32_e32 v214, v16, v235
	v_fmac_f32_e32 v212, v16, v236
	v_fmac_f32_e32 v210, v16, v237
	ds_read_b128 v[234:237], v105 offset:28672
	s_waitcnt lgkmcnt(2)
	v_fmac_f32_e32 v209, v14, v242
	v_fmac_f32_e32 v207, v14, v243
	v_fmac_f32_e32 v205, v14, v244
	v_fmac_f32_e32 v153, v14, v245
	v_fmac_f32_e32 v208, v16, v242
	v_fmac_f32_e32 v206, v16, v243
	v_fmac_f32_e32 v158, v16, v244
	v_fmac_f32_e32 v57, v16, v245
	ds_read_b128 v[242:245], v105 offset:29696
	s_waitcnt lgkmcnt(2)
	v_fmac_f32_e32 v159, v14, v246
	v_fmac_f32_e32 v152, v14, v247
	v_fmac_f32_e32 v53, v14, v248
	v_fmac_f32_e32 v49, v14, v249
	v_fmac_f32_e32 v156, v16, v246
	v_fmac_f32_e32 v55, v16, v247
	v_fmac_f32_e32 v51, v16, v248
	v_fmac_f32_e32 v47, v16, v249
	ds_read_b128 v[246:249], v105 offset:30720
	s_waitcnt lgkmcnt(2)
	v_fmac_f32_e32 v224, v15, v234
	v_fmac_f32_e32 v223, v15, v235
	v_fmac_f32_e32 v221, v15, v236
	v_fmac_f32_e32 v217, v15, v237
	v_fmac_f32_e32 v225, v17, v234
	v_fmac_f32_e32 v222, v17, v235
	v_fmac_f32_e32 v219, v17, v236
	v_fmac_f32_e32 v215, v17, v237
	ds_read_b128 v[234:237], v105 offset:31744
	s_waitcnt lgkmcnt(2)
	v_fmac_f32_e32 v220, v15, v242
	v_fmac_f32_e32 v216, v15, v243
	v_fmac_f32_e32 v213, v15, v244
	v_fmac_f32_e32 v211, v15, v245
	v_fmac_f32_e32 v218, v17, v242
	v_fmac_f32_e32 v214, v17, v243
	v_fmac_f32_e32 v212, v17, v244
	v_fmac_f32_e32 v210, v17, v245
	ds_read_b128 v[242:245], v105 offset:32768
	s_waitcnt lgkmcnt(2)
	v_fmac_f32_e32 v57, v17, v249
	v_fmac_f32_e32 v209, v15, v246
	v_fmac_f32_e32 v207, v15, v247
	v_fmac_f32_e32 v205, v15, v248
	s_waitcnt lgkmcnt(1)
	v_fmac_f32_e32 v53, v15, v236
	v_fmac_f32_e32 v55, v17, v235
	v_fmac_f32_e32 v51, v17, v236
	v_fmac_f32_e32 v153, v15, v249
	v_fmac_f32_e32 v208, v17, v246
	v_fmac_f32_e32 v206, v17, v247
	v_fmac_f32_e32 v158, v17, v248
	ds_read_b128 v[246:249], v105 offset:33792
	v_fmac_f32_e32 v159, v15, v234
	v_fmac_f32_e32 v152, v15, v235
	v_fmac_f32_e32 v49, v15, v237
	v_fmac_f32_e32 v156, v17, v234
	v_fmac_f32_e32 v47, v17, v237
	ds_read_b128 v[234:237], v105 offset:34816
	s_waitcnt vmcnt(3)
	v_pk_add_f32 v[10:11], v[10:11], 1.0 op_sel_hi:[1,0]
	v_pk_mul_f32 v[142:143], v[102:103], v[142:143] op_sel_hi:[0,1]
	s_waitcnt vmcnt(2)
	v_pk_mul_f32 v[144:145], v[2:3], v[10:11]
	v_pk_add_f32 v[12:13], v[12:13], 1.0 op_sel_hi:[1,0]
	v_pk_fma_f32 v[146:147], v[142:143], v[144:145], v[6:7]
	v_pk_mul_f32 v[138:139], v[104:105], v[138:139] op_sel_hi:[0,1]
	v_pk_mul_f32 v[16:17], v[4:5], v[12:13]
	v_pk_mul_f32 v[14:15], v[102:103], v[140:141] op_sel_hi:[0,1]
	v_pk_mul_f32 v[136:137], v[104:105], v[136:137] op_sel_hi:[0,1]
	v_pk_fma_f32 v[144:145], v[138:139], v[144:145], v[6:7]
	v_med3_f32 v6, v146, s33, v233
	v_med3_f32 v7, v147, s33, v233
	v_mov_b32_e32 v140, 0
	v_pk_fma_f32 v[14:15], v[14:15], v[16:17], v[8:9]
	v_pk_fma_f32 v[16:17], v[136:137], v[16:17], v[8:9]
	v_cvt_pk_fp8_f32 v140, v6, v7
	v_med3_f32 v8, v144, s33, v233
	v_med3_f32 v9, v145, s33, v233
	v_mov_b32_e32 v141, 0
	v_cvt_pk_fp8_f32 v141, v8, v9
	v_med3_f32 v6, v14, s33, v233
	v_med3_f32 v7, v15, s33, v233
	v_cvt_pk_fp8_f32 v140, v6, v7 op_sel:[0,0,1]
	v_med3_f32 v6, v16, s33, v233
	v_med3_f32 v7, v17, s33, v233
	global_load_dwordx4 v[2:5], v[74:75], off
	global_load_dwordx4 v[10:13], v[76:77], off
	v_cvt_pk_fp8_f32 v141, v6, v7 op_sel:[0,0,1]
	global_load_dwordx4 v[6:9], v[32:33], off
	global_store_dword v[118:119], v140, off offset:512
	global_store_dword v[118:119], v141, off offset:2560
	s_waitcnt lgkmcnt(2)
	v_fmac_f32_e32 v224, v146, v242
	v_fmac_f32_e32 v223, v146, v243
	v_fmac_f32_e32 v221, v146, v244
	v_fmac_f32_e32 v217, v146, v245
	v_fmac_f32_e32 v225, v144, v242
	v_fmac_f32_e32 v222, v144, v243
	v_fmac_f32_e32 v219, v144, v244
	v_fmac_f32_e32 v215, v144, v245
	ds_read_b128 v[242:245], v105 offset:35840
	s_waitcnt lgkmcnt(2)
	v_fmac_f32_e32 v220, v146, v246
	v_fmac_f32_e32 v216, v146, v247
	v_fmac_f32_e32 v213, v146, v248
	v_fmac_f32_e32 v211, v146, v249
	v_fmac_f32_e32 v218, v144, v246
	v_fmac_f32_e32 v214, v144, v247
	v_fmac_f32_e32 v212, v144, v248
	v_fmac_f32_e32 v210, v144, v249
	ds_read_b128 v[246:249], v105 offset:36864
	s_waitcnt lgkmcnt(2)
	v_fmac_f32_e32 v209, v146, v234
	v_fmac_f32_e32 v207, v146, v235
	v_fmac_f32_e32 v205, v146, v236
	v_fmac_f32_e32 v153, v146, v237
	v_fmac_f32_e32 v208, v144, v234
	v_fmac_f32_e32 v206, v144, v235
	v_fmac_f32_e32 v158, v144, v236
	v_fmac_f32_e32 v57, v144, v237
	ds_read_b128 v[234:237], v105 offset:37888
	s_waitcnt lgkmcnt(2)
	v_fmac_f32_e32 v159, v146, v242
	v_fmac_f32_e32 v152, v146, v243
	v_fmac_f32_e32 v53, v146, v244
	v_fmac_f32_e32 v49, v146, v245
	v_fmac_f32_e32 v156, v144, v242
	v_fmac_f32_e32 v55, v144, v243
	v_fmac_f32_e32 v51, v144, v244
	v_fmac_f32_e32 v47, v144, v245
	ds_read_b128 v[242:245], v105 offset:38912
	s_waitcnt lgkmcnt(2)
	v_fmac_f32_e32 v224, v147, v246
	v_fmac_f32_e32 v223, v147, v247
	v_fmac_f32_e32 v221, v147, v248
	v_fmac_f32_e32 v217, v147, v249
	v_fmac_f32_e32 v225, v145, v246
	v_fmac_f32_e32 v222, v145, v247
	v_fmac_f32_e32 v219, v145, v248
	v_fmac_f32_e32 v215, v145, v249
	ds_read_b128 v[246:249], v105 offset:39936
	s_waitcnt lgkmcnt(2)
	v_fmac_f32_e32 v220, v147, v234
	v_fmac_f32_e32 v216, v147, v235
	v_fmac_f32_e32 v213, v147, v236
	v_fmac_f32_e32 v211, v147, v237
	v_fmac_f32_e32 v218, v145, v234
	v_fmac_f32_e32 v214, v145, v235
	v_fmac_f32_e32 v212, v145, v236
	v_fmac_f32_e32 v210, v145, v237
	ds_read_b128 v[234:237], v105 offset:40960
	s_waitcnt lgkmcnt(2)
	v_fmac_f32_e32 v209, v147, v242
	v_fmac_f32_e32 v207, v147, v243
	v_fmac_f32_e32 v205, v147, v244
	v_fmac_f32_e32 v153, v147, v245
	v_fmac_f32_e32 v208, v145, v242
	v_fmac_f32_e32 v206, v145, v243
	v_fmac_f32_e32 v158, v145, v244
	v_fmac_f32_e32 v57, v145, v245
	ds_read_b128 v[242:245], v105 offset:41984
	s_waitcnt lgkmcnt(2)
	v_fmac_f32_e32 v159, v147, v246
	v_fmac_f32_e32 v152, v147, v247
	v_fmac_f32_e32 v53, v147, v248
	v_fmac_f32_e32 v49, v147, v249
	v_fmac_f32_e32 v156, v145, v246
	v_fmac_f32_e32 v55, v145, v247
	v_fmac_f32_e32 v51, v145, v248
	v_fmac_f32_e32 v47, v145, v249
	ds_read_b128 v[246:249], v105 offset:43008
	s_waitcnt lgkmcnt(2)
	v_fmac_f32_e32 v224, v14, v234
	v_fmac_f32_e32 v223, v14, v235
	v_fmac_f32_e32 v221, v14, v236
	v_fmac_f32_e32 v217, v14, v237
	v_fmac_f32_e32 v225, v16, v234
	v_fmac_f32_e32 v222, v16, v235
	v_fmac_f32_e32 v219, v16, v236
	v_fmac_f32_e32 v215, v16, v237
	ds_read_b128 v[234:237], v105 offset:44032
	s_waitcnt lgkmcnt(2)
	v_fmac_f32_e32 v220, v14, v242
	v_fmac_f32_e32 v216, v14, v243
	v_fmac_f32_e32 v213, v14, v244
	v_fmac_f32_e32 v211, v14, v245
	v_fmac_f32_e32 v218, v16, v242
	v_fmac_f32_e32 v214, v16, v243
	v_fmac_f32_e32 v212, v16, v244
	v_fmac_f32_e32 v210, v16, v245
	ds_read_b128 v[242:245], v105 offset:45056
	s_waitcnt lgkmcnt(2)
	v_fmac_f32_e32 v209, v14, v246
	v_fmac_f32_e32 v207, v14, v247
	v_fmac_f32_e32 v205, v14, v248
	v_fmac_f32_e32 v153, v14, v249
	v_fmac_f32_e32 v208, v16, v246
	v_fmac_f32_e32 v206, v16, v247
	v_fmac_f32_e32 v158, v16, v248
	v_fmac_f32_e32 v57, v16, v249
	ds_read_b128 v[246:249], v105 offset:46080
	s_waitcnt lgkmcnt(2)
	v_fmac_f32_e32 v159, v14, v234
	v_fmac_f32_e32 v152, v14, v235
	v_fmac_f32_e32 v53, v14, v236
	v_fmac_f32_e32 v49, v14, v237
	v_fmac_f32_e32 v156, v16, v234
	v_fmac_f32_e32 v55, v16, v235
	v_fmac_f32_e32 v51, v16, v236
	v_fmac_f32_e32 v47, v16, v237
	ds_read_b128 v[234:237], v105 offset:47104
	s_waitcnt lgkmcnt(2)
	v_fmac_f32_e32 v224, v15, v242
	v_fmac_f32_e32 v223, v15, v243
	v_fmac_f32_e32 v221, v15, v244
	v_fmac_f32_e32 v217, v15, v245
	v_fmac_f32_e32 v225, v17, v242
	v_fmac_f32_e32 v222, v17, v243
	v_fmac_f32_e32 v219, v17, v244
	v_fmac_f32_e32 v215, v17, v245
	ds_read_b128 v[242:245], v105 offset:48128
	s_waitcnt lgkmcnt(2)
	v_fmac_f32_e32 v220, v15, v246
	v_fmac_f32_e32 v216, v15, v247
	v_fmac_f32_e32 v213, v15, v248
	v_fmac_f32_e32 v211, v15, v249
	v_fmac_f32_e32 v218, v17, v246
	v_fmac_f32_e32 v214, v17, v247
	v_fmac_f32_e32 v212, v17, v248
	v_fmac_f32_e32 v210, v17, v249
	ds_read_b128 v[246:249], v105 offset:49152
	s_waitcnt lgkmcnt(2)
	v_fmac_f32_e32 v57, v17, v237
	v_fmac_f32_e32 v209, v15, v234
	v_fmac_f32_e32 v207, v15, v235
	v_fmac_f32_e32 v205, v15, v236
	s_waitcnt lgkmcnt(1)
	v_fmac_f32_e32 v53, v15, v244
	v_fmac_f32_e32 v55, v17, v243
	v_fmac_f32_e32 v51, v17, v244
	v_fmac_f32_e32 v153, v15, v237
	v_fmac_f32_e32 v208, v17, v234
	v_fmac_f32_e32 v206, v17, v235
	v_fmac_f32_e32 v158, v17, v236
	ds_read_b128 v[234:237], v105 offset:50176
	v_fmac_f32_e32 v159, v15, v242
	v_fmac_f32_e32 v152, v15, v243
	v_fmac_f32_e32 v49, v15, v245
	v_fmac_f32_e32 v156, v17, v242
	v_fmac_f32_e32 v47, v17, v245
	ds_read_b128 v[242:245], v105 offset:51200
	s_waitcnt vmcnt(3)
	v_pk_add_f32 v[10:11], v[10:11], 1.0 op_sel_hi:[1,0]
	v_pk_mul_f32 v[130:131], v[102:103], v[130:131] op_sel_hi:[0,1]
	s_waitcnt vmcnt(2)
	v_pk_mul_f32 v[136:137], v[6:7], v[10:11]
	v_pk_add_f32 v[12:13], v[12:13], 1.0 op_sel_hi:[1,0]
	v_pk_mul_f32 v[14:15], v[102:103], v[128:129] op_sel_hi:[0,1]
	v_pk_fma_f32 v[138:139], v[130:131], v[136:137], v[2:3]
	v_pk_mul_f32 v[128:129], v[104:105], v[132:133] op_sel_hi:[0,1]
	v_pk_mul_f32 v[16:17], v[8:9], v[12:13]
	v_pk_mul_f32 v[130:131], v[104:105], v[134:135] op_sel_hi:[0,1]
	v_pk_fma_f32 v[136:137], v[128:129], v[136:137], v[2:3]
	v_med3_f32 v2, v138, s33, v233
	v_med3_f32 v3, v139, s33, v233
	v_mov_b32_e32 v132, 0
	v_pk_fma_f32 v[14:15], v[14:15], v[16:17], v[4:5]
	v_pk_fma_f32 v[16:17], v[130:131], v[16:17], v[4:5]
	v_cvt_pk_fp8_f32 v132, v2, v3
	v_med3_f32 v4, v136, s33, v233
	v_med3_f32 v5, v137, s33, v233
	v_mov_b32_e32 v133, 0
	v_cvt_pk_fp8_f32 v133, v4, v5
	v_med3_f32 v2, v14, s33, v233
	v_med3_f32 v3, v15, s33, v233
	v_cvt_pk_fp8_f32 v132, v2, v3 op_sel:[0,0,1]
	v_med3_f32 v2, v16, s33, v233
	v_med3_f32 v3, v17, s33, v233
	global_load_dwordx4 v[10:13], v[78:79], off
	global_load_dwordx4 v[6:9], v[80:81], off
	v_cvt_pk_fp8_f32 v133, v2, v3 op_sel:[0,0,1]
	global_load_dwordx4 v[2:5], v[34:35], off
	global_store_dword v[118:119], v132, off offset:768
	global_store_dword v[118:119], v133, off offset:2816
	s_waitcnt lgkmcnt(2)
	v_fmac_f32_e32 v224, v138, v246
	v_fmac_f32_e32 v223, v138, v247
	v_fmac_f32_e32 v221, v138, v248
	v_fmac_f32_e32 v217, v138, v249
	v_fmac_f32_e32 v225, v136, v246
	v_fmac_f32_e32 v222, v136, v247
	v_fmac_f32_e32 v219, v136, v248
	v_fmac_f32_e32 v215, v136, v249
	ds_read_b128 v[246:249], v105 offset:52224
	s_waitcnt lgkmcnt(2)
	v_fmac_f32_e32 v220, v138, v234
	v_fmac_f32_e32 v216, v138, v235
	v_fmac_f32_e32 v213, v138, v236
	v_fmac_f32_e32 v211, v138, v237
	v_fmac_f32_e32 v218, v136, v234
	v_fmac_f32_e32 v214, v136, v235
	v_fmac_f32_e32 v212, v136, v236
	v_fmac_f32_e32 v210, v136, v237
	ds_read_b128 v[234:237], v105 offset:53248
	s_waitcnt lgkmcnt(2)
	v_fmac_f32_e32 v209, v138, v242
	v_fmac_f32_e32 v207, v138, v243
	v_fmac_f32_e32 v205, v138, v244
	v_fmac_f32_e32 v153, v138, v245
	v_fmac_f32_e32 v208, v136, v242
	v_fmac_f32_e32 v206, v136, v243
	v_fmac_f32_e32 v158, v136, v244
	v_fmac_f32_e32 v57, v136, v245
	ds_read_b128 v[242:245], v105 offset:54272
	s_waitcnt lgkmcnt(2)
	v_fmac_f32_e32 v159, v138, v246
	v_fmac_f32_e32 v152, v138, v247
	v_fmac_f32_e32 v53, v138, v248
	v_fmac_f32_e32 v49, v138, v249
	v_fmac_f32_e32 v156, v136, v246
	v_fmac_f32_e32 v55, v136, v247
	v_fmac_f32_e32 v51, v136, v248
	v_fmac_f32_e32 v47, v136, v249
	ds_read_b128 v[246:249], v105 offset:55296
	s_waitcnt lgkmcnt(2)
	v_fmac_f32_e32 v224, v139, v234
	v_fmac_f32_e32 v223, v139, v235
	v_fmac_f32_e32 v221, v139, v236
	v_fmac_f32_e32 v217, v139, v237
	v_fmac_f32_e32 v225, v137, v234
	v_fmac_f32_e32 v222, v137, v235
	v_fmac_f32_e32 v219, v137, v236
	v_fmac_f32_e32 v215, v137, v237
	ds_read_b128 v[234:237], v105 offset:56320
	s_waitcnt lgkmcnt(2)
	v_fmac_f32_e32 v220, v139, v242
	v_fmac_f32_e32 v216, v139, v243
	v_fmac_f32_e32 v213, v139, v244
	v_fmac_f32_e32 v211, v139, v245
	v_fmac_f32_e32 v218, v137, v242
	v_fmac_f32_e32 v214, v137, v243
	v_fmac_f32_e32 v212, v137, v244
	v_fmac_f32_e32 v210, v137, v245
	ds_read_b128 v[242:245], v105 offset:57344
	s_waitcnt lgkmcnt(2)
	v_fmac_f32_e32 v209, v139, v246
	v_fmac_f32_e32 v207, v139, v247
	v_fmac_f32_e32 v205, v139, v248
	v_fmac_f32_e32 v153, v139, v249
	v_fmac_f32_e32 v208, v137, v246
	v_fmac_f32_e32 v206, v137, v247
	v_fmac_f32_e32 v158, v137, v248
	v_fmac_f32_e32 v57, v137, v249
	ds_read_b128 v[246:249], v105 offset:58368
	s_waitcnt lgkmcnt(2)
	v_fmac_f32_e32 v159, v139, v234
	v_fmac_f32_e32 v152, v139, v235
	v_fmac_f32_e32 v53, v139, v236
	v_fmac_f32_e32 v49, v139, v237
	v_fmac_f32_e32 v156, v137, v234
	v_fmac_f32_e32 v55, v137, v235
	v_fmac_f32_e32 v51, v137, v236
	v_fmac_f32_e32 v47, v137, v237
	ds_read_b128 v[234:237], v105 offset:59392
	s_waitcnt lgkmcnt(2)
	v_fmac_f32_e32 v224, v14, v242
	v_fmac_f32_e32 v223, v14, v243
	v_fmac_f32_e32 v221, v14, v244
	v_fmac_f32_e32 v217, v14, v245
	v_fmac_f32_e32 v225, v16, v242
	v_fmac_f32_e32 v222, v16, v243
	v_fmac_f32_e32 v219, v16, v244
	v_fmac_f32_e32 v215, v16, v245
	ds_read_b128 v[242:245], v105 offset:60416
	s_waitcnt lgkmcnt(2)
	v_fmac_f32_e32 v220, v14, v246
	v_fmac_f32_e32 v216, v14, v247
	v_fmac_f32_e32 v213, v14, v248
	v_fmac_f32_e32 v211, v14, v249
	v_fmac_f32_e32 v218, v16, v246
	v_fmac_f32_e32 v214, v16, v247
	v_fmac_f32_e32 v212, v16, v248
	v_fmac_f32_e32 v210, v16, v249
	ds_read_b128 v[246:249], v105 offset:61440
	s_waitcnt lgkmcnt(2)
	v_fmac_f32_e32 v209, v14, v234
	v_fmac_f32_e32 v207, v14, v235
	v_fmac_f32_e32 v205, v14, v236
	v_fmac_f32_e32 v153, v14, v237
	v_fmac_f32_e32 v208, v16, v234
	v_fmac_f32_e32 v206, v16, v235
	v_fmac_f32_e32 v158, v16, v236
	v_fmac_f32_e32 v57, v16, v237
	ds_read_b128 v[234:237], v105 offset:62464
	s_waitcnt lgkmcnt(2)
	v_fmac_f32_e32 v159, v14, v242
	v_fmac_f32_e32 v152, v14, v243
	v_fmac_f32_e32 v53, v14, v244
	v_fmac_f32_e32 v49, v14, v245
	v_fmac_f32_e32 v156, v16, v242
	v_fmac_f32_e32 v55, v16, v243
	v_fmac_f32_e32 v51, v16, v244
	v_fmac_f32_e32 v47, v16, v245
	ds_read_b128 v[242:245], v105 offset:63488
	s_waitcnt lgkmcnt(2)
	v_fmac_f32_e32 v224, v15, v246
	v_fmac_f32_e32 v223, v15, v247
	v_fmac_f32_e32 v221, v15, v248
	v_fmac_f32_e32 v217, v15, v249
	v_fmac_f32_e32 v225, v17, v246
	v_fmac_f32_e32 v222, v17, v247
	v_fmac_f32_e32 v219, v17, v248
	v_fmac_f32_e32 v215, v17, v249
	ds_read_b128 v[246:249], v105 offset:64512
	s_waitcnt lgkmcnt(2)
	v_fmac_f32_e32 v220, v15, v234
	v_fmac_f32_e32 v216, v15, v235
	v_fmac_f32_e32 v213, v15, v236
	v_fmac_f32_e32 v211, v15, v237
	v_fmac_f32_e32 v218, v17, v234
	v_fmac_f32_e32 v214, v17, v235
	v_fmac_f32_e32 v212, v17, v236
	v_fmac_f32_e32 v210, v17, v237
	s_waitcnt lgkmcnt(1)
	v_fmac_f32_e32 v57, v17, v245
	v_fmac_f32_e32 v209, v15, v242
	v_fmac_f32_e32 v207, v15, v243
	v_fmac_f32_e32 v205, v15, v244
	s_waitcnt lgkmcnt(0)
	v_fmac_f32_e32 v53, v15, v248
	v_fmac_f32_e32 v55, v17, v247
	v_fmac_f32_e32 v51, v17, v248
	v_fmac_f32_e32 v153, v15, v245
	v_fmac_f32_e32 v208, v17, v242
	v_fmac_f32_e32 v206, v17, v243
	v_fmac_f32_e32 v158, v17, v244
	v_fmac_f32_e32 v159, v15, v246
	v_fmac_f32_e32 v152, v15, v247
	v_fmac_f32_e32 v49, v15, v249
	v_fmac_f32_e32 v156, v17, v246
	v_fmac_f32_e32 v47, v17, v249
	s_waitcnt vmcnt(3)
	v_pk_add_f32 v[6:7], v[6:7], 1.0 op_sel_hi:[1,0]
	v_pk_mul_f32 v[126:127], v[102:103], v[126:127] op_sel_hi:[0,1]
	s_waitcnt vmcnt(2)
	v_pk_mul_f32 v[128:129], v[2:3], v[6:7]
	v_pk_add_f32 v[8:9], v[8:9], 1.0 op_sel_hi:[1,0]
	v_pk_fma_f32 v[130:131], v[126:127], v[128:129], v[10:11]
	v_pk_mul_f32 v[122:123], v[104:105], v[122:123] op_sel_hi:[0,1]
	v_pk_mul_f32 v[16:17], v[4:5], v[8:9]
	v_pk_mul_f32 v[14:15], v[102:103], v[124:125] op_sel_hi:[0,1]
	v_pk_mul_f32 v[120:121], v[104:105], v[120:121] op_sel_hi:[0,1]
	v_pk_fma_f32 v[128:129], v[122:123], v[128:129], v[10:11]
	v_med3_f32 v10, v130, s33, v233
	v_med3_f32 v11, v131, s33, v233
	v_mov_b32_e32 v124, 0
	v_pk_fma_f32 v[14:15], v[14:15], v[16:17], v[12:13]
	v_pk_fma_f32 v[16:17], v[120:121], v[16:17], v[12:13]
	v_cvt_pk_fp8_f32 v124, v10, v11
	v_med3_f32 v12, v128, s33, v233
	v_med3_f32 v13, v129, s33, v233
	v_mov_b32_e32 v125, 0
	v_cvt_pk_fp8_f32 v125, v12, v13
	v_med3_f32 v10, v14, s33, v233
	v_med3_f32 v11, v15, s33, v233
	v_cvt_pk_fp8_f32 v124, v10, v11 op_sel:[0,0,1]
	v_med3_f32 v10, v16, s33, v233
	v_med3_f32 v11, v17, s33, v233
	global_load_dwordx4 v[6:9], v[82:83], off
	global_load_dwordx4 v[2:5], v[84:85], off
	v_cvt_pk_fp8_f32 v125, v10, v11 op_sel:[0,0,1]
	v_add_u32_e32 v10, 0x10000, v105
	ds_read_b128 v[120:123], v10
	global_load_dwordx4 v[10:13], v[36:37], off
	s_nop 0
	global_store_dword v[118:119], v124, off offset:1024
	global_store_dword v[118:119], v125, off offset:3072
	v_add_u32_e32 v124, 0x10400, v105
	ds_read_b128 v[124:127], v124
	s_waitcnt lgkmcnt(1)
	v_fmac_f32_e32 v224, v130, v120
	v_fmac_f32_e32 v225, v128, v120
	v_add_u32_e32 v120, 0x10800, v105
	v_fmac_f32_e32 v223, v130, v121
	v_fmac_f32_e32 v221, v130, v122
	v_fmac_f32_e32 v217, v130, v123
	v_fmac_f32_e32 v222, v128, v121
	v_fmac_f32_e32 v219, v128, v122
	v_fmac_f32_e32 v215, v128, v123
	ds_read_b128 v[120:123], v120
	s_waitcnt lgkmcnt(1)
	v_fmac_f32_e32 v220, v130, v124
	v_fmac_f32_e32 v218, v128, v124
	v_add_u32_e32 v124, 0x10c00, v105
	v_fmac_f32_e32 v216, v130, v125
	v_fmac_f32_e32 v213, v130, v126
	v_fmac_f32_e32 v211, v130, v127
	v_fmac_f32_e32 v214, v128, v125
	v_fmac_f32_e32 v212, v128, v126
	v_fmac_f32_e32 v210, v128, v127
	ds_read_b128 v[124:127], v124
	s_waitcnt lgkmcnt(1)
	v_fmac_f32_e32 v209, v130, v120
	v_fmac_f32_e32 v208, v128, v120
	v_add_u32_e32 v120, 0x11000, v105
	v_fmac_f32_e32 v207, v130, v121
	v_fmac_f32_e32 v205, v130, v122
	v_fmac_f32_e32 v153, v130, v123
	v_fmac_f32_e32 v206, v128, v121
	v_fmac_f32_e32 v158, v128, v122
	v_fmac_f32_e32 v57, v128, v123
	ds_read_b128 v[120:123], v120
	s_waitcnt lgkmcnt(1)
	v_fmac_f32_e32 v159, v130, v124
	v_fmac_f32_e32 v156, v128, v124
	v_add_u32_e32 v124, 0x11400, v105
	v_fmac_f32_e32 v152, v130, v125
	v_fmac_f32_e32 v53, v130, v126
	v_fmac_f32_e32 v49, v130, v127
	v_fmac_f32_e32 v55, v128, v125
	v_fmac_f32_e32 v51, v128, v126
	v_fmac_f32_e32 v47, v128, v127
	ds_read_b128 v[124:127], v124
	s_waitcnt lgkmcnt(1)
	v_fmac_f32_e32 v224, v131, v120
	v_fmac_f32_e32 v225, v129, v120
	v_add_u32_e32 v120, 0x11800, v105
	v_fmac_f32_e32 v223, v131, v121
	v_fmac_f32_e32 v221, v131, v122
	v_fmac_f32_e32 v217, v131, v123
	v_fmac_f32_e32 v222, v129, v121
	v_fmac_f32_e32 v219, v129, v122
	v_fmac_f32_e32 v215, v129, v123
	ds_read_b128 v[120:123], v120
	s_waitcnt lgkmcnt(1)
	v_fmac_f32_e32 v220, v131, v124
	v_fmac_f32_e32 v218, v129, v124
	v_add_u32_e32 v124, 0x11c00, v105
	v_fmac_f32_e32 v216, v131, v125
	v_fmac_f32_e32 v213, v131, v126
	v_fmac_f32_e32 v211, v131, v127
	v_fmac_f32_e32 v214, v129, v125
	v_fmac_f32_e32 v212, v129, v126
	v_fmac_f32_e32 v210, v129, v127
	ds_read_b128 v[124:127], v124
	s_waitcnt lgkmcnt(1)
	v_fmac_f32_e32 v209, v131, v120
	v_fmac_f32_e32 v208, v129, v120
	v_add_u32_e32 v120, 0x12000, v105
	v_fmac_f32_e32 v207, v131, v121
	v_fmac_f32_e32 v205, v131, v122
	v_fmac_f32_e32 v153, v131, v123
	v_fmac_f32_e32 v206, v129, v121
	v_fmac_f32_e32 v158, v129, v122
	v_fmac_f32_e32 v57, v129, v123
	ds_read_b128 v[120:123], v120
	s_waitcnt lgkmcnt(1)
	v_fmac_f32_e32 v159, v131, v124
	v_fmac_f32_e32 v156, v129, v124
	v_add_u32_e32 v124, 0x12400, v105
	v_fmac_f32_e32 v152, v131, v125
	v_fmac_f32_e32 v53, v131, v126
	v_fmac_f32_e32 v49, v131, v127
	v_fmac_f32_e32 v55, v129, v125
	v_fmac_f32_e32 v51, v129, v126
	v_fmac_f32_e32 v47, v129, v127
	ds_read_b128 v[124:127], v124
	s_waitcnt lgkmcnt(1)
	v_fmac_f32_e32 v224, v14, v120
	v_fmac_f32_e32 v225, v16, v120
	v_add_u32_e32 v120, 0x12800, v105
	v_fmac_f32_e32 v223, v14, v121
	v_fmac_f32_e32 v221, v14, v122
	v_fmac_f32_e32 v217, v14, v123
	v_fmac_f32_e32 v222, v16, v121
	v_fmac_f32_e32 v219, v16, v122
	v_fmac_f32_e32 v215, v16, v123
	ds_read_b128 v[120:123], v120
	s_waitcnt lgkmcnt(1)
	v_fmac_f32_e32 v220, v14, v124
	v_fmac_f32_e32 v218, v16, v124
	v_add_u32_e32 v124, 0x12c00, v105
	v_fmac_f32_e32 v216, v14, v125
	v_fmac_f32_e32 v213, v14, v126
	v_fmac_f32_e32 v211, v14, v127
	v_fmac_f32_e32 v214, v16, v125
	v_fmac_f32_e32 v212, v16, v126
	v_fmac_f32_e32 v210, v16, v127
	ds_read_b128 v[124:127], v124
	s_waitcnt lgkmcnt(1)
	v_fmac_f32_e32 v209, v14, v120
	v_fmac_f32_e32 v207, v14, v121
	v_fmac_f32_e32 v205, v14, v122
	v_fmac_f32_e32 v153, v14, v123
	s_waitcnt lgkmcnt(0)
	v_fmac_f32_e32 v159, v14, v124
	v_fmac_f32_e32 v152, v14, v125
	v_fmac_f32_e32 v53, v14, v126
	v_fmac_f32_e32 v49, v14, v127
	v_add_u32_e32 v14, 0x13000, v105
	v_fmac_f32_e32 v208, v16, v120
	v_fmac_f32_e32 v206, v16, v121
	v_fmac_f32_e32 v158, v16, v122
	v_fmac_f32_e32 v57, v16, v123
	ds_read_b128 v[120:123], v14
	v_add_u32_e32 v14, 0x13400, v105
	v_fmac_f32_e32 v156, v16, v124
	v_fmac_f32_e32 v55, v16, v125
	v_fmac_f32_e32 v51, v16, v126
	v_fmac_f32_e32 v47, v16, v127
	ds_read_b128 v[124:127], v14
	v_add_u32_e32 v14, 0x13800, v105
	s_waitcnt lgkmcnt(1)
	v_fmac_f32_e32 v224, v15, v120
	v_fmac_f32_e32 v223, v15, v121
	v_fmac_f32_e32 v221, v15, v122
	v_fmac_f32_e32 v217, v15, v123
	v_fmac_f32_e32 v225, v17, v120
	v_fmac_f32_e32 v222, v17, v121
	v_fmac_f32_e32 v219, v17, v122
	v_fmac_f32_e32 v215, v17, v123
	ds_read_b128 v[120:123], v14
	v_add_u32_e32 v14, 0x13c00, v105
	s_waitcnt lgkmcnt(1)
	v_fmac_f32_e32 v220, v15, v124
	v_fmac_f32_e32 v216, v15, v125
	v_fmac_f32_e32 v213, v15, v126
	v_fmac_f32_e32 v211, v15, v127
	v_fmac_f32_e32 v218, v17, v124
	v_fmac_f32_e32 v214, v17, v125
	v_fmac_f32_e32 v212, v17, v126
	v_fmac_f32_e32 v210, v17, v127
	ds_read_b128 v[124:127], v14
	s_waitcnt lgkmcnt(1)
	v_fmac_f32_e32 v57, v17, v123
	v_fmac_f32_e32 v209, v15, v120
	v_fmac_f32_e32 v207, v15, v121
	v_fmac_f32_e32 v205, v15, v122
	s_waitcnt lgkmcnt(0)
	v_fmac_f32_e32 v53, v15, v126
	v_fmac_f32_e32 v55, v17, v125
	v_fmac_f32_e32 v51, v17, v126
	v_fmac_f32_e32 v153, v15, v123
	v_fmac_f32_e32 v208, v17, v120
	v_fmac_f32_e32 v206, v17, v121
	v_fmac_f32_e32 v158, v17, v122
	v_fmac_f32_e32 v159, v15, v124
	v_fmac_f32_e32 v152, v15, v125
	v_fmac_f32_e32 v49, v15, v127
	v_fmac_f32_e32 v156, v17, v124
	v_fmac_f32_e32 v47, v17, v127
	s_waitcnt vmcnt(3)
	v_pk_add_f32 v[2:3], v[2:3], 1.0 op_sel_hi:[1,0]
	v_pk_mul_f32 v[116:117], v[102:103], v[116:117] op_sel_hi:[0,1]
	s_waitcnt vmcnt(2)
	v_pk_mul_f32 v[120:121], v[10:11], v[2:3]
	v_pk_add_f32 v[4:5], v[4:5], 1.0 op_sel_hi:[1,0]
	v_pk_fma_f32 v[122:123], v[116:117], v[120:121], v[6:7]
	v_pk_mul_f32 v[112:113], v[104:105], v[112:113] op_sel_hi:[0,1]
	v_pk_mul_f32 v[16:17], v[12:13], v[4:5]
	v_pk_mul_f32 v[14:15], v[102:103], v[114:115] op_sel_hi:[0,1]
	v_pk_mul_f32 v[110:111], v[104:105], v[110:111] op_sel_hi:[0,1]
	v_pk_fma_f32 v[120:121], v[112:113], v[120:121], v[6:7]
	v_med3_f32 v6, v122, s33, v233
	v_med3_f32 v7, v123, s33, v233
	v_mov_b32_e32 v114, 0
	v_pk_fma_f32 v[14:15], v[14:15], v[16:17], v[8:9]
	v_pk_fma_f32 v[16:17], v[110:111], v[16:17], v[8:9]
	v_cvt_pk_fp8_f32 v114, v6, v7
	v_med3_f32 v8, v120, s33, v233
	v_med3_f32 v9, v121, s33, v233
	v_mov_b32_e32 v115, 0
	v_cvt_pk_fp8_f32 v115, v8, v9
	v_med3_f32 v6, v14, s33, v233
	v_med3_f32 v7, v15, s33, v233
	v_cvt_pk_fp8_f32 v114, v6, v7 op_sel:[0,0,1]
	v_med3_f32 v6, v16, s33, v233
	v_med3_f32 v7, v17, s33, v233
	v_cvt_pk_fp8_f32 v115, v6, v7 op_sel:[0,0,1]
	v_add_u32_e32 v6, 0x14000, v105
	global_load_dwordx4 v[2:5], v[86:87], off
	global_load_dwordx4 v[10:13], v[88:89], off
	ds_read_b128 v[110:113], v6
	global_load_dwordx4 v[6:9], v[38:39], off
	s_nop 0
	global_store_dword v[118:119], v114, off offset:1280
	global_store_dword v[118:119], v115, off offset:3328
	v_add_u32_e32 v114, 0x14400, v105
	ds_read_b128 v[114:117], v114
	s_waitcnt lgkmcnt(1)
	v_fmac_f32_e32 v224, v122, v110
	v_fmac_f32_e32 v225, v120, v110
	v_add_u32_e32 v110, 0x14800, v105
	v_fmac_f32_e32 v223, v122, v111
	v_fmac_f32_e32 v221, v122, v112
	v_fmac_f32_e32 v217, v122, v113
	v_fmac_f32_e32 v222, v120, v111
	v_fmac_f32_e32 v219, v120, v112
	v_fmac_f32_e32 v215, v120, v113
	ds_read_b128 v[110:113], v110
	s_waitcnt lgkmcnt(1)
	v_fmac_f32_e32 v220, v122, v114
	v_fmac_f32_e32 v218, v120, v114
	v_add_u32_e32 v114, 0x14c00, v105
	v_fmac_f32_e32 v216, v122, v115
	v_fmac_f32_e32 v213, v122, v116
	v_fmac_f32_e32 v211, v122, v117
	v_fmac_f32_e32 v214, v120, v115
	v_fmac_f32_e32 v212, v120, v116
	v_fmac_f32_e32 v210, v120, v117
	ds_read_b128 v[114:117], v114
	s_waitcnt lgkmcnt(1)
	v_fmac_f32_e32 v209, v122, v110
	v_fmac_f32_e32 v208, v120, v110
	v_add_u32_e32 v110, 0x15000, v105
	v_fmac_f32_e32 v207, v122, v111
	v_fmac_f32_e32 v205, v122, v112
	v_fmac_f32_e32 v153, v122, v113
	v_fmac_f32_e32 v206, v120, v111
	v_fmac_f32_e32 v158, v120, v112
	v_fmac_f32_e32 v57, v120, v113
	ds_read_b128 v[110:113], v110
	s_waitcnt lgkmcnt(1)
	v_fmac_f32_e32 v159, v122, v114
	v_fmac_f32_e32 v152, v122, v115
	v_fmac_f32_e32 v53, v122, v116
	v_fmac_f32_e32 v49, v122, v117
	v_fmac_f32_e32 v156, v120, v114
	v_fmac_f32_e32 v55, v120, v115
	v_fmac_f32_e32 v51, v120, v116
	v_fmac_f32_e32 v47, v120, v117
	ds_read_b128 v[114:117], v230
	s_waitcnt lgkmcnt(1)
	v_fmac_f32_e32 v224, v123, v110
	v_fmac_f32_e32 v223, v123, v111
	v_fmac_f32_e32 v221, v123, v112
	v_fmac_f32_e32 v217, v123, v113
	v_fmac_f32_e32 v225, v121, v110
	v_fmac_f32_e32 v222, v121, v111
	v_fmac_f32_e32 v219, v121, v112
	v_fmac_f32_e32 v215, v121, v113
	ds_read_b128 v[110:113], v250
	s_waitcnt lgkmcnt(1)
	v_fmac_f32_e32 v220, v123, v114
	v_fmac_f32_e32 v216, v123, v115
	v_fmac_f32_e32 v213, v123, v116
	v_fmac_f32_e32 v211, v123, v117
	v_fmac_f32_e32 v218, v121, v114
	v_fmac_f32_e32 v214, v121, v115
	v_fmac_f32_e32 v212, v121, v116
	v_fmac_f32_e32 v210, v121, v117
	ds_read_b128 v[114:117], v251
	s_waitcnt lgkmcnt(1)
	v_fmac_f32_e32 v209, v123, v110
	v_fmac_f32_e32 v207, v123, v111
	v_fmac_f32_e32 v205, v123, v112
	v_fmac_f32_e32 v153, v123, v113
	v_fmac_f32_e32 v208, v121, v110
	v_fmac_f32_e32 v206, v121, v111
	v_fmac_f32_e32 v158, v121, v112
	v_fmac_f32_e32 v57, v121, v113
	s_waitcnt lgkmcnt(0)
	v_fmac_f32_e32 v159, v123, v114
	v_fmac_f32_e32 v152, v123, v115
	v_fmac_f32_e32 v53, v123, v116
	v_fmac_f32_e32 v49, v123, v117
	v_fmac_f32_e32 v156, v121, v114
	ds_read_b128 v[110:113], v164
	v_fmac_f32_e32 v55, v121, v115
	v_fmac_f32_e32 v51, v121, v116
	v_fmac_f32_e32 v47, v121, v117
	ds_read_b128 v[114:117], v165
	s_waitcnt lgkmcnt(1)
	v_fmac_f32_e32 v224, v14, v110
	v_fmac_f32_e32 v223, v14, v111
	v_fmac_f32_e32 v221, v14, v112
	v_fmac_f32_e32 v217, v14, v113
	v_fmac_f32_e32 v225, v16, v110
	v_fmac_f32_e32 v222, v16, v111
	v_fmac_f32_e32 v219, v16, v112
	v_fmac_f32_e32 v215, v16, v113
	s_waitcnt lgkmcnt(0)
	v_fmac_f32_e32 v220, v14, v114
	v_fmac_f32_e32 v216, v14, v115
	v_fmac_f32_e32 v213, v14, v116
	v_fmac_f32_e32 v211, v14, v117
	v_fmac_f32_e32 v218, v16, v114
	ds_read_b128 v[110:113], v166
	v_fmac_f32_e32 v214, v16, v115
	v_fmac_f32_e32 v212, v16, v116
	v_fmac_f32_e32 v210, v16, v117
	ds_read_b128 v[114:117], v167
	s_waitcnt lgkmcnt(1)
	v_fmac_f32_e32 v209, v14, v110
	v_fmac_f32_e32 v207, v14, v111
	v_fmac_f32_e32 v205, v14, v112
	v_fmac_f32_e32 v153, v14, v113
	v_fmac_f32_e32 v208, v16, v110
	v_fmac_f32_e32 v206, v16, v111
	v_fmac_f32_e32 v158, v16, v112
	v_fmac_f32_e32 v57, v16, v113
	s_waitcnt lgkmcnt(0)
	v_fmac_f32_e32 v159, v14, v114
	v_fmac_f32_e32 v152, v14, v115
	v_fmac_f32_e32 v53, v14, v116
	v_fmac_f32_e32 v49, v14, v117
	v_fmac_f32_e32 v156, v16, v114
	ds_read_b128 v[110:113], v168
	v_fmac_f32_e32 v55, v16, v115
	v_fmac_f32_e32 v51, v16, v116
	v_fmac_f32_e32 v47, v16, v117
	ds_read_b128 v[114:117], v169
	s_waitcnt lgkmcnt(1)
	v_fmac_f32_e32 v224, v15, v110
	v_fmac_f32_e32 v223, v15, v111
	v_fmac_f32_e32 v221, v15, v112
	v_fmac_f32_e32 v217, v15, v113
	v_fmac_f32_e32 v225, v17, v110
	v_fmac_f32_e32 v222, v17, v111
	v_fmac_f32_e32 v219, v17, v112
	v_fmac_f32_e32 v215, v17, v113
	s_waitcnt lgkmcnt(0)
	v_fmac_f32_e32 v220, v15, v114
	v_fmac_f32_e32 v216, v15, v115
	v_fmac_f32_e32 v213, v15, v116
	v_fmac_f32_e32 v211, v15, v117
	v_fmac_f32_e32 v218, v17, v114
	ds_read_b128 v[110:113], v170
	v_fmac_f32_e32 v214, v17, v115
	v_fmac_f32_e32 v212, v17, v116
	v_fmac_f32_e32 v210, v17, v117
	ds_read_b128 v[114:117], v171
	s_waitcnt lgkmcnt(1)
	v_fmac_f32_e32 v57, v17, v113
	v_fmac_f32_e32 v209, v15, v110
	v_fmac_f32_e32 v207, v15, v111
	v_fmac_f32_e32 v205, v15, v112
	s_waitcnt lgkmcnt(0)
	v_fmac_f32_e32 v53, v15, v116
	v_fmac_f32_e32 v55, v17, v115
	v_fmac_f32_e32 v51, v17, v116
	v_fmac_f32_e32 v153, v15, v113
	v_fmac_f32_e32 v208, v17, v110
	v_fmac_f32_e32 v206, v17, v111
	v_fmac_f32_e32 v158, v17, v112
	v_fmac_f32_e32 v159, v15, v114
	v_fmac_f32_e32 v152, v15, v115
	v_fmac_f32_e32 v49, v15, v117
	v_fmac_f32_e32 v156, v17, v114
	v_fmac_f32_e32 v47, v17, v117
	s_waitcnt vmcnt(3)
	v_pk_add_f32 v[12:13], v[12:13], 1.0 op_sel_hi:[1,0]
	v_pk_add_f32 v[10:11], v[10:11], 1.0 op_sel_hi:[1,0]
	s_waitcnt vmcnt(2)
	v_pk_mul_f32 v[12:13], v[8:9], v[12:13]
	v_pk_mul_f32 v[10:11], v[6:7], v[10:11]
	global_load_dwordx4 v[6:9], v[90:91], off
	global_load_dwordx4 v[114:117], v[92:93], off
	global_load_dwordx4 v[120:123], v[40:41], off
	v_pk_mul_f32 v[14:15], v[102:103], v[108:109] op_sel_hi:[0,1]
	v_pk_mul_f32 v[16:17], v[102:103], v[106:107] op_sel_hi:[0,1]
	v_pk_fma_f32 v[106:107], v[16:17], v[12:13], v[4:5]
	v_pk_fma_f32 v[108:109], v[14:15], v[10:11], v[2:3]
	v_pk_mul_f32 v[14:15], v[104:105], v[20:21] op_sel_hi:[0,1]
	v_pk_mul_f32 v[16:17], v[104:105], v[18:19] op_sel_hi:[0,1]
	v_pk_fma_f32 v[110:111], v[16:17], v[12:13], v[4:5]
	v_pk_fma_f32 v[112:113], v[14:15], v[10:11], v[2:3]
	v_med3_f32 v2, v108, s33, v233
	v_med3_f32 v3, v109, s33, v233
	v_mov_b32_e32 v4, 0
	v_cvt_pk_fp8_f32 v4, v2, v3
	v_med3_f32 v2, v106, s33, v233
	v_med3_f32 v3, v107, s33, v233
	v_cvt_pk_fp8_f32 v4, v2, v3 op_sel:[0,0,1]
	v_med3_f32 v2, v112, s33, v233
	v_med3_f32 v3, v113, s33, v233
	global_store_dword v[118:119], v4, off offset:1536
	v_mov_b32_e32 v4, 0
	v_cvt_pk_fp8_f32 v4, v2, v3
	v_med3_f32 v2, v110, s33, v233
	v_med3_f32 v3, v111, s33, v233
	v_cvt_pk_fp8_f32 v4, v2, v3 op_sel:[0,0,1]
	global_store_dword v[118:119], v4, off offset:3584
	ds_read_b128 v[10:13], v172
	ds_read_b128 v[124:127], v173
	ds_read_b128 v[128:131], v174
	ds_read_b128 v[132:135], v175
	ds_read_b128 v[14:17], v176
	ds_read_b128 v[136:139], v177
	ds_read_b128 v[140:143], v178
	ds_read_b128 v[144:147], v179
	ds_read_b128 v[18:21], v180
	ds_read_b128 v[148:151], v181
	ds_read_b128 v[238:241], v182
	ds_read_b128 v[242:245], v183
	ds_read_b128 v[2:5], v184
	ds_read_b128 v[246:249], v185
	ds_read_b128 v[234:237], v186
	ds_read_b128 v[160:163], v187
	s_waitcnt vmcnt(3)
	v_pk_add_f32 v[116:117], v[116:117], 1.0 op_sel_hi:[1,0]
	v_pk_add_f32 v[154:155], v[114:115], 1.0 op_sel_hi:[1,0]
	s_waitcnt lgkmcnt(14)
	v_fmac_f32_e32 v215, v112, v13
	v_fmac_f32_e32 v219, v112, v12
	v_fmac_f32_e32 v222, v112, v11
	v_fmac_f32_e32 v225, v112, v10
	v_fmac_f32_e32 v217, v108, v13
	v_fmac_f32_e32 v221, v108, v12
	v_fmac_f32_e32 v223, v108, v11
	v_fmac_f32_e32 v224, v108, v10
	s_waitcnt vmcnt(2)
	v_pk_mul_f32 v[114:115], v[122:123], v[116:117]
	v_pk_mul_f32 v[116:117], v[120:121], v[154:155]
	s_waitcnt lgkmcnt(11)
	v_fmac_f32_e32 v215, v113, v17
	v_fmac_f32_e32 v219, v113, v16
	v_fmac_f32_e32 v222, v113, v15
	v_fmac_f32_e32 v225, v113, v14
	v_fmac_f32_e32 v217, v109, v17
	v_fmac_f32_e32 v221, v109, v16
	v_fmac_f32_e32 v223, v109, v15
	v_fmac_f32_e32 v224, v109, v14
	v_pk_mul_f32 v[10:11], v[102:103], v[100:101] op_sel_hi:[0,1]
	s_waitcnt lgkmcnt(7)
	v_fmac_f32_e32 v215, v110, v21
	v_fmac_f32_e32 v219, v110, v20
	v_fmac_f32_e32 v222, v110, v19
	v_fmac_f32_e32 v225, v110, v18
	v_fmac_f32_e32 v217, v106, v21
	v_fmac_f32_e32 v221, v106, v20
	v_fmac_f32_e32 v223, v106, v19
	v_fmac_f32_e32 v224, v106, v18
	v_pk_fma_f32 v[18:19], v[10:11], v[116:117], v[6:7]
	v_pk_mul_f32 v[10:11], v[104:105], v[96:97] op_sel_hi:[0,1]
	s_waitcnt lgkmcnt(3)
	v_fmac_f32_e32 v215, v111, v5
	v_fmac_f32_e32 v219, v111, v4
	v_fmac_f32_e32 v222, v111, v3
	v_fmac_f32_e32 v217, v107, v5
	v_fmac_f32_e32 v221, v107, v4
	v_fmac_f32_e32 v223, v107, v3
	v_pk_mul_f32 v[4:5], v[102:103], v[98:99] op_sel_hi:[0,1]
	v_pk_mul_f32 v[12:13], v[104:105], v[94:95] op_sel_hi:[0,1]
	v_pk_fma_f32 v[6:7], v[10:11], v[116:117], v[6:7]
	v_med3_f32 v3, v18, s33, v233
	v_med3_f32 v10, v19, s33, v233
	v_mov_b32_e32 v14, 0
	v_pk_fma_f32 v[4:5], v[4:5], v[114:115], v[8:9]
	v_pk_fma_f32 v[8:9], v[12:13], v[114:115], v[8:9]
	v_cvt_pk_fp8_f32 v14, v3, v10
	v_med3_f32 v11, v6, s33, v233
	v_med3_f32 v12, v7, s33, v233
	v_mov_b32_e32 v15, 0
	v_cvt_pk_fp8_f32 v15, v11, v12
	v_med3_f32 v3, v4, s33, v233
	v_med3_f32 v10, v5, s33, v233
	v_cvt_pk_fp8_f32 v14, v3, v10 op_sel:[0,0,1]
	v_med3_f32 v3, v8, s33, v233
	v_med3_f32 v10, v9, s33, v233
	v_cvt_pk_fp8_f32 v15, v3, v10 op_sel:[0,0,1]
	ds_read_b128 v[10:13], v188
	global_store_dword v[118:119], v14, off offset:1792
	global_store_dword v[118:119], v15, off offset:3840
	ds_read_b128 v[14:17], v189
	v_fmac_f32_e32 v210, v112, v127
	v_fmac_f32_e32 v212, v112, v126
	v_fmac_f32_e32 v214, v112, v125
	v_fmac_f32_e32 v218, v112, v124
	v_fmac_f32_e32 v211, v108, v127
	v_fmac_f32_e32 v213, v108, v126
	v_fmac_f32_e32 v216, v108, v125
	v_fmac_f32_e32 v220, v108, v124
	v_fmac_f32_e32 v210, v113, v139
	v_fmac_f32_e32 v212, v113, v138
	v_fmac_f32_e32 v214, v113, v137
	v_fmac_f32_e32 v218, v113, v136
	v_fmac_f32_e32 v211, v109, v139
	v_fmac_f32_e32 v213, v109, v138
	v_fmac_f32_e32 v216, v109, v137
	v_fmac_f32_e32 v220, v109, v136
	v_fmac_f32_e32 v210, v110, v151
	v_fmac_f32_e32 v212, v110, v150
	v_fmac_f32_e32 v214, v110, v149
	v_fmac_f32_e32 v218, v110, v148
	v_fmac_f32_e32 v211, v106, v151
	v_fmac_f32_e32 v213, v106, v150
	v_fmac_f32_e32 v216, v106, v149
	v_fmac_f32_e32 v220, v106, v148
	s_waitcnt lgkmcnt(4)
	v_fmac_f32_e32 v210, v111, v249
	v_fmac_f32_e32 v212, v111, v248
	v_fmac_f32_e32 v214, v111, v247
	v_fmac_f32_e32 v218, v111, v246
	v_fmac_f32_e32 v211, v107, v249
	v_fmac_f32_e32 v213, v107, v248
	v_fmac_f32_e32 v216, v107, v247
	v_fmac_f32_e32 v220, v107, v246
	v_fmac_f32_e32 v225, v111, v2
	v_fmac_f32_e32 v224, v107, v2
	s_waitcnt lgkmcnt(1)
	v_fmac_f32_e32 v224, v18, v10
	v_fmac_f32_e32 v223, v18, v11
	v_fmac_f32_e32 v221, v18, v12
	v_fmac_f32_e32 v217, v18, v13
	v_fmac_f32_e32 v225, v6, v10
	v_fmac_f32_e32 v222, v6, v11
	v_fmac_f32_e32 v219, v6, v12
	v_fmac_f32_e32 v215, v6, v13
	ds_read_b128 v[10:13], v190
	s_waitcnt lgkmcnt(1)
	v_fmac_f32_e32 v220, v18, v14
	v_fmac_f32_e32 v216, v18, v15
	v_fmac_f32_e32 v213, v18, v16
	v_fmac_f32_e32 v211, v18, v17
	v_fmac_f32_e32 v218, v6, v14
	v_fmac_f32_e32 v214, v6, v15
	v_fmac_f32_e32 v212, v6, v16
	v_fmac_f32_e32 v210, v6, v17
	ds_read_b128 v[14:17], v191
	v_fmac_f32_e32 v47, v112, v135
	v_fmac_f32_e32 v51, v112, v134
	v_fmac_f32_e32 v55, v112, v133
	v_fmac_f32_e32 v156, v112, v132
	v_fmac_f32_e32 v49, v108, v135
	v_fmac_f32_e32 v53, v108, v134
	v_fmac_f32_e32 v152, v108, v133
	v_fmac_f32_e32 v159, v108, v132
	v_fmac_f32_e32 v57, v112, v131
	v_fmac_f32_e32 v158, v112, v130
	v_fmac_f32_e32 v206, v112, v129
	v_fmac_f32_e32 v208, v112, v128
	v_fmac_f32_e32 v153, v108, v131
	v_fmac_f32_e32 v205, v108, v130
	v_fmac_f32_e32 v207, v108, v129
	v_fmac_f32_e32 v209, v108, v128
	v_fmac_f32_e32 v47, v113, v147
	v_fmac_f32_e32 v51, v113, v146
	v_fmac_f32_e32 v55, v113, v145
	v_fmac_f32_e32 v156, v113, v144
	v_fmac_f32_e32 v49, v109, v147
	v_fmac_f32_e32 v53, v109, v146
	v_fmac_f32_e32 v152, v109, v145
	v_fmac_f32_e32 v159, v109, v144
	v_fmac_f32_e32 v57, v113, v143
	v_fmac_f32_e32 v158, v113, v142
	v_fmac_f32_e32 v206, v113, v141
	v_fmac_f32_e32 v208, v113, v140
	v_fmac_f32_e32 v153, v109, v143
	v_fmac_f32_e32 v205, v109, v142
	v_fmac_f32_e32 v207, v109, v141
	v_fmac_f32_e32 v209, v109, v140
	v_fmac_f32_e32 v47, v110, v245
	v_fmac_f32_e32 v51, v110, v244
	v_fmac_f32_e32 v55, v110, v243
	v_fmac_f32_e32 v156, v110, v242
	v_fmac_f32_e32 v49, v106, v245
	v_fmac_f32_e32 v53, v106, v244
	v_fmac_f32_e32 v152, v106, v243
	v_fmac_f32_e32 v159, v106, v242
	v_fmac_f32_e32 v57, v110, v241
	v_fmac_f32_e32 v158, v110, v240
	v_fmac_f32_e32 v206, v110, v239
	v_fmac_f32_e32 v208, v110, v238
	v_fmac_f32_e32 v153, v106, v241
	v_fmac_f32_e32 v205, v106, v240
	v_fmac_f32_e32 v207, v106, v239
	v_fmac_f32_e32 v209, v106, v238
	v_fmac_f32_e32 v47, v111, v163
	v_fmac_f32_e32 v51, v111, v162
	v_fmac_f32_e32 v55, v111, v161
	v_fmac_f32_e32 v156, v111, v160
	v_fmac_f32_e32 v49, v107, v163
	v_fmac_f32_e32 v53, v107, v162
	v_fmac_f32_e32 v152, v107, v161
	v_fmac_f32_e32 v159, v107, v160
	v_fmac_f32_e32 v57, v111, v237
	v_fmac_f32_e32 v158, v111, v236
	v_fmac_f32_e32 v206, v111, v235
	v_fmac_f32_e32 v208, v111, v234
	v_fmac_f32_e32 v153, v107, v237
	v_fmac_f32_e32 v205, v107, v236
	v_fmac_f32_e32 v207, v107, v235
	v_fmac_f32_e32 v209, v107, v234
	s_waitcnt lgkmcnt(1)
	v_fmac_f32_e32 v209, v18, v10
	v_fmac_f32_e32 v207, v18, v11
	v_fmac_f32_e32 v205, v18, v12
	v_fmac_f32_e32 v153, v18, v13
	v_fmac_f32_e32 v208, v6, v10
	v_fmac_f32_e32 v206, v6, v11
	v_fmac_f32_e32 v158, v6, v12
	v_fmac_f32_e32 v57, v6, v13
	ds_read_b128 v[10:13], v192
	s_waitcnt lgkmcnt(1)
	v_fmac_f32_e32 v159, v18, v14
	v_fmac_f32_e32 v152, v18, v15
	v_fmac_f32_e32 v53, v18, v16
	v_fmac_f32_e32 v49, v18, v17
	v_fmac_f32_e32 v156, v6, v14
	v_fmac_f32_e32 v55, v6, v15
	v_fmac_f32_e32 v51, v6, v16
	v_fmac_f32_e32 v47, v6, v17
	ds_read_b128 v[14:17], v193
	s_waitcnt lgkmcnt(1)
	v_fmac_f32_e32 v224, v19, v10
	v_fmac_f32_e32 v223, v19, v11
	v_fmac_f32_e32 v221, v19, v12
	v_fmac_f32_e32 v217, v19, v13
	v_fmac_f32_e32 v225, v7, v10
	v_fmac_f32_e32 v222, v7, v11
	v_fmac_f32_e32 v219, v7, v12
	v_fmac_f32_e32 v215, v7, v13
	ds_read_b128 v[10:13], v194
	s_waitcnt lgkmcnt(1)
	v_fmac_f32_e32 v220, v19, v14
	v_fmac_f32_e32 v216, v19, v15
	v_fmac_f32_e32 v213, v19, v16
	v_fmac_f32_e32 v211, v19, v17
	v_fmac_f32_e32 v218, v7, v14
	v_fmac_f32_e32 v214, v7, v15
	v_fmac_f32_e32 v212, v7, v16
	v_fmac_f32_e32 v210, v7, v17
	ds_read_b128 v[14:17], v195
	s_waitcnt lgkmcnt(1)
	v_fmac_f32_e32 v209, v19, v10
	v_fmac_f32_e32 v207, v19, v11
	v_fmac_f32_e32 v205, v19, v12
	v_fmac_f32_e32 v153, v19, v13
	v_fmac_f32_e32 v208, v7, v10
	v_fmac_f32_e32 v206, v7, v11
	v_fmac_f32_e32 v158, v7, v12
	v_fmac_f32_e32 v57, v7, v13
	ds_read_b128 v[10:13], v196
	s_waitcnt lgkmcnt(1)
	v_fmac_f32_e32 v159, v19, v14
	v_fmac_f32_e32 v152, v19, v15
	v_fmac_f32_e32 v53, v19, v16
	v_fmac_f32_e32 v49, v19, v17
	v_fmac_f32_e32 v156, v7, v14
	v_fmac_f32_e32 v55, v7, v15
	v_fmac_f32_e32 v51, v7, v16
	v_fmac_f32_e32 v47, v7, v17
	ds_read_b128 v[14:17], v197
	s_waitcnt lgkmcnt(1)
	v_fmac_f32_e32 v224, v4, v10
	v_fmac_f32_e32 v223, v4, v11
	v_fmac_f32_e32 v221, v4, v12
	v_fmac_f32_e32 v217, v4, v13
	v_fmac_f32_e32 v225, v8, v10
	v_fmac_f32_e32 v222, v8, v11
	v_fmac_f32_e32 v219, v8, v12
	v_fmac_f32_e32 v215, v8, v13
	ds_read_b128 v[10:13], v198
	s_waitcnt lgkmcnt(1)
	v_fmac_f32_e32 v220, v4, v14
	v_fmac_f32_e32 v216, v4, v15
	v_fmac_f32_e32 v213, v4, v16
	v_fmac_f32_e32 v211, v4, v17
	v_fmac_f32_e32 v218, v8, v14
	v_fmac_f32_e32 v214, v8, v15
	v_fmac_f32_e32 v212, v8, v16
	v_fmac_f32_e32 v210, v8, v17
	ds_read_b128 v[14:17], v199
	s_waitcnt lgkmcnt(1)
	v_fmac_f32_e32 v209, v4, v10
	v_fmac_f32_e32 v207, v4, v11
	v_fmac_f32_e32 v205, v4, v12
	v_fmac_f32_e32 v153, v4, v13
	v_fmac_f32_e32 v208, v8, v10
	v_fmac_f32_e32 v206, v8, v11
	v_fmac_f32_e32 v158, v8, v12
	v_fmac_f32_e32 v57, v8, v13
	ds_read_b128 v[10:13], v200
	s_waitcnt lgkmcnt(1)
	v_fmac_f32_e32 v159, v4, v14
	v_fmac_f32_e32 v152, v4, v15
	v_fmac_f32_e32 v53, v4, v16
	v_fmac_f32_e32 v49, v4, v17
	v_fmac_f32_e32 v156, v8, v14
	v_fmac_f32_e32 v55, v8, v15
	v_fmac_f32_e32 v51, v8, v16
	v_fmac_f32_e32 v47, v8, v17
	ds_read_b128 v[14:17], v201
	s_waitcnt lgkmcnt(1)
	v_fmac_f32_e32 v224, v5, v10
	v_fmac_f32_e32 v223, v5, v11
	v_fmac_f32_e32 v221, v5, v12
	v_fmac_f32_e32 v217, v5, v13
	v_fmac_f32_e32 v225, v9, v10
	v_fmac_f32_e32 v222, v9, v11
	v_fmac_f32_e32 v219, v9, v12
	v_fmac_f32_e32 v215, v9, v13
	ds_read_b128 v[10:13], v202
	s_waitcnt lgkmcnt(1)
	v_fmac_f32_e32 v220, v5, v14
	v_fmac_f32_e32 v216, v5, v15
	v_fmac_f32_e32 v213, v5, v16
	v_fmac_f32_e32 v211, v5, v17
	v_fmac_f32_e32 v218, v9, v14
	v_fmac_f32_e32 v214, v9, v15
	v_fmac_f32_e32 v212, v9, v16
	v_fmac_f32_e32 v210, v9, v17
	ds_read_b128 v[14:17], v203
	s_waitcnt lgkmcnt(1)
	v_fmac_f32_e32 v57, v9, v13
	v_fmac_f32_e32 v209, v5, v10
	v_fmac_f32_e32 v207, v5, v11
	v_fmac_f32_e32 v205, v5, v12
	s_waitcnt lgkmcnt(0)
	v_fmac_f32_e32 v53, v5, v16
	v_fmac_f32_e32 v55, v9, v15
	v_fmac_f32_e32 v51, v9, v16
	v_fmac_f32_e32 v153, v5, v13
	v_fmac_f32_e32 v208, v9, v10
	v_fmac_f32_e32 v206, v9, v11
	v_fmac_f32_e32 v158, v9, v12
	v_fmac_f32_e32 v159, v5, v14
	v_fmac_f32_e32 v152, v5, v15
	v_fmac_f32_e32 v49, v5, v17
	v_fmac_f32_e32 v156, v9, v14
	v_fmac_f32_e32 v47, v9, v17
	v_mov_b32_dpp v10, v221 quad_perm:[1,0,3,2] row_mask:0xf bank_mask:0xf
	v_mov_b32_dpp v12, v219 quad_perm:[1,0,3,2] row_mask:0xf bank_mask:0xf
	v_mov_b32_dpp v14, v217 quad_perm:[1,0,3,2] row_mask:0xf bank_mask:0xf
	v_mov_b32_dpp v2, v224 quad_perm:[1,0,3,2] row_mask:0xf bank_mask:0xf
	v_mov_b32_dpp v3, v225 quad_perm:[1,0,3,2] row_mask:0xf bank_mask:0xf
	v_add_f32_e32 v10, v221, v10
	s_nop 1
	v_mov_b32_dpp v11, v10 quad_perm:[2,3,0,1] row_mask:0xf bank_mask:0xf
	v_add_f32_e32 v12, v219, v12
	s_nop 1
	v_mov_b32_dpp v13, v12 quad_perm:[2,3,0,1] row_mask:0xf bank_mask:0xf
	v_mov_b32_dpp v6, v223 quad_perm:[1,0,3,2] row_mask:0xf bank_mask:0xf
	v_mov_b32_dpp v8, v222 quad_perm:[1,0,3,2] row_mask:0xf bank_mask:0xf
	v_add_f32_e32 v10, v10, v11
	s_nop 1
	v_mov_b32_dpp v11, v10 row_half_mirror row_mask:0xf bank_mask:0xf
	v_add_f32_e32 v12, v12, v13
	s_nop 1
	v_mov_b32_dpp v13, v12 row_half_mirror row_mask:0xf bank_mask:0xf
	v_add_f32_e32 v2, v224, v2
	v_add_f32_e32 v3, v225, v3
	v_add_f32_e32 v10, v10, v11
	s_nop 1
	v_mov_b32_dpp v11, v10 row_mirror row_mask:0xf bank_mask:0xf
	v_add_f32_e32 v6, v223, v6
	v_add_f32_e32 v8, v222, v8
	v_mov_b32_dpp v4, v2 quad_perm:[2,3,0,1] row_mask:0xf bank_mask:0xf
	v_mov_b32_dpp v5, v3 quad_perm:[2,3,0,1] row_mask:0xf bank_mask:0xf
	v_add_f32_e32 v10, v10, v11
	v_mov_b32_e32 v11, v10
	s_nop 1
	v_permlane16_swap_b32_e32 v10, v11
	v_add_f32_e32 v19, v10, v11
	v_add_f32_e32 v10, v12, v13
	v_add_f32_e32 v12, v217, v14
	s_nop 1
	v_mov_b32_dpp v13, v12 quad_perm:[2,3,0,1] row_mask:0xf bank_mask:0xf
	v_mov_b32_dpp v11, v10 row_mirror row_mask:0xf bank_mask:0xf
	v_mov_b32_dpp v14, v215 quad_perm:[1,0,3,2] row_mask:0xf bank_mask:0xf
	v_mov_b32_dpp v7, v6 quad_perm:[2,3,0,1] row_mask:0xf bank_mask:0xf
	v_mov_b32_dpp v9, v8 quad_perm:[2,3,0,1] row_mask:0xf bank_mask:0xf
	v_add_f32_e32 v12, v12, v13
	s_nop 1
	v_mov_b32_dpp v13, v12 row_half_mirror row_mask:0xf bank_mask:0xf
	v_add_f32_e32 v10, v10, v11
	v_mov_b32_e32 v11, v10
	s_nop 1
	v_permlane16_swap_b32_e32 v10, v11
	v_add_f32_e32 v97, v10, v11
	v_add_f32_e32 v10, v12, v13
	v_add_f32_e32 v12, v215, v14
	s_nop 1
	v_mov_b32_dpp v13, v12 quad_perm:[2,3,0,1] row_mask:0xf bank_mask:0xf
	v_mov_b32_dpp v11, v10 row_mirror row_mask:0xf bank_mask:0xf
	v_mov_b32_dpp v14, v220 quad_perm:[1,0,3,2] row_mask:0xf bank_mask:0xf
	v_add_f32_e32 v2, v2, v4
	v_add_f32_e32 v3, v3, v5
	v_add_f32_e32 v12, v12, v13
	s_nop 1
	v_mov_b32_dpp v13, v12 row_half_mirror row_mask:0xf bank_mask:0xf
	v_add_f32_e32 v10, v10, v11
	v_mov_b32_e32 v11, v10
	s_nop 1
	v_permlane16_swap_b32_e32 v10, v11
	v_add_f32_e32 v21, v10, v11
	v_add_f32_e32 v10, v12, v13
	v_add_f32_e32 v12, v220, v14
	s_nop 1
	v_mov_b32_dpp v13, v12 quad_perm:[2,3,0,1] row_mask:0xf bank_mask:0xf
	v_mov_b32_dpp v11, v10 row_mirror row_mask:0xf bank_mask:0xf
	v_mov_b32_dpp v14, v218 quad_perm:[1,0,3,2] row_mask:0xf bank_mask:0xf
	v_add_f32_e32 v6, v6, v7
	v_add_f32_e32 v8, v8, v9
	v_add_f32_e32 v12, v12, v13
	s_nop 1
	v_mov_b32_dpp v13, v12 row_half_mirror row_mask:0xf bank_mask:0xf
	v_add_f32_e32 v10, v10, v11
	v_mov_b32_e32 v11, v10
	s_nop 1
	v_permlane16_swap_b32_e32 v10, v11
	v_add_f32_e32 v99, v10, v11
	v_add_f32_e32 v10, v12, v13
	v_add_f32_e32 v12, v218, v14
	s_nop 1
	v_mov_b32_dpp v13, v12 quad_perm:[2,3,0,1] row_mask:0xf bank_mask:0xf
	v_mov_b32_dpp v11, v10 row_mirror row_mask:0xf bank_mask:0xf
	v_mov_b32_dpp v14, v216 quad_perm:[1,0,3,2] row_mask:0xf bank_mask:0xf
	v_mov_b32_dpp v4, v2 row_half_mirror row_mask:0xf bank_mask:0xf
	v_mov_b32_dpp v5, v3 row_half_mirror row_mask:0xf bank_mask:0xf
	v_add_f32_e32 v12, v12, v13
	s_nop 1
	v_mov_b32_dpp v13, v12 row_half_mirror row_mask:0xf bank_mask:0xf
	v_add_f32_e32 v10, v10, v11
	v_mov_b32_e32 v11, v10
	s_nop 1
	v_permlane16_swap_b32_e32 v10, v11
	v_add_f32_e32 v95, v10, v11
	v_add_f32_e32 v10, v12, v13
	v_add_f32_e32 v12, v216, v14
	s_nop 1
	v_mov_b32_dpp v13, v12 quad_perm:[2,3,0,1] row_mask:0xf bank_mask:0xf
	v_mov_b32_dpp v11, v10 row_mirror row_mask:0xf bank_mask:0xf
	v_mov_b32_dpp v14, v214 quad_perm:[1,0,3,2] row_mask:0xf bank_mask:0xf
	v_mov_b32_dpp v7, v6 row_half_mirror row_mask:0xf bank_mask:0xf
	v_mov_b32_dpp v9, v8 row_half_mirror row_mask:0xf bank_mask:0xf
	v_add_f32_e32 v12, v12, v13
	s_nop 1
	v_mov_b32_dpp v13, v12 row_half_mirror row_mask:0xf bank_mask:0xf
	v_add_f32_e32 v10, v10, v11
	v_mov_b32_e32 v11, v10
	s_nop 1
	v_permlane16_swap_b32_e32 v10, v11
	v_add_f32_e32 v101, v10, v11
	v_add_f32_e32 v10, v12, v13
	v_add_f32_e32 v12, v214, v14
	s_nop 1
	v_mov_b32_dpp v13, v12 quad_perm:[2,3,0,1] row_mask:0xf bank_mask:0xf
	v_mov_b32_dpp v11, v10 row_mirror row_mask:0xf bank_mask:0xf
	v_mov_b32_dpp v14, v213 quad_perm:[1,0,3,2] row_mask:0xf bank_mask:0xf
	v_add_f32_e32 v2, v2, v4
	v_add_f32_e32 v3, v3, v5
	v_add_f32_e32 v12, v12, v13
	s_nop 1
	v_mov_b32_dpp v13, v12 row_half_mirror row_mask:0xf bank_mask:0xf
	v_add_f32_e32 v10, v10, v11
	v_mov_b32_e32 v11, v10
	s_nop 1
	v_permlane16_swap_b32_e32 v10, v11
	v_add_f32_e32 v107, v10, v11
	v_add_f32_e32 v10, v12, v13
	v_add_f32_e32 v12, v213, v14
	s_nop 1
	v_mov_b32_dpp v13, v12 quad_perm:[2,3,0,1] row_mask:0xf bank_mask:0xf
	v_mov_b32_dpp v11, v10 row_mirror row_mask:0xf bank_mask:0xf
	v_mov_b32_dpp v14, v212 quad_perm:[1,0,3,2] row_mask:0xf bank_mask:0xf
	v_add_f32_e32 v6, v6, v7
	v_add_f32_e32 v8, v8, v9
	v_add_f32_e32 v12, v12, v13
	s_nop 1
	v_mov_b32_dpp v13, v12 row_half_mirror row_mask:0xf bank_mask:0xf
	v_add_f32_e32 v10, v10, v11
	v_mov_b32_e32 v11, v10
	s_nop 1
	v_permlane16_swap_b32_e32 v10, v11
	v_add_f32_e32 v115, v10, v11
	v_add_f32_e32 v10, v12, v13
	v_add_f32_e32 v12, v212, v14
	s_nop 1
	v_mov_b32_dpp v13, v12 quad_perm:[2,3,0,1] row_mask:0xf bank_mask:0xf
	v_mov_b32_dpp v11, v10 row_mirror row_mask:0xf bank_mask:0xf
	v_mov_b32_dpp v14, v211 quad_perm:[1,0,3,2] row_mask:0xf bank_mask:0xf
	v_mov_b32_dpp v4, v2 row_mirror row_mask:0xf bank_mask:0xf
	v_mov_b32_dpp v5, v3 row_mirror row_mask:0xf bank_mask:0xf
	v_add_f32_e32 v12, v12, v13
	s_nop 1
	v_mov_b32_dpp v13, v12 row_half_mirror row_mask:0xf bank_mask:0xf
	v_add_f32_e32 v10, v10, v11
	v_mov_b32_e32 v11, v10
	s_nop 1
	v_permlane16_swap_b32_e32 v10, v11
	v_add_f32_e32 v104, v10, v11
	v_add_f32_e32 v10, v12, v13
	v_add_f32_e32 v12, v211, v14
	s_nop 1
	v_mov_b32_dpp v13, v12 quad_perm:[2,3,0,1] row_mask:0xf bank_mask:0xf
	v_mov_b32_dpp v11, v10 row_mirror row_mask:0xf bank_mask:0xf
	v_mov_b32_dpp v14, v210 quad_perm:[1,0,3,2] row_mask:0xf bank_mask:0xf
	v_mov_b32_dpp v7, v6 row_mirror row_mask:0xf bank_mask:0xf
	v_mov_b32_dpp v9, v8 row_mirror row_mask:0xf bank_mask:0xf
	v_add_f32_e32 v12, v12, v13
	s_nop 1
	v_mov_b32_dpp v13, v12 row_half_mirror row_mask:0xf bank_mask:0xf
	v_add_f32_e32 v10, v10, v11
	v_mov_b32_e32 v11, v10
	s_nop 1
	v_permlane16_swap_b32_e32 v10, v11
	v_add_f32_e32 v113, v10, v11
	v_add_f32_e32 v10, v12, v13
	v_add_f32_e32 v12, v210, v14
	s_nop 1
	v_mov_b32_dpp v13, v12 quad_perm:[2,3,0,1] row_mask:0xf bank_mask:0xf
	v_mov_b32_dpp v11, v10 row_mirror row_mask:0xf bank_mask:0xf
	v_mov_b32_dpp v14, v209 quad_perm:[1,0,3,2] row_mask:0xf bank_mask:0xf
	v_add_f32_e32 v2, v2, v4
	v_add_f32_e32 v4, v3, v5
	v_add_f32_e32 v12, v12, v13
	s_nop 1
	v_mov_b32_dpp v13, v12 row_half_mirror row_mask:0xf bank_mask:0xf
	v_add_f32_e32 v10, v10, v11
	v_mov_b32_e32 v11, v10
	s_nop 1
	v_permlane16_swap_b32_e32 v10, v11
	v_add_f32_e32 v109, v10, v11
	v_add_f32_e32 v10, v12, v13
	v_add_f32_e32 v12, v209, v14
	s_nop 1
	v_mov_b32_dpp v13, v12 quad_perm:[2,3,0,1] row_mask:0xf bank_mask:0xf
	v_mov_b32_dpp v11, v10 row_mirror row_mask:0xf bank_mask:0xf
	v_mov_b32_dpp v14, v208 quad_perm:[1,0,3,2] row_mask:0xf bank_mask:0xf
	v_add_f32_e32 v6, v6, v7
	v_add_f32_e32 v8, v8, v9
	v_add_f32_e32 v12, v12, v13
	s_nop 1
	v_mov_b32_dpp v13, v12 row_half_mirror row_mask:0xf bank_mask:0xf
	v_add_f32_e32 v10, v10, v11
	v_mov_b32_e32 v11, v10
	s_nop 1
	v_permlane16_swap_b32_e32 v10, v11
	v_add_f32_e32 v117, v10, v11
	v_add_f32_e32 v10, v12, v13
	v_add_f32_e32 v12, v208, v14
	s_nop 1
	v_mov_b32_dpp v13, v12 quad_perm:[2,3,0,1] row_mask:0xf bank_mask:0xf
	v_mov_b32_dpp v11, v10 row_mirror row_mask:0xf bank_mask:0xf
	v_mov_b32_dpp v14, v207 quad_perm:[1,0,3,2] row_mask:0xf bank_mask:0xf
	v_mov_b32_e32 v3, v2
	v_mov_b32_e32 v5, v4
	v_add_f32_e32 v12, v12, v13
	s_nop 1
	v_mov_b32_dpp v13, v12 row_half_mirror row_mask:0xf bank_mask:0xf
	v_add_f32_e32 v10, v10, v11
	v_mov_b32_e32 v11, v10
	s_nop 1
	v_permlane16_swap_b32_e32 v10, v11
	v_add_f32_e32 v111, v10, v11
	v_add_f32_e32 v10, v12, v13
	v_add_f32_e32 v12, v207, v14
	s_nop 1
	v_mov_b32_dpp v13, v12 quad_perm:[2,3,0,1] row_mask:0xf bank_mask:0xf
	v_mov_b32_dpp v11, v10 row_mirror row_mask:0xf bank_mask:0xf
	v_mov_b32_dpp v14, v206 quad_perm:[1,0,3,2] row_mask:0xf bank_mask:0xf
	v_mov_b32_e32 v7, v6
	v_mov_b32_e32 v9, v8
	v_add_f32_e32 v12, v12, v13
	s_nop 1
	v_mov_b32_dpp v13, v12 row_half_mirror row_mask:0xf bank_mask:0xf
	v_add_f32_e32 v10, v10, v11
	v_mov_b32_e32 v11, v10
	s_nop 1
	v_permlane16_swap_b32_e32 v10, v11
	v_add_f32_e32 v119, v10, v11
	v_add_f32_e32 v10, v12, v13
	v_add_f32_e32 v12, v206, v14
	s_nop 1
	v_mov_b32_dpp v13, v12 quad_perm:[2,3,0,1] row_mask:0xf bank_mask:0xf
	v_mov_b32_dpp v11, v10 row_mirror row_mask:0xf bank_mask:0xf
	v_mov_b32_dpp v14, v205 quad_perm:[1,0,3,2] row_mask:0xf bank_mask:0xf
	v_permlane16_swap_b32_e32 v2, v3
	v_add_f32_e32 v12, v12, v13
	s_nop 1
	v_mov_b32_dpp v13, v12 row_half_mirror row_mask:0xf bank_mask:0xf
	v_add_f32_e32 v10, v10, v11
	v_mov_b32_e32 v11, v10
	s_nop 1
	v_permlane16_swap_b32_e32 v10, v11
	v_add_f32_e32 v123, v10, v11
	v_add_f32_e32 v10, v12, v13
	v_add_f32_e32 v12, v205, v14
	s_nop 1
	v_mov_b32_dpp v13, v12 quad_perm:[2,3,0,1] row_mask:0xf bank_mask:0xf
	v_mov_b32_dpp v11, v10 row_mirror row_mask:0xf bank_mask:0xf
	v_mov_b32_dpp v14, v158 quad_perm:[1,0,3,2] row_mask:0xf bank_mask:0xf
	v_permlane16_swap_b32_e32 v4, v5
	v_add_f32_e32 v12, v12, v13
	s_nop 1
	v_mov_b32_dpp v13, v12 row_half_mirror row_mask:0xf bank_mask:0xf
	v_add_f32_e32 v10, v10, v11
	v_mov_b32_e32 v11, v10
	s_nop 1
	v_permlane16_swap_b32_e32 v10, v11
	v_add_f32_e32 v130, v10, v11
	v_add_f32_e32 v10, v12, v13
	v_add_f32_e32 v12, v158, v14
	s_nop 1
	v_mov_b32_dpp v13, v12 quad_perm:[2,3,0,1] row_mask:0xf bank_mask:0xf
	v_mov_b32_dpp v11, v10 row_mirror row_mask:0xf bank_mask:0xf
	v_mov_b32_dpp v14, v153 quad_perm:[1,0,3,2] row_mask:0xf bank_mask:0xf
	v_permlane16_swap_b32_e32 v6, v7
	v_add_f32_e32 v12, v12, v13
	s_nop 1
	v_mov_b32_dpp v13, v12 row_half_mirror row_mask:0xf bank_mask:0xf
	v_add_f32_e32 v10, v10, v11
	v_mov_b32_e32 v11, v10
	s_nop 1
	v_permlane16_swap_b32_e32 v10, v11
	v_add_f32_e32 v121, v10, v11
	v_add_f32_e32 v10, v12, v13
	v_add_f32_e32 v12, v153, v14
	s_nop 1
	v_mov_b32_dpp v13, v12 quad_perm:[2,3,0,1] row_mask:0xf bank_mask:0xf
	v_mov_b32_dpp v11, v10 row_mirror row_mask:0xf bank_mask:0xf
	v_mov_b32_dpp v14, v57 quad_perm:[1,0,3,2] row_mask:0xf bank_mask:0xf
	v_permlane16_swap_b32_e32 v8, v9
	v_add_f32_e32 v12, v12, v13
	s_nop 1
	v_mov_b32_dpp v13, v12 row_half_mirror row_mask:0xf bank_mask:0xf
	v_add_f32_e32 v10, v10, v11
	v_mov_b32_e32 v11, v10
	s_nop 1
	v_permlane16_swap_b32_e32 v10, v11
	v_add_f32_e32 v128, v10, v11
	v_add_f32_e32 v10, v12, v13
	v_add_f32_e32 v12, v57, v14
	s_nop 1
	v_mov_b32_dpp v13, v12 quad_perm:[2,3,0,1] row_mask:0xf bank_mask:0xf
	v_mov_b32_dpp v11, v10 row_mirror row_mask:0xf bank_mask:0xf
	v_mov_b32_dpp v14, v159 quad_perm:[1,0,3,2] row_mask:0xf bank_mask:0xf
	v_add_f32_e32 v2, v2, v3
	v_add_f32_e32 v4, v4, v5
	v_add_f32_e32 v12, v12, v13
	s_nop 1
	v_mov_b32_dpp v13, v12 row_half_mirror row_mask:0xf bank_mask:0xf
	v_add_f32_e32 v10, v10, v11
	v_mov_b32_e32 v11, v10
	s_nop 1
	v_permlane16_swap_b32_e32 v10, v11
	v_add_f32_e32 v57, v10, v11
	v_add_f32_e32 v10, v12, v13
	v_add_f32_e32 v12, v159, v14
	s_nop 1
	v_mov_b32_dpp v13, v12 quad_perm:[2,3,0,1] row_mask:0xf bank_mask:0xf
	v_mov_b32_dpp v11, v10 row_mirror row_mask:0xf bank_mask:0xf
	v_mov_b32_dpp v14, v156 quad_perm:[1,0,3,2] row_mask:0xf bank_mask:0xf
	v_add_f32_e32 v6, v6, v7
	v_add_f32_e32 v8, v8, v9
	v_add_f32_e32 v12, v12, v13
	s_nop 1
	v_mov_b32_dpp v13, v12 row_half_mirror row_mask:0xf bank_mask:0xf
	v_add_f32_e32 v10, v10, v11
	v_mov_b32_e32 v11, v10
	s_nop 1
	v_permlane16_swap_b32_e32 v10, v11
	v_add_f32_e32 v132, v10, v11
	v_add_f32_e32 v10, v12, v13
	v_add_f32_e32 v12, v156, v14
	s_nop 1
	v_mov_b32_dpp v13, v12 quad_perm:[2,3,0,1] row_mask:0xf bank_mask:0xf
	v_mov_b32_dpp v11, v10 row_mirror row_mask:0xf bank_mask:0xf
	v_mov_b32_dpp v14, v152 quad_perm:[1,0,3,2] row_mask:0xf bank_mask:0xf
	v_mov_b32_e32 v3, v2
	v_mov_b32_e32 v5, v4
	v_add_f32_e32 v12, v12, v13
	s_nop 1
	v_mov_b32_dpp v13, v12 row_half_mirror row_mask:0xf bank_mask:0xf
	v_add_f32_e32 v10, v10, v11
	v_mov_b32_e32 v11, v10
	s_nop 1
	v_permlane16_swap_b32_e32 v10, v11
	v_add_f32_e32 v126, v10, v11
	v_add_f32_e32 v10, v12, v13
	v_add_f32_e32 v12, v152, v14
	s_nop 1
	v_mov_b32_dpp v13, v12 quad_perm:[2,3,0,1] row_mask:0xf bank_mask:0xf
	v_mov_b32_dpp v11, v10 row_mirror row_mask:0xf bank_mask:0xf
	v_mov_b32_dpp v14, v55 quad_perm:[1,0,3,2] row_mask:0xf bank_mask:0xf
	v_mov_b32_e32 v7, v6
	v_mov_b32_e32 v9, v8
	v_add_f32_e32 v12, v12, v13
	s_nop 1
	v_mov_b32_dpp v13, v12 row_half_mirror row_mask:0xf bank_mask:0xf
	v_add_f32_e32 v10, v10, v11
	v_mov_b32_e32 v11, v10
	s_nop 1
	v_permlane16_swap_b32_e32 v10, v11
	v_add_f32_e32 v134, v10, v11
	v_add_f32_e32 v10, v12, v13
	v_add_f32_e32 v12, v55, v14
	s_nop 1
	v_mov_b32_dpp v13, v12 quad_perm:[2,3,0,1] row_mask:0xf bank_mask:0xf
	v_mov_b32_dpp v11, v10 row_mirror row_mask:0xf bank_mask:0xf
	v_mov_b32_dpp v14, v53 quad_perm:[1,0,3,2] row_mask:0xf bank_mask:0xf
	v_mov_b32_e32 v20, v19
	v_mov_b32_e32 v98, v97
	v_add_f32_e32 v12, v12, v13
	s_nop 1
	v_mov_b32_dpp v13, v12 row_half_mirror row_mask:0xf bank_mask:0xf
	v_add_f32_e32 v10, v10, v11
	v_mov_b32_e32 v11, v10
	s_nop 1
	v_permlane16_swap_b32_e32 v10, v11
	v_add_f32_e32 v55, v10, v11
	v_add_f32_e32 v10, v12, v13
	v_add_f32_e32 v12, v53, v14
	s_nop 1
	v_mov_b32_dpp v13, v12 quad_perm:[2,3,0,1] row_mask:0xf bank_mask:0xf
	v_mov_b32_dpp v11, v10 row_mirror row_mask:0xf bank_mask:0xf
	v_mov_b32_dpp v14, v51 quad_perm:[1,0,3,2] row_mask:0xf bank_mask:0xf
	v_mov_b32_e32 v94, v21
	v_mov_b32_e32 v100, v99
	v_add_f32_e32 v12, v12, v13
	s_nop 1
	v_mov_b32_dpp v13, v12 row_half_mirror row_mask:0xf bank_mask:0xf
	v_add_f32_e32 v10, v10, v11
	v_mov_b32_e32 v11, v10
	s_nop 1
	v_permlane16_swap_b32_e32 v10, v11
	v_add_f32_e32 v143, v10, v11
	v_add_f32_e32 v10, v12, v13
	v_add_f32_e32 v12, v51, v14
	s_nop 0
	v_mov_b32_dpp v11, v10 row_mirror row_mask:0xf bank_mask:0xf
	s_nop 0
	v_mov_b32_dpp v13, v12 quad_perm:[2,3,0,1] row_mask:0xf bank_mask:0xf
	v_mov_b32_dpp v14, v47 quad_perm:[1,0,3,2] row_mask:0xf bank_mask:0xf
	v_mov_b32_e32 v96, v95
	v_mov_b32_e32 v102, v101
	v_add_f32_e32 v10, v10, v11
	v_add_f32_e32 v11, v12, v13
	s_nop 1
	v_mov_b32_dpp v12, v11 row_half_mirror row_mask:0xf bank_mask:0xf
	v_mov_b32_e32 v13, v10
	s_nop 1
	v_permlane16_swap_b32_e32 v10, v13
	v_add_f32_e32 v51, v10, v13
	v_add_f32_e32 v10, v11, v12
	s_nop 1
	v_mov_b32_dpp v11, v10 row_mirror row_mask:0xf bank_mask:0xf
	v_mov_b32_dpp v12, v49 quad_perm:[1,0,3,2] row_mask:0xf bank_mask:0xf
	v_mov_b32_e32 v108, v107
	v_mov_b32_e32 v116, v115
	v_mov_b32_e32 v106, v104
	v_add_f32_e32 v10, v10, v11
	v_add_f32_e32 v11, v49, v12
	v_mov_b32_e32 v13, v10
	s_nop 0
	v_mov_b32_dpp v12, v11 quad_perm:[2,3,0,1] row_mask:0xf bank_mask:0xf
	s_nop 0
	v_permlane16_swap_b32_e32 v10, v13
	v_add_f32_e32 v141, v10, v13
	v_add_f32_e32 v10, v47, v14
	s_nop 1
	v_mov_b32_dpp v13, v10 quad_perm:[2,3,0,1] row_mask:0xf bank_mask:0xf
	v_add_f32_e32 v11, v11, v12
	s_nop 1
	v_mov_b32_dpp v12, v11 row_half_mirror row_mask:0xf bank_mask:0xf
	v_mov_b32_e32 v114, v113
	v_mov_b32_e32 v110, v109
	v_add_f32_e32 v10, v10, v13
	s_nop 1
	v_mov_b32_dpp v13, v10 row_half_mirror row_mask:0xf bank_mask:0xf
	v_add_f32_e32 v11, v11, v12
	s_nop 1
	v_mov_b32_dpp v12, v11 row_mirror row_mask:0xf bank_mask:0xf
	v_mov_b32_e32 v118, v117
	v_mov_b32_e32 v112, v111
	v_add_f32_e32 v10, v10, v13
	s_nop 1
	v_mov_b32_dpp v13, v10 row_mirror row_mask:0xf bank_mask:0xf
	v_add_f32_e32 v11, v11, v12
	v_mov_b32_e32 v12, v11
	s_nop 1
	v_permlane16_swap_b32_e32 v11, v12
	v_add_f32_e32 v10, v10, v13
	v_add_f32_e32 v136, v11, v12
	v_mov_b32_e32 v11, v10
	s_nop 1
	v_permlane16_swap_b32_e32 v10, v11
	v_add_f32_e32 v139, v10, v11
	v_mov_b32_e32 v120, v119
	v_mov_b32_e32 v124, v123
	v_mov_b32_e32 v131, v130
	v_mov_b32_e32 v122, v121
	v_mov_b32_e32 v129, v128
	v_mov_b32_e32 v125, v57
	v_mov_b32_e32 v133, v132
	v_mov_b32_e32 v127, v126
	v_mov_b32_e32 v135, v134
	v_mov_b32_e32 v137, v55
	v_mov_b32_e32 v144, v143
	v_mov_b32_e32 v53, v51
	v_mov_b32_e32 v142, v141
	v_mov_b32_e32 v138, v136
	v_mov_b32_e32 v140, v139
	v_permlane32_swap_b32_e32 v2, v3
	v_permlane32_swap_b32_e32 v4, v5
	v_permlane32_swap_b32_e32 v6, v7
	v_permlane32_swap_b32_e32 v8, v9
	v_permlane32_swap_b32_e32 v19, v20
	v_permlane32_swap_b32_e32 v97, v98
	v_permlane32_swap_b32_e32 v21, v94
	v_permlane32_swap_b32_e32 v99, v100
	v_permlane32_swap_b32_e32 v95, v96
	v_permlane32_swap_b32_e32 v101, v102
	v_permlane32_swap_b32_e32 v107, v108
	v_permlane32_swap_b32_e32 v115, v116
	v_permlane32_swap_b32_e32 v104, v106
	v_permlane32_swap_b32_e32 v113, v114
	v_permlane32_swap_b32_e32 v109, v110
	v_permlane32_swap_b32_e32 v117, v118
	v_permlane32_swap_b32_e32 v111, v112
	v_permlane32_swap_b32_e32 v119, v120
	v_permlane32_swap_b32_e32 v123, v124
	v_permlane32_swap_b32_e32 v130, v131
	v_permlane32_swap_b32_e32 v121, v122
	v_permlane32_swap_b32_e32 v128, v129
	v_permlane32_swap_b32_e32 v57, v125
	v_permlane32_swap_b32_e32 v132, v133
	v_permlane32_swap_b32_e32 v126, v127
	v_permlane32_swap_b32_e32 v134, v135
	v_permlane32_swap_b32_e32 v55, v137
	v_permlane32_swap_b32_e32 v143, v144
	v_permlane32_swap_b32_e32 v51, v53
	v_permlane32_swap_b32_e32 v141, v142
	v_permlane32_swap_b32_e32 v136, v138
	v_permlane32_swap_b32_e32 v139, v140
	s_and_saveexec_b64 s[4:5], s[42:43]
	s_cbranch_execz .LBB0_1299
	v_add_f32_e32 v4, v4, v5
	v_add_f32_e32 v2, v2, v3
	v_cndmask_b32_e64 v2, v2, v4, s[40:41]
	v_mul_f32_e32 v2, 0xbfb8aa3b, v2
	s_load_dwordx2 s[6:7], s[56:57], 0xd0
	v_exp_f32_e32 v2, v2
	v_add_f32_e32 v8, v8, v9
	v_add_f32_e32 v6, v6, v7
	v_cndmask_b32_e64 v49, v6, v8, s[40:41]
	v_add_f32_e32 v2, 1.0, v2
	v_rcp_f32_e32 v18, v2
	s_waitcnt lgkmcnt(0)
	global_load_dwordx4 v[2:5], v1, s[6:7] offset:48
	global_load_dwordx4 v[6:9], v1, s[6:7] offset:32
	global_load_dwordx4 v[10:13], v1, s[6:7] offset:16
	global_load_dwordx4 v[14:17], v1, s[6:7]
	s_mov_b32 s6, 0xf149f2ca
	s_waitcnt vmcnt(0)
	v_add_f32_e32 v47, v18, v14
	v_mul_f32_e32 v14, 0xbfb8aa3b, v49
	v_exp_f32_e32 v14, v14
	v_cmp_nlt_f32_e32 vcc, s6, v47
	v_add_f32_e32 v14, 1.0, v14
	v_rcp_f32_e32 v14, v14
	s_nop 0
	v_add_f32_e32 v49, v14, v15
	v_mov_b32_e32 v15, 0xf149f2ca
	v_cndmask_b32_e32 v145, v47, v15, vcc
	v_cmp_gt_f32_e64 s[44:45], v49, v145
	v_cmp_ngt_f32_e64 s[46:47], v49, v145
	v_mov_b32_e32 v148, v49
	v_mov_b32_e32 v147, v145
	s_and_saveexec_b64 s[6:7], s[46:47]
	s_cbranch_execz .LBB0_1305
	v_mov_b32_e32 v147, 0xf149f2ca
	v_cmp_gt_f32_e64 s[46:47], v49, v147
	s_and_saveexec_b64 s[8:9], s[46:47]
	v_mov_b32_e32 v147, v49
	s_or_b64 exec, exec, s[8:9]
	v_mov_b32_e32 v148, v145

.LBB0_1613:
	s_add_u32 s2, s0, s17
	s_addc_u32 s3, s1, s18
	global_load_dwordx4 v[106:109], v65, s[2:3] nt
	v_add_co_u32_e32 v84, vcc, s13, v80
	v_lshl_add_u64 v[82:83], s[0:1], 0, v[78:79]
	s_nop 0
	v_addc_co_u32_e32 v85, vcc, -1, v81, vcc
	v_add_co_u32_e32 v82, vcc, 0x11100000, v82
	s_add_i32 s15, s15, s66
	s_nop 0
	v_addc_co_u32_e32 v83, vcc, 0, v83, vcc
	global_load_dwordx2 v[110:111], v[82:83], off nt
	global_load_dwordx2 v[112:113], v[82:83], off offset:512 nt
	global_load_dwordx2 v[114:115], v[82:83], off offset:1024 nt
	global_load_dwordx2 v[116:117], v[82:83], off offset:1536 nt
	global_load_dwordx2 v[118:119], v[82:83], off offset:2048 nt
	global_load_dwordx2 v[120:121], v[82:83], off offset:2560 nt
	global_load_dwordx2 v[122:123], v[82:83], off offset:3072 nt
	global_load_dwordx2 v[124:125], v[82:83], off offset:3584 nt
	v_lshl_add_u64 v[78:79], v[78:79], 0, s[94:95]
	s_waitcnt vmcnt(8)
	v_readfirstlane_b32 s2, v106
	v_readfirstlane_b32 s3, v107
	s_lshr_b32 s4, s2, 18
	s_lshl_b32 s2, s2, 11
	s_lshr_b32 s11, s3, 18
	s_and_b32 s19, s4, 0x3ffc
	s_and_b32 s4, s2, 0x7ffff800
	s_and_b32 s2, s11, 0x3ffc
	s_add_i32 s11, s81, s19
	s_add_i32 s2, s81, s2
	v_mov_b32_e32 v105, s11
	v_mov_b32_e32 v139, s2
	ds_read_b32 v138, v105
	ds_read_b32 v140, v139
	s_lshl_b32 s3, s3, 11
	v_pk_mul_f32 v[82:83], v[108:109], s[8:9] op_sel_hi:[1,0]
	s_waitcnt vmcnt(7)
	v_lshlrev_b32_e32 v106, 16, v110
	s_waitcnt lgkmcnt(1)
	v_ashrrev_i32_e32 v139, 31, v138
	s_waitcnt lgkmcnt(0)
	v_ashrrev_i32_e32 v141, 31, v140
	v_lshlrev_b64 v[138:139], 19, v[138:139]
	v_lshlrev_b64 v[140:141], 19, v[140:141]
	v_lshl_add_u64 v[138:139], s[6:7], 0, v[138:139]
	v_lshl_add_u64 v[140:141], s[6:7], 0, v[140:141]
	v_lshl_add_u64 v[138:139], v[138:139], 0, s[4:5]
	s_and_b32 s4, s3, 0x7ffff800
	v_lshl_add_u64 v[140:141], v[140:141], 0, s[4:5]
	v_readfirstlane_b32 s2, v138
	v_readfirstlane_b32 s3, v139
	s_nop 4
	global_load_dword v105, v93, s[2:3] nt
	global_load_dword v139, v93, s[2:3] offset:256 nt
	global_load_dword v143, v93, s[2:3] offset:512 nt
	global_load_dword v145, v93, s[2:3] offset:768 nt
	global_load_dword v147, v93, s[2:3] offset:1024 nt
	global_load_dword v149, v93, s[2:3] offset:1280 nt
	global_load_dword v151, v93, s[2:3] offset:1536 nt
	global_load_dword v153, v93, s[2:3] offset:1792 nt
	v_readfirstlane_b32 s2, v140
	v_readfirstlane_b32 s3, v141
	s_nop 4
	global_load_dword v155, v93, s[2:3] nt
	global_load_dword v157, v93, s[2:3] offset:256 nt
	global_load_dword v159, v93, s[2:3] offset:512 nt
	global_load_dword v167, v93, s[2:3] offset:768 nt
	global_load_dword v175, v93, s[2:3] offset:1024 nt
	global_load_dword v183, v93, s[2:3] offset:1280 nt
	global_load_dword v191, v93, s[2:3] offset:1536 nt
	global_load_dword v199, v93, s[2:3] offset:1792 nt
	v_and_b32_e32 v107, 0xffff0000, v110
	v_lshlrev_b32_e32 v108, 16, v111
	v_and_b32_e32 v109, 0xffff0000, v111
	s_waitcnt vmcnt(22)
	v_lshlrev_b32_e32 v110, 16, v112
	v_and_b32_e32 v111, 0xffff0000, v112
	v_lshlrev_b32_e32 v112, 16, v113
	v_and_b32_e32 v113, 0xffff0000, v113
	s_waitcnt vmcnt(21)
	v_lshlrev_b32_e32 v126, 16, v114
	v_and_b32_e32 v127, 0xffff0000, v114
	v_lshlrev_b32_e32 v114, 16, v115
	v_and_b32_e32 v115, 0xffff0000, v115
	s_waitcnt vmcnt(16)
	v_lshlrev_b32_e32 v136, 16, v124
	v_and_b32_e32 v137, 0xffff0000, v124
	v_lshlrev_b32_e32 v124, 16, v125
	v_and_b32_e32 v125, 0xffff0000, v125
	v_lshlrev_b32_e32 v128, 16, v116
	v_and_b32_e32 v129, 0xffff0000, v116
	v_lshlrev_b32_e32 v116, 16, v117
	v_and_b32_e32 v117, 0xffff0000, v117
	v_lshlrev_b32_e32 v130, 16, v118
	v_and_b32_e32 v131, 0xffff0000, v118
	v_lshlrev_b32_e32 v118, 16, v119
	v_and_b32_e32 v119, 0xffff0000, v119
	v_lshlrev_b32_e32 v132, 16, v120
	v_and_b32_e32 v133, 0xffff0000, v120
	v_lshlrev_b32_e32 v120, 16, v121
	v_and_b32_e32 v121, 0xffff0000, v121
	v_lshlrev_b32_e32 v134, 16, v122
	v_and_b32_e32 v135, 0xffff0000, v122
	v_lshlrev_b32_e32 v122, 16, v123
	v_and_b32_e32 v123, 0xffff0000, v123
	s_add_u32 s17, s17, s68
	s_addc_u32 s18, s18, s69
	s_cmp_ge_i32 s15, s16
	s_waitcnt vmcnt(15)
	v_cvt_f32_fp8_sdwa v140, v105 src0_sel:BYTE_1
	v_cvt_f32_fp8_sdwa v144, v105 src0_sel:BYTE_3
	s_waitcnt vmcnt(14)
	v_cvt_f32_fp8_sdwa v148, v139 src0_sel:BYTE_1
	v_cvt_f32_fp8_sdwa v152, v139 src0_sel:BYTE_3
	s_waitcnt vmcnt(12)
	v_cvt_f32_fp8_e32 v162, v145
	v_cvt_f32_fp8_sdwa v164, v145 src0_sel:BYTE_1
	v_cvt_f32_fp8_sdwa v166, v145 src0_sel:BYTE_2
	v_cvt_f32_fp8_sdwa v168, v145 src0_sel:BYTE_3
	s_waitcnt vmcnt(10)
	v_cvt_f32_fp8_e32 v178, v149
	v_cvt_f32_fp8_sdwa v180, v149 src0_sel:BYTE_1
	v_cvt_f32_fp8_sdwa v182, v149 src0_sel:BYTE_2
	v_cvt_f32_fp8_sdwa v184, v149 src0_sel:BYTE_3
	s_waitcnt vmcnt(8)
	v_cvt_f32_fp8_e32 v194, v153
	v_cvt_f32_fp8_sdwa v196, v153 src0_sel:BYTE_1
	v_cvt_f32_fp8_sdwa v198, v153 src0_sel:BYTE_2
	v_cvt_f32_fp8_sdwa v200, v153 src0_sel:BYTE_3
	s_waitcnt vmcnt(7)
	v_cvt_f32_fp8_e32 v141, v155
	v_cvt_f32_fp8_sdwa v145, v155 src0_sel:BYTE_2
	s_waitcnt vmcnt(6)
	v_cvt_f32_fp8_e32 v149, v157
	v_cvt_f32_fp8_sdwa v153, v157 src0_sel:BYTE_2
	v_cvt_f32_fp8_e32 v138, v105
	v_cvt_f32_fp8_sdwa v142, v105 src0_sel:BYTE_2
	v_cvt_f32_fp8_e32 v146, v139
	v_cvt_f32_fp8_sdwa v150, v139 src0_sel:BYTE_2
	v_cvt_f32_fp8_e32 v154, v143
	v_cvt_f32_fp8_sdwa v156, v143 src0_sel:BYTE_1
	v_cvt_f32_fp8_sdwa v158, v143 src0_sel:BYTE_2
	v_cvt_f32_fp8_sdwa v160, v143 src0_sel:BYTE_3
	v_cvt_f32_fp8_e32 v170, v147
	v_cvt_f32_fp8_sdwa v172, v147 src0_sel:BYTE_1
	v_cvt_f32_fp8_sdwa v174, v147 src0_sel:BYTE_2
	v_cvt_f32_fp8_sdwa v176, v147 src0_sel:BYTE_3
	v_cvt_f32_fp8_e32 v186, v151
	v_cvt_f32_fp8_sdwa v188, v151 src0_sel:BYTE_1
	v_cvt_f32_fp8_sdwa v190, v151 src0_sel:BYTE_2
	v_cvt_f32_fp8_sdwa v192, v151 src0_sel:BYTE_3
	v_cvt_f32_fp8_sdwa v139, v155 src0_sel:BYTE_1
	v_cvt_f32_fp8_sdwa v143, v155 src0_sel:BYTE_3
	v_cvt_f32_fp8_sdwa v147, v157 src0_sel:BYTE_1
	v_cvt_f32_fp8_sdwa v151, v157 src0_sel:BYTE_3
	s_waitcnt vmcnt(5)
	v_cvt_f32_fp8_e32 v157, v159
	v_cvt_f32_fp8_sdwa v161, v159 src0_sel:BYTE_2
	s_waitcnt vmcnt(4)
	v_cvt_f32_fp8_e32 v165, v167
	v_cvt_f32_fp8_sdwa v169, v167 src0_sel:BYTE_2
	s_waitcnt vmcnt(3)
	v_cvt_f32_fp8_e32 v173, v175
	v_cvt_f32_fp8_sdwa v177, v175 src0_sel:BYTE_2
	s_waitcnt vmcnt(2)
	v_cvt_f32_fp8_e32 v181, v183
	v_cvt_f32_fp8_sdwa v185, v183 src0_sel:BYTE_2
	s_waitcnt vmcnt(1)
	v_cvt_f32_fp8_e32 v189, v191
	v_cvt_f32_fp8_sdwa v193, v191 src0_sel:BYTE_2
	s_waitcnt vmcnt(0)
	v_cvt_f32_fp8_e32 v197, v199
	v_cvt_f32_fp8_sdwa v201, v199 src0_sel:BYTE_2
	v_cvt_f32_fp8_sdwa v155, v159 src0_sel:BYTE_1
	v_cvt_f32_fp8_sdwa v159, v159 src0_sel:BYTE_3
	v_cvt_f32_fp8_sdwa v163, v167 src0_sel:BYTE_1
	v_cvt_f32_fp8_sdwa v167, v167 src0_sel:BYTE_3
	v_cvt_f32_fp8_sdwa v171, v175 src0_sel:BYTE_1
	v_cvt_f32_fp8_sdwa v175, v175 src0_sel:BYTE_3
	v_cvt_f32_fp8_sdwa v179, v183 src0_sel:BYTE_1
	v_cvt_f32_fp8_sdwa v183, v183 src0_sel:BYTE_3
	v_cvt_f32_fp8_sdwa v187, v191 src0_sel:BYTE_1
	v_cvt_f32_fp8_sdwa v191, v191 src0_sel:BYTE_3
	v_cvt_f32_fp8_sdwa v195, v199 src0_sel:BYTE_1
	v_cvt_f32_fp8_sdwa v199, v199 src0_sel:BYTE_3
	v_pk_mul_f32 v[140:141], v[82:83], v[140:141]
	v_pk_mul_f32 v[144:145], v[82:83], v[144:145]
	v_pk_mul_f32 v[148:149], v[82:83], v[148:149]
	v_pk_mul_f32 v[152:153], v[82:83], v[152:153]
	v_pk_mul_f32 v[156:157], v[82:83], v[156:157]
	v_pk_mul_f32 v[160:161], v[82:83], v[160:161]
	v_pk_mul_f32 v[164:165], v[82:83], v[164:165]
	v_pk_mul_f32 v[168:169], v[82:83], v[168:169]
	v_pk_mul_f32 v[172:173], v[82:83], v[172:173]
	v_pk_mul_f32 v[176:177], v[82:83], v[176:177]
	v_pk_mul_f32 v[180:181], v[82:83], v[180:181]
	v_pk_mul_f32 v[184:185], v[82:83], v[184:185]
	v_pk_mul_f32 v[188:189], v[82:83], v[188:189]
	v_pk_mul_f32 v[192:193], v[82:83], v[192:193]
	v_pk_mul_f32 v[196:197], v[82:83], v[196:197]
	v_pk_mul_f32 v[200:201], v[82:83], v[200:201]
	v_pk_fma_f32 v[138:139], v[82:83], v[138:139], v[140:141] op_sel:[0,0,1] op_sel_hi:[1,1,0]
	v_pk_fma_f32 v[140:141], v[82:83], v[142:143], v[144:145] op_sel:[0,0,1] op_sel_hi:[1,1,0]
	v_pk_fma_f32 v[142:143], v[82:83], v[146:147], v[148:149] op_sel:[0,0,1] op_sel_hi:[1,1,0]
	v_pk_fma_f32 v[144:145], v[82:83], v[150:151], v[152:153] op_sel:[0,0,1] op_sel_hi:[1,1,0]
	v_pk_fma_f32 v[146:147], v[82:83], v[154:155], v[156:157] op_sel:[0,0,1] op_sel_hi:[1,1,0]
	v_pk_fma_f32 v[148:149], v[82:83], v[158:159], v[160:161] op_sel:[0,0,1] op_sel_hi:[1,1,0]
	v_pk_fma_f32 v[150:151], v[82:83], v[162:163], v[164:165] op_sel:[0,0,1] op_sel_hi:[1,1,0]
	v_pk_fma_f32 v[152:153], v[82:83], v[166:167], v[168:169] op_sel:[0,0,1] op_sel_hi:[1,1,0]
	v_pk_fma_f32 v[154:155], v[82:83], v[170:171], v[172:173] op_sel:[0,0,1] op_sel_hi:[1,1,0]
	v_pk_fma_f32 v[156:157], v[82:83], v[174:175], v[176:177] op_sel:[0,0,1] op_sel_hi:[1,1,0]
	v_pk_fma_f32 v[158:159], v[82:83], v[178:179], v[180:181] op_sel:[0,0,1] op_sel_hi:[1,1,0]
	v_pk_fma_f32 v[160:161], v[82:83], v[182:183], v[184:185] op_sel:[0,0,1] op_sel_hi:[1,1,0]
	v_pk_fma_f32 v[162:163], v[82:83], v[186:187], v[188:189] op_sel:[0,0,1] op_sel_hi:[1,1,0]
	v_pk_fma_f32 v[164:165], v[82:83], v[190:191], v[192:193] op_sel:[0,0,1] op_sel_hi:[1,1,0]
	v_pk_fma_f32 v[166:167], v[82:83], v[194:195], v[196:197] op_sel:[0,0,1] op_sel_hi:[1,1,0]
	v_pk_fma_f32 v[82:83], v[82:83], v[198:199], v[200:201] op_sel:[0,0,1] op_sel_hi:[1,1,0]
	v_pk_fma_f32 v[108:109], v[10:11], v[140:141], v[108:109]
	v_pk_fma_f32 v[106:107], v[8:9], v[138:139], v[106:107]
	v_pk_fma_f32 v[112:113], v[14:15], v[144:145], v[112:113]
	v_pk_fma_f32 v[110:111], v[12:13], v[142:143], v[110:111]
	v_pk_fma_f32 v[114:115], v[26:27], v[148:149], v[114:115]
	v_pk_fma_f32 v[126:127], v[24:25], v[146:147], v[126:127]
	v_pk_fma_f32 v[82:83], v[62:63], v[82:83], v[124:125]
	v_pk_fma_f32 v[124:125], v[60:61], v[166:167], v[136:137]
	v_mul_f32_e32 v105, v107, v107
	v_mul_f32_e32 v136, v109, v109
	v_mul_f32_e32 v137, v111, v111
	v_mul_f32_e32 v138, v113, v113
	v_pk_fma_f32 v[116:117], v[30:31], v[152:153], v[116:117]
	v_pk_fma_f32 v[128:129], v[28:29], v[150:151], v[128:129]
	v_mul_f32_e32 v139, v127, v127
	v_mul_f32_e32 v140, v115, v115
	v_fmac_f32_e32 v105, v106, v106
	v_fmac_f32_e32 v136, v108, v108
	v_fmac_f32_e32 v137, v110, v110
	v_fmac_f32_e32 v138, v112, v112
	v_pk_fma_f32 v[118:119], v[42:43], v[156:157], v[118:119]
	v_pk_fma_f32 v[130:131], v[40:41], v[154:155], v[130:131]
	v_mul_f32_e32 v141, v129, v129
	v_mul_f32_e32 v142, v117, v117
	v_fmac_f32_e32 v139, v126, v126
	v_fmac_f32_e32 v140, v114, v114
	v_add_f32_e32 v105, v105, v136
	v_add_f32_e32 v136, v137, v138
	v_pk_fma_f32 v[120:121], v[46:47], v[160:161], v[120:121]
	v_pk_fma_f32 v[132:133], v[44:45], v[158:159], v[132:133]
	v_mul_f32_e32 v143, v131, v131
	v_mul_f32_e32 v144, v119, v119
	v_fmac_f32_e32 v141, v128, v128
	v_fmac_f32_e32 v142, v116, v116
	v_add_f32_e32 v137, v139, v140
	v_add_f32_e32 v105, v105, v136
	v_pk_fma_f32 v[122:123], v[58:59], v[164:165], v[122:123]
	v_pk_fma_f32 v[134:135], v[56:57], v[162:163], v[134:135]
	v_mul_f32_e32 v145, v133, v133
	v_mul_f32_e32 v146, v121, v121
	v_fmac_f32_e32 v143, v130, v130
	v_fmac_f32_e32 v144, v118, v118
	v_add_f32_e32 v138, v141, v142
	v_add_f32_e32 v105, v105, v137
	v_mul_f32_e32 v147, v135, v135
	v_mul_f32_e32 v148, v123, v123
	v_fmac_f32_e32 v145, v132, v132
	v_fmac_f32_e32 v146, v120, v120
	v_add_f32_e32 v139, v143, v144
	v_add_f32_e32 v105, v105, v138
	v_mul_f32_e32 v149, v125, v125
	v_mul_f32_e32 v150, v83, v83
	v_fmac_f32_e32 v147, v134, v134
	v_fmac_f32_e32 v148, v122, v122
	v_add_f32_e32 v140, v145, v146
	v_add_f32_e32 v105, v105, v139
	v_fmac_f32_e32 v149, v124, v124
	v_fmac_f32_e32 v150, v82, v82
	v_add_f32_e32 v141, v147, v148
	v_add_f32_e32 v105, v105, v140
	v_add_f32_e32 v142, v149, v150
	v_add_f32_e32 v105, v105, v141
	v_add_f32_e32 v105, v105, v142
	s_nop 1
	v_mov_b32_dpp v136, v105 quad_perm:[1,0,3,2] row_mask:0xf bank_mask:0xf
	v_add_f32_e32 v105, v105, v136
	s_nop 1
	v_mov_b32_dpp v136, v105 quad_perm:[2,3,0,1] row_mask:0xf bank_mask:0xf
	v_add_f32_e32 v105, v105, v136
	s_nop 1
	v_mov_b32_dpp v136, v105 row_half_mirror row_mask:0xf bank_mask:0xf
	v_add_f32_e32 v105, v105, v136
	s_nop 1
	v_mov_b32_dpp v136, v105 row_mirror row_mask:0xf bank_mask:0xf
	v_add_f32_e32 v105, v105, v136
	v_mov_b32_e32 v136, v105
	s_nop 1
	v_permlane16_swap_b32_e32 v105, v136
	v_add_f32_e32 v105, v105, v136
	v_mov_b32_e32 v136, v105
	s_nop 1
	v_permlane32_swap_b32_e32 v105, v136
	v_add_f32_e32 v105, v105, v136
	v_fmamk_f32 v105, v105, 0x3a000000, v94
	v_mul_f32_e32 v136, 0x4f800000, v105
	v_cmp_gt_f32_e32 vcc, s12, v105
	s_nop 1
	v_cndmask_b32_e32 v105, v105, v136, vcc
	v_sqrt_f32_e32 v136, v105
	s_nop 0
	v_add_u32_e32 v137, -1, v136
	v_add_u32_e32 v138, 1, v136
	v_fma_f32 v139, -v137, v136, v105
	v_fma_f32 v140, -v138, v136, v105
	v_cmp_ge_f32_e64 s[2:3], 0, v139
	s_nop 1
	v_cndmask_b32_e64 v136, v136, v137, s[2:3]
	v_cmp_lt_f32_e64 s[2:3], 0, v140
	s_nop 1
	v_cndmask_b32_e64 v136, v136, v138, s[2:3]
	v_mul_f32_e32 v137, 0x37800000, v136
	v_cndmask_b32_e32 v136, v136, v137, vcc
	v_cmp_class_f32_e32 vcc, v105, v95
	s_nop 1
	v_cndmask_b32_e32 v105, v136, v105, vcc
	v_div_scale_f32 v136, s[2:3], v105, v105, 1.0
	v_rcp_f32_e32 v138, v136
	v_div_scale_f32 v137, vcc, 1.0, v105, 1.0
	v_fma_f32 v139, -v136, v138, 1.0
	v_fmac_f32_e32 v138, v139, v138
	v_mul_f32_e32 v139, v137, v138
	v_fma_f32 v140, -v136, v139, v137
	v_fmac_f32_e32 v139, v140, v138
	v_fma_f32 v136, -v136, v139, v137
	v_div_fmas_f32 v136, v136, v138, v139
	v_div_fixup_f32 v136, v136, v105, 1.0
	v_pk_mul_f32 v[106:107], v[106:107], v[136:137] op_sel_hi:[1,0]
	v_pk_mul_f32 v[108:109], v[108:109], v[136:137] op_sel_hi:[1,0]
	v_pk_mul_f32 v[110:111], v[110:111], v[136:137] op_sel_hi:[1,0]
	v_pk_mul_f32 v[112:113], v[112:113], v[136:137] op_sel_hi:[1,0]
	v_pk_mul_f32 v[126:127], v[126:127], v[136:137] op_sel_hi:[1,0]
	v_pk_mul_f32 v[114:115], v[114:115], v[136:137] op_sel_hi:[1,0]
	v_pk_mul_f32 v[128:129], v[128:129], v[136:137] op_sel_hi:[1,0]
	v_pk_mul_f32 v[138:139], v[116:117], v[136:137] op_sel_hi:[1,0]
	v_pk_mul_f32 v[130:131], v[130:131], v[136:137] op_sel_hi:[1,0]
	v_pk_mul_f32 v[140:141], v[118:119], v[136:137] op_sel_hi:[1,0]
	v_pk_mul_f32 v[132:133], v[132:133], v[136:137] op_sel_hi:[1,0]
	v_pk_mul_f32 v[142:143], v[120:121], v[136:137] op_sel_hi:[1,0]
	v_pk_mul_f32 v[134:135], v[134:135], v[136:137] op_sel_hi:[1,0]
	v_pk_mul_f32 v[144:145], v[122:123], v[136:137] op_sel_hi:[1,0]
	v_pk_mul_f32 v[146:147], v[124:125], v[136:137] op_sel_hi:[1,0]
	v_pk_mul_f32 v[82:83], v[82:83], v[136:137] op_sel_hi:[1,0]
	v_pk_mul_f32 v[108:109], v[2:3], v[108:109]
	v_pk_mul_f32 v[106:107], v[0:1], v[106:107]
	v_pk_mul_f32 v[112:113], v[6:7], v[112:113]
	v_pk_mul_f32 v[110:111], v[4:5], v[110:111]
	v_pk_mul_f32 v[116:117], v[18:19], v[114:115]
	v_pk_mul_f32 v[114:115], v[16:17], v[126:127]
	v_pk_mul_f32 v[120:121], v[22:23], v[138:139]
	v_pk_mul_f32 v[118:119], v[20:21], v[128:129]
	v_pk_mul_f32 v[124:125], v[34:35], v[140:141]
	v_pk_mul_f32 v[122:123], v[32:33], v[130:131]
	v_pk_mul_f32 v[128:129], v[38:39], v[142:143]
	v_pk_mul_f32 v[126:127], v[36:37], v[132:133]
	v_pk_mul_f32 v[132:133], v[50:51], v[144:145]
	v_pk_mul_f32 v[130:131], v[48:49], v[134:135]
	v_pk_mul_f32 v[136:137], v[54:55], v[82:83]
	v_pk_mul_f32 v[134:135], v[52:53], v[146:147]
	global_store_dwordx4 v[84:85], v[106:109], off offset:-3072 sc1
	global_store_dwordx4 v[84:85], v[110:113], off offset:-2048 sc1
	global_store_dwordx4 v[84:85], v[114:117], off offset:-1024 sc1
	global_store_dwordx4 v[80:81], v[118:121], off offset:-4096 sc1
	global_store_dwordx4 v[80:81], v[122:125], off offset:-3072 sc1
	global_store_dwordx4 v[80:81], v[126:129], off offset:-2048 sc1
	global_store_dwordx4 v[80:81], v[130:133], off offset:-1024 sc1
	global_store_dwordx4 v[80:81], v[134:137], off sc1
	v_lshl_add_u64 v[80:81], v[80:81], 0, s[24:25]
	s_cbranch_scc0 .LBB0_1613
	s_branch .LBB0_1610
